# K-loop back-edge rotation step 2: loop-header tests pre-evaluated before the closing barrier, common path goes barrier -> body
# baseline (speedup 1.0000x reference)
; #define PG8_STAGE_A(bufoff, kbase, h, gv) do { if constexpr (GATHER) { PG8_STAGE(bufoff, kbase, (gv)[h]); } else { PG8_STAGE(bufoff, (kbase) + (h) * hstep, voffA); } } while (0)
; #define PG8_SCHED __builtin_amdgcn_sched_barrier(0)
; template <class Epi, class Sched, bool ALIGN_EPI = false, bool SP2 = false, bool FP8 = false, bool GATHER = false>
; __device__ __forceinline__ void gemm_phase(PG8_LAS unsigned char* lds, const Gemm g, const Sched& S, const Epi& E) {
;     ...
;             const char* a1 = cA + (size_t)(t + 1) * kstep;
;             const char* a2 = last ? nA : cA + (size_t)(t + 2) * kstep; const char* b2 = last ? nB : cB + (size_t)(t + 2) * kstep;
;             const char* a3 = a2 + kstep; const char* b3 = b2 + kstep;
;             if (last && has_next) S.a_ready(nxt);
;             if (last) E.pre(cur, wid, lane);
;             if constexpr (GATHER) { if (t == nt - 4 && has_next) { _Pragma("unroll") for (int h_ = 0; h_ < 2; ++h_) _Pragma("unroll") for (int i_ = 0; i_ < 2; ++i_)
;                 asm volatile("global_load_dword %0, %1, off" : "+v"(graw[h_][i_]) : "v"(S.rowtok + (nxt.pm * BM + h_ * HALF + gR[i_])) : "memory"); } }
;             unsigned gsel[2][2];
;             if constexpr (GATHER) { _Pragma("unroll") for (int h_ = 0; h_ < 2; ++h_) _Pragma("unroll") for (int i_ = 0; i_ < 2; ++i_) { if (last && has_next) gnxt[h_][i_] = graw[h_][i_] * (unsigned)(K * 2) + gC[i_]; gsel[h_][i_] = (last && has_next) ? gnxt[h_][i_] : gcur[h_][i_]; } }
;             if constexpr (SP2) {
;             PG8_LDB(B0, 0, 0); PG8_LDB(B1, 0, 1); PG8_SCHED; PG8_LDA(At, 0, 0); PG8_STAGE_A(PG8_SA(1, 1), a1, 1, gcur);
;     ...
; #pragma unroll
;         for (int a = 0; a < 2; ++a)
; #pragma unroll
;             for (int b = 0; b < 2; ++b)
; #pragma unroll
;                 for (int m = 0; m < 4; ++m)
; #pragma unroll
;                     for (int n = 0; n < 2; ++n) acc[a][b][m][n] = (f32x4){0.f, 0.f, 0.f, 0.f};
;         cur = nxt; cA = nA; cB = nB; ++ui;
.LBB0_591:
	s_ashr_i32 s47, s46, 31
	s_lshl_b64 s[48:49], s[46:47], 19
	s_add_u32 s48, s65, s48
	s_addc_u32 s49, s66, s49
	s_and_b64 s[50:51], s[6:7], exec
	s_cselect_b32 s47, s49, s57
	s_cselect_b32 s85, s48, s56
	s_lshl_b32 s50, s84, 8
	s_ashr_i32 s51, s50, 31
	s_lshl_b64 s[50:51], s[50:51], 11
	s_add_u32 s50, s62, s50
	s_addc_u32 s51, s63, s51
	s_and_b64 s[60:61], s[6:7], exec
	s_cselect_b32 s86, s51, s59
	s_cselect_b32 s87, s50, s58
	s_lshl_b32 s54, s54, 8
	s_ashr_i32 s60, s52, 4
	s_ashr_i32 s55, s54, 31
	s_cmpk_lt_i32 s52, 0x100
	s_mul_i32 s88, s60, 0x1800
	s_mul_hi_i32 s60, s60, 0x1800
	s_cselect_b32 s61, s60, 0
	s_cselect_b32 s60, s88, 0x18000
	s_lshl_b64 s[60:61], s[60:61], 2
	s_add_u32 s88, s74, s60
	s_addc_u32 s89, s75, s61
	s_lshl_b64 s[60:61], s[54:55], 2
	s_add_u32 s60, s88, s60
	s_addc_u32 s61, s89, s61
	s_add_u32 s56, s56, 0x40080
	s_addc_u32 s57, s57, 0
	s_add_u32 s55, s58, 0x100
	v_mov_b32_e32 v2, 0
	v_lshl_add_u64 v[122:123], s[60:61], 0, v[162:163]
	s_addc_u32 s88, s59, 0
	s_mov_b32 s89, -2
	v_mov_b32_e32 v3, v2
	v_mov_b32_e32 v4, v2
	v_mov_b32_e32 v5, v2
	v_mov_b32_e32 v6, v2
	v_mov_b32_e32 v7, v2
	v_mov_b32_e32 v8, v2
	v_mov_b32_e32 v9, v2
	v_mov_b32_e32 v14, v2
	v_mov_b32_e32 v15, v2
	v_mov_b32_e32 v16, v2
	v_mov_b32_e32 v17, v2
	v_mov_b32_e32 v18, v2
	v_mov_b32_e32 v19, v2
	v_mov_b32_e32 v20, v2
	v_mov_b32_e32 v21, v2
	v_mov_b32_e32 v30, v2
	v_mov_b32_e32 v31, v2
	v_mov_b32_e32 v32, v2
	v_mov_b32_e32 v33, v2
	v_mov_b32_e32 v34, v2
	v_mov_b32_e32 v35, v2
	v_mov_b32_e32 v36, v2
	v_mov_b32_e32 v37, v2
	v_mov_b32_e32 v46, v2
	v_mov_b32_e32 v47, v2
	v_mov_b32_e32 v48, v2
	v_mov_b32_e32 v49, v2
	v_mov_b32_e32 v50, v2
	v_mov_b32_e32 v51, v2
	v_mov_b32_e32 v52, v2
	v_mov_b32_e32 v53, v2
	v_mov_b32_e32 v10, v2
	v_mov_b32_e32 v11, v2
	v_mov_b32_e32 v12, v2
	v_mov_b32_e32 v13, v2
	v_mov_b32_e32 v22, v2
	v_mov_b32_e32 v23, v2
	v_mov_b32_e32 v24, v2
	v_mov_b32_e32 v25, v2
	v_mov_b32_e32 v26, v2
	v_mov_b32_e32 v27, v2
	v_mov_b32_e32 v28, v2
	v_mov_b32_e32 v29, v2
	v_mov_b32_e32 v38, v2
	v_mov_b32_e32 v39, v2
	v_mov_b32_e32 v40, v2
	v_mov_b32_e32 v41, v2
	v_mov_b32_e32 v42, v2
	v_mov_b32_e32 v43, v2
	v_mov_b32_e32 v44, v2
	v_mov_b32_e32 v45, v2
	v_mov_b32_e32 v54, v2
	v_mov_b32_e32 v55, v2
	v_mov_b32_e32 v56, v2
	v_mov_b32_e32 v57, v2
	v_mov_b32_e32 v58, v2
	v_mov_b32_e32 v59, v2
	v_mov_b32_e32 v60, v2
	v_mov_b32_e32 v61, v2
	v_mov_b32_e32 v62, v2
	v_mov_b32_e32 v63, v2
	v_mov_b32_e32 v64, v2
	v_mov_b32_e32 v65, v2
	v_mov_b32_e32 v66, v2
	v_mov_b32_e32 v67, v2
	v_mov_b32_e32 v68, v2
	v_mov_b32_e32 v69, v2
	v_mov_b32_e32 v70, v2
	v_mov_b32_e32 v71, v2
	v_mov_b32_e32 v72, v2
	v_mov_b32_e32 v73, v2
	v_mov_b32_e32 v78, v2
	v_mov_b32_e32 v79, v2
	v_mov_b32_e32 v80, v2
	v_mov_b32_e32 v81, v2
	v_mov_b32_e32 v82, v2
	v_mov_b32_e32 v83, v2
	v_mov_b32_e32 v84, v2
	v_mov_b32_e32 v85, v2
	v_mov_b32_e32 v94, v2
	v_mov_b32_e32 v95, v2
	v_mov_b32_e32 v96, v2
	v_mov_b32_e32 v97, v2
	v_mov_b32_e32 v98, v2
	v_mov_b32_e32 v99, v2
	v_mov_b32_e32 v100, v2
	v_mov_b32_e32 v101, v2
	v_mov_b32_e32 v110, v2
	v_mov_b32_e32 v111, v2
	v_mov_b32_e32 v112, v2
	v_mov_b32_e32 v113, v2
	v_mov_b32_e32 v114, v2
	v_mov_b32_e32 v115, v2
	v_mov_b32_e32 v116, v2
	v_mov_b32_e32 v117, v2
	v_mov_b32_e32 v74, v2
	v_mov_b32_e32 v75, v2
	v_mov_b32_e32 v76, v2
	v_mov_b32_e32 v77, v2
	v_mov_b32_e32 v86, v2
	v_mov_b32_e32 v87, v2
	v_mov_b32_e32 v88, v2
	v_mov_b32_e32 v89, v2
	v_mov_b32_e32 v90, v2
	v_mov_b32_e32 v91, v2
	v_mov_b32_e32 v92, v2
	v_mov_b32_e32 v93, v2
	v_mov_b32_e32 v102, v2
	v_mov_b32_e32 v103, v2
	v_mov_b32_e32 v104, v2
	v_mov_b32_e32 v105, v2
	v_mov_b32_e32 v106, v2
	v_mov_b32_e32 v107, v2
	v_mov_b32_e32 v108, v2
	v_mov_b32_e32 v109, v2
	v_mov_b32_e32 v118, v2
	v_mov_b32_e32 v119, v2
	v_mov_b32_e32 v120, v2
	v_mov_b32_e32 v121, v2
	v_mov_b32_e32 v138, v2
	v_mov_b32_e32 v139, v2
	v_mov_b32_e32 v140, v2
	v_mov_b32_e32 v141, v2
	v_mov_b32_e32 v142, v2
	v_mov_b32_e32 v143, v2
	v_mov_b32_e32 v144, v2
	v_mov_b32_e32 v145, v2
	s_waitcnt vmcnt(0)
	s_branch .LBB0_593
.Lrot592_head:
	s_barrier
.LBB0_592:
	v_add_u32_e32 v136, s82, v169
	ds_read_b128 v[124:127], v136
	ds_read_b128 v[128:131], v136 offset:1024
	ds_read_b128 v[132:135], v136 offset:2048
	ds_read_b128 v[164:167], v136 offset:3072
	v_add_u32_e32 v136, s83, v169
	ds_read_b128 v[172:175], v136
	ds_read_b128 v[176:179], v136 offset:1024
	ds_read_b128 v[180:183], v136 offset:2048
	ds_read_b128 v[184:187], v136 offset:3072
	s_add_u32 s60, s56, 0xfffc0080
	s_addc_u32 s61, s57, -1
	s_and_b64 s[58:59], s[58:59], exec
	s_cselect_b32 s61, s61, s47
	s_cselect_b32 s60, s60, s85
	s_cselect_b32 s59, s88, s86
	s_cselect_b32 s58, s55, s87
	v_lshl_add_u64 v[136:137], s[56:57], 0, v[154:155]
	s_add_i32 m0, s53, 0xc000
	ds_read_b128 v[188:191], v170
	ds_read_b128 v[192:195], v170 offset:1024
	ds_read_b128 v[196:199], v170 offset:2048
	ds_read_b128 v[200:203], v170 offset:3072
	ds_read_b128 v[204:207], v170 offset:4096
	ds_read_b128 v[208:211], v170 offset:5120
	ds_read_b128 v[212:215], v170 offset:6144
	ds_read_b128 v[216:219], v170 offset:7168
	global_load_lds_dwordx4 v[136:137], off
	v_lshl_add_u64 v[136:137], s[56:57], 0, v[156:157]
	s_add_i32 m0, s53, 0xe000
	s_nop 0
	global_load_lds_dwordx4 v[136:137], off
	s_waitcnt vmcnt(8)
	s_waitcnt lgkmcnt(0)
	s_barrier
; #define PG8_STAGE(bufoff, gbase, voff) do { _Pragma("unroll") for (int _i = 0; _i < 2; ++_i) \
;         __builtin_amdgcn_global_load_lds((const unsigned*)((const char*)(gbase) + (voff)[_i]), (PG8_LAS unsigned*)(lds + (bufoff) + ldsw + _i * 8192), 16, 0, 0); } while (0)
; #define PG8_STAGE_A(bufoff, kbase, h, gv) do { if constexpr (GATHER) { PG8_STAGE(bufoff, kbase, (gv)[h]); } else { PG8_STAGE(bufoff, (kbase) + (h) * hstep, voffA); } } while (0)
; #define PG8_WAIT_V(n) asm volatile("s_waitcnt vmcnt(" #n ")" ::: "memory")
; #define PG8_WAIT_L(n) asm volatile("s_waitcnt lgkmcnt(" #n ")" ::: "memory")
; #define PG8_BAR __builtin_amdgcn_s_barrier()
; #define PG8_SCHED __builtin_amdgcn_sched_barrier(0)
; template <class Epi, class Sched, bool ALIGN_EPI = false, bool SP2 = false, bool FP8 = false, bool GATHER = false>
; __device__ __forceinline__ void gemm_phase(PG8_LAS unsigned char* lds, const Gemm g, const Sched& S, const Epi& E) {
;     ...
;             PG8_LDB(B0, 0, 0); PG8_LDB(B1, 0, 1); PG8_SCHED; PG8_LDA(At, 0, 0); PG8_STAGE_A(PG8_SA(1, 1), a1, 1, gcur);
;             PG8_WAIT_V(8); PG8_WAIT_L(0); PG8_BAR; PG8_MMA(0, 0, At, B0); PG8_MMA(0, 1, At, B1); PG8_BAR; PG8_SCHED;
;             PG8_LDA(At, 0, 1); PG8_STAGE(PG8_SB(0, 0), b2, voffB); PG8_STAGE(PG8_SB(0, 1), b2 + hstep, voffB); PG8_STAGE_A(PG8_SA(0, 0), a2, 0, gsel);
;             PG8_WAIT_V(8); PG8_WAIT_L(0); PG8_BAR; PG8_MMA(1, 0, At, B0); PG8_MMA(1, 1, At, B1); PG8_BAR; PG8_SCHED;
	s_setprio 1
	s_waitcnt lgkmcnt(0)
	v_mfma_f32_16x16x32_bf16 v[142:145], v[124:127], v[188:191], v[142:145]
	v_mfma_f32_16x16x32_bf16 v[136:139], v[132:135], v[188:191], v[138:141]
	v_mfma_f32_16x16x32_bf16 v[118:121], v[124:127], v[196:199], v[118:121]
	v_mfma_f32_16x16x32_bf16 v[106:109], v[132:135], v[196:199], v[106:109]
	v_mfma_f32_16x16x32_bf16 v[102:105], v[124:127], v[204:207], v[102:105]
	v_mfma_f32_16x16x32_bf16 v[90:93], v[132:135], v[204:207], v[90:93]
	v_mfma_f32_16x16x32_bf16 v[86:89], v[124:127], v[212:215], v[86:89]
	v_mfma_f32_16x16x32_bf16 v[74:77], v[132:135], v[212:215], v[74:77]
	v_mfma_f32_16x16x32_bf16 v[142:145], v[128:131], v[192:195], v[142:145]
	v_mfma_f32_16x16x32_bf16 v[136:139], v[164:167], v[192:195], v[136:139]
	v_mfma_f32_16x16x32_bf16 v[118:121], v[128:131], v[200:203], v[118:121]
	v_mfma_f32_16x16x32_bf16 v[106:109], v[164:167], v[200:203], v[106:109]
	v_mfma_f32_16x16x32_bf16 v[102:105], v[128:131], v[208:211], v[102:105]
	v_mfma_f32_16x16x32_bf16 v[90:93], v[164:167], v[208:211], v[90:93]
	v_mfma_f32_16x16x32_bf16 v[86:89], v[128:131], v[216:219], v[86:89]
	v_mfma_f32_16x16x32_bf16 v[74:77], v[164:167], v[216:219], v[74:77]
	s_setprio 0
	s_setprio 1
	v_mfma_f32_16x16x32_bf16 v[114:117], v[172:175], v[188:191], v[114:117]
	v_mfma_f32_16x16x32_bf16 v[110:113], v[180:183], v[188:191], v[110:113]
	v_mfma_f32_16x16x32_bf16 v[98:101], v[172:175], v[196:199], v[98:101]
	v_mfma_f32_16x16x32_bf16 v[94:97], v[180:183], v[196:199], v[94:97]
	v_mfma_f32_16x16x32_bf16 v[82:85], v[172:175], v[204:207], v[82:85]
	v_mfma_f32_16x16x32_bf16 v[78:81], v[180:183], v[204:207], v[78:81]
	v_mfma_f32_16x16x32_bf16 v[70:73], v[172:175], v[212:215], v[70:73]
	v_mfma_f32_16x16x32_bf16 v[66:69], v[180:183], v[212:215], v[66:69]
	v_mfma_f32_16x16x32_bf16 v[114:117], v[176:179], v[192:195], v[114:117]
	v_mfma_f32_16x16x32_bf16 v[110:113], v[184:187], v[192:195], v[110:113]
	v_mfma_f32_16x16x32_bf16 v[98:101], v[176:179], v[200:203], v[98:101]
	v_mfma_f32_16x16x32_bf16 v[94:97], v[184:187], v[200:203], v[94:97]
	v_mfma_f32_16x16x32_bf16 v[82:85], v[176:179], v[208:211], v[82:85]
	v_mfma_f32_16x16x32_bf16 v[78:81], v[184:187], v[208:211], v[78:81]
	v_mfma_f32_16x16x32_bf16 v[70:73], v[176:179], v[216:219], v[70:73]
	v_mfma_f32_16x16x32_bf16 v[66:69], v[184:187], v[216:219], v[66:69]
	s_setprio 0
	s_barrier
	s_add_i32 s90, s82, s67
	v_lshl_add_u64 v[220:221], s[58:59], 0, v[150:151]
	s_mov_b32 m0, s90
	ds_read_b128 v[188:191], v170 offset:16384
	ds_read_b128 v[192:195], v170 offset:17408
	ds_read_b128 v[196:199], v170 offset:18432
	ds_read_b128 v[200:203], v170 offset:19456
	ds_read_b128 v[204:207], v170 offset:20480
	ds_read_b128 v[208:211], v170 offset:21504
	ds_read_b128 v[212:215], v170 offset:22528
	ds_read_b128 v[216:219], v170 offset:23552
	global_load_lds_dwordx4 v[220:221], off
	s_add_i32 m0, s90, 0x2000
	s_add_u32 s90, s58, 0x40000
	v_lshl_add_u64 v[222:223], s[58:59], 0, v[146:147]
	s_addc_u32 s91, s59, 0
	s_add_i32 s92, s83, s67
	global_load_lds_dwordx4 v[222:223], off
	v_lshl_add_u64 v[140:141], s[90:91], 0, v[150:151]
	s_mov_b32 m0, s92
	v_lshl_add_u64 v[224:225], s[60:61], 0, v[152:153]
	global_load_lds_dwordx4 v[140:141], off
	v_lshl_add_u64 v[140:141], s[90:91], 0, v[146:147]
	s_add_i32 m0, s92, 0x2000
	v_lshl_add_u64 v[226:227], s[60:61], 0, v[148:149]
	global_load_lds_dwordx4 v[140:141], off
	s_mov_b32 m0, s53
	s_nop 0
	global_load_lds_dwordx4 v[224:225], off
	s_mov_b32 m0, s70
	s_nop 0
	global_load_lds_dwordx4 v[226:227], off
	s_waitcnt vmcnt(8)
	s_waitcnt lgkmcnt(0)
	s_barrier
	s_setprio 1
	s_waitcnt lgkmcnt(0)
	v_mfma_f32_16x16x32_bf16 v[62:65], v[124:127], v[188:191], v[62:65]
	v_mfma_f32_16x16x32_bf16 v[58:61], v[132:135], v[188:191], v[58:61]
	v_mfma_f32_16x16x32_bf16 v[54:57], v[124:127], v[196:199], v[54:57]
	v_mfma_f32_16x16x32_bf16 v[42:45], v[132:135], v[196:199], v[42:45]
	v_mfma_f32_16x16x32_bf16 v[38:41], v[124:127], v[204:207], v[38:41]
	v_mfma_f32_16x16x32_bf16 v[26:29], v[132:135], v[204:207], v[26:29]
	v_mfma_f32_16x16x32_bf16 v[22:25], v[124:127], v[212:215], v[22:25]
	v_mfma_f32_16x16x32_bf16 v[10:13], v[132:135], v[212:215], v[10:13]
	v_mfma_f32_16x16x32_bf16 v[62:65], v[128:131], v[192:195], v[62:65]
	v_mfma_f32_16x16x32_bf16 v[58:61], v[164:167], v[192:195], v[58:61]
	v_mfma_f32_16x16x32_bf16 v[54:57], v[128:131], v[200:203], v[54:57]
	v_mfma_f32_16x16x32_bf16 v[42:45], v[164:167], v[200:203], v[42:45]
	v_mfma_f32_16x16x32_bf16 v[38:41], v[128:131], v[208:211], v[38:41]
	v_mfma_f32_16x16x32_bf16 v[26:29], v[164:167], v[208:211], v[26:29]
	v_mfma_f32_16x16x32_bf16 v[22:25], v[128:131], v[216:219], v[22:25]
	v_mfma_f32_16x16x32_bf16 v[10:13], v[164:167], v[216:219], v[10:13]
	s_setprio 0
	s_setprio 1
	v_mfma_f32_16x16x32_bf16 v[50:53], v[172:175], v[188:191], v[50:53]
	v_mfma_f32_16x16x32_bf16 v[46:49], v[180:183], v[188:191], v[46:49]
	v_mfma_f32_16x16x32_bf16 v[34:37], v[172:175], v[196:199], v[34:37]
	v_mfma_f32_16x16x32_bf16 v[30:33], v[180:183], v[196:199], v[30:33]
	v_mfma_f32_16x16x32_bf16 v[18:21], v[172:175], v[204:207], v[18:21]
	v_mfma_f32_16x16x32_bf16 v[14:17], v[180:183], v[204:207], v[14:17]
	v_mfma_f32_16x16x32_bf16 v[6:9], v[172:175], v[212:215], v[6:9]
	v_mfma_f32_16x16x32_bf16 v[2:5], v[180:183], v[212:215], v[2:5]
	v_mfma_f32_16x16x32_bf16 v[50:53], v[176:179], v[192:195], v[50:53]
	v_mfma_f32_16x16x32_bf16 v[46:49], v[184:187], v[192:195], v[46:49]
	v_mfma_f32_16x16x32_bf16 v[34:37], v[176:179], v[200:203], v[34:37]
	v_mfma_f32_16x16x32_bf16 v[30:33], v[184:187], v[200:203], v[30:33]
	v_mfma_f32_16x16x32_bf16 v[18:21], v[176:179], v[208:211], v[18:21]
	v_mfma_f32_16x16x32_bf16 v[14:17], v[184:187], v[208:211], v[14:17]
	v_mfma_f32_16x16x32_bf16 v[6:9], v[176:179], v[216:219], v[6:9]
	v_mfma_f32_16x16x32_bf16 v[2:5], v[184:187], v[216:219], v[2:5]
	s_setprio 0
	s_barrier
; #define PG8_STAGE_A(bufoff, kbase, h, gv) do { if constexpr (GATHER) { PG8_STAGE(bufoff, kbase, (gv)[h]); } else { PG8_STAGE(bufoff, (kbase) + (h) * hstep, voffA); } } while (0)
; #define PG8_WAIT_V(n) asm volatile("s_waitcnt vmcnt(" #n ")" ::: "memory")
; #define PG8_WAIT_L(n) asm volatile("s_waitcnt lgkmcnt(" #n ")" ::: "memory")
; #define PG8_BAR __builtin_amdgcn_s_barrier()
; #define PG8_SCHED __builtin_amdgcn_sched_barrier(0)
; template <class Epi, class Sched, bool ALIGN_EPI = false, bool SP2 = false, bool FP8 = false, bool GATHER = false>
; __device__ __forceinline__ void gemm_phase(PG8_LAS unsigned char* lds, const Gemm g, const Sched& S, const Epi& E) {
;     ...
;             PG8_LDB(B0, 1, 0); PG8_LDB(B1, 1, 1); PG8_SCHED; PG8_LDA(At, 1, 0); PG8_STAGE_A(PG8_SA(0, 1), a2, 1, gsel);
;             PG8_WAIT_V(8); PG8_WAIT_L(0); PG8_BAR; PG8_MMA(0, 0, At, B0); PG8_MMA(0, 1, At, B1); PG8_BAR; PG8_SCHED;
	s_add_i32 s90, 0, 0x18000
	v_add_u32_e32 v140, s90, v169
	s_add_i32 s91, 0, 0x1c000
	ds_read_b128 v[124:127], v140
	ds_read_b128 v[128:131], v140 offset:1024
	ds_read_b128 v[132:135], v140 offset:2048
	ds_read_b128 v[164:167], v140 offset:3072
	v_add_u32_e32 v140, s91, v169
	ds_read_b128 v[172:175], v140
	ds_read_b128 v[176:179], v140 offset:1024
	ds_read_b128 v[180:183], v140 offset:2048
	ds_read_b128 v[184:187], v140 offset:3072
	s_add_u32 s60, s60, 0x40000
	s_addc_u32 s61, s61, 0
	s_mov_b32 m0, s71
	v_lshl_add_u64 v[140:141], s[60:61], 0, v[152:153]
	ds_read_b128 v[188:191], v170 offset:32768
	ds_read_b128 v[192:195], v170 offset:33792
	ds_read_b128 v[196:199], v170 offset:34816
	ds_read_b128 v[200:203], v170 offset:35840
	ds_read_b128 v[204:207], v170 offset:36864
	ds_read_b128 v[208:211], v170 offset:37888
	ds_read_b128 v[212:215], v170 offset:38912
	ds_read_b128 v[216:219], v170 offset:39936
	global_load_lds_dwordx4 v[140:141], off
	v_lshl_add_u64 v[140:141], s[60:61], 0, v[148:149]
	s_mov_b32 m0, s72
	s_nop 0
	global_load_lds_dwordx4 v[140:141], off
	s_waitcnt vmcnt(8)
	s_waitcnt lgkmcnt(0)
	s_barrier
	s_setprio 1
	s_waitcnt lgkmcnt(0)
	v_mfma_f32_16x16x32_bf16 v[140:143], v[124:127], v[188:191], v[142:145]
	v_mfma_f32_16x16x32_bf16 v[136:139], v[132:135], v[188:191], v[136:139]
	v_mfma_f32_16x16x32_bf16 v[118:121], v[124:127], v[196:199], v[118:121]
	v_mfma_f32_16x16x32_bf16 v[106:109], v[132:135], v[196:199], v[106:109]
	v_mfma_f32_16x16x32_bf16 v[102:105], v[124:127], v[204:207], v[102:105]
	v_mfma_f32_16x16x32_bf16 v[90:93], v[132:135], v[204:207], v[90:93]
	v_mfma_f32_16x16x32_bf16 v[86:89], v[124:127], v[212:215], v[86:89]
	v_mfma_f32_16x16x32_bf16 v[74:77], v[132:135], v[212:215], v[74:77]
	v_mfma_f32_16x16x32_bf16 v[142:145], v[128:131], v[192:195], v[140:143]
	v_mfma_f32_16x16x32_bf16 v[138:141], v[164:167], v[192:195], v[136:139]
	v_mfma_f32_16x16x32_bf16 v[118:121], v[128:131], v[200:203], v[118:121]
	v_mfma_f32_16x16x32_bf16 v[106:109], v[164:167], v[200:203], v[106:109]
	v_mfma_f32_16x16x32_bf16 v[102:105], v[128:131], v[208:211], v[102:105]
	v_mfma_f32_16x16x32_bf16 v[90:93], v[164:167], v[208:211], v[90:93]
	v_mfma_f32_16x16x32_bf16 v[86:89], v[128:131], v[216:219], v[86:89]
	v_mfma_f32_16x16x32_bf16 v[74:77], v[164:167], v[216:219], v[74:77]
	s_setprio 0
	s_setprio 1
	v_mfma_f32_16x16x32_bf16 v[114:117], v[172:175], v[188:191], v[114:117]
	v_mfma_f32_16x16x32_bf16 v[110:113], v[180:183], v[188:191], v[110:113]
	v_mfma_f32_16x16x32_bf16 v[98:101], v[172:175], v[196:199], v[98:101]
	v_mfma_f32_16x16x32_bf16 v[94:97], v[180:183], v[196:199], v[94:97]
	v_mfma_f32_16x16x32_bf16 v[82:85], v[172:175], v[204:207], v[82:85]
	v_mfma_f32_16x16x32_bf16 v[78:81], v[180:183], v[204:207], v[78:81]
	v_mfma_f32_16x16x32_bf16 v[70:73], v[172:175], v[212:215], v[70:73]
	v_mfma_f32_16x16x32_bf16 v[66:69], v[180:183], v[212:215], v[66:69]
	v_mfma_f32_16x16x32_bf16 v[114:117], v[176:179], v[192:195], v[114:117]
	v_mfma_f32_16x16x32_bf16 v[110:113], v[184:187], v[192:195], v[110:113]
	v_mfma_f32_16x16x32_bf16 v[98:101], v[176:179], v[200:203], v[98:101]
	v_mfma_f32_16x16x32_bf16 v[94:97], v[184:187], v[200:203], v[94:97]
	v_mfma_f32_16x16x32_bf16 v[82:85], v[176:179], v[208:211], v[82:85]
	v_mfma_f32_16x16x32_bf16 v[78:81], v[184:187], v[208:211], v[78:81]
	v_mfma_f32_16x16x32_bf16 v[70:73], v[176:179], v[216:219], v[70:73]
	v_mfma_f32_16x16x32_bf16 v[66:69], v[184:187], v[216:219], v[66:69]
	s_setprio 0
	s_barrier
; #define PG8_STAGE(bufoff, gbase, voff) do { _Pragma("unroll") for (int _i = 0; _i < 2; ++_i) \
;         __builtin_amdgcn_global_load_lds((const unsigned*)((const char*)(gbase) + (voff)[_i]), (PG8_LAS unsigned*)(lds + (bufoff) + ldsw + _i * 8192), 16, 0, 0); } while (0)
; #define PG8_STAGE_A(bufoff, kbase, h, gv) do { if constexpr (GATHER) { PG8_STAGE(bufoff, kbase, (gv)[h]); } else { PG8_STAGE(bufoff, (kbase) + (h) * hstep, voffA); } } while (0)
; #define PG8_WAIT_V(n) asm volatile("s_waitcnt vmcnt(" #n ")" ::: "memory")
; #define PG8_WAIT_L(n) asm volatile("s_waitcnt lgkmcnt(" #n ")" ::: "memory")
; #define PG8_BAR __builtin_amdgcn_s_barrier()
; #define PG8_SCHED __builtin_amdgcn_sched_barrier(0)
; template <class Epi, class Sched, bool ALIGN_EPI = false, bool SP2 = false, bool FP8 = false, bool GATHER = false>
; __device__ __forceinline__ void gemm_phase(PG8_LAS unsigned char* lds, const Gemm g, const Sched& S, const Epi& E) {
;     ...
;         for (int t = 0; t < nt; t += 2) {
;             const bool last = (t == nt - 2);
;             const char* a1 = cA + (size_t)(t + 1) * kstep;
;             const char* a2 = last ? nA : cA + (size_t)(t + 2) * kstep; const char* b2 = last ? nB : cB + (size_t)(t + 2) * kstep;
;             const char* a3 = a2 + kstep; const char* b3 = b2 + kstep;
;     ...
;             PG8_LDA(At, 1, 1); PG8_STAGE(PG8_SB(1, 0), b3, voffB); PG8_STAGE(PG8_SB(1, 1), b3 + hstep, voffB); PG8_STAGE_A(PG8_SA(1, 0), a3, 0, gsel);
;             PG8_WAIT_V(8); PG8_WAIT_L(0); PG8_BAR; PG8_MMA(1, 0, At, B0); PG8_MMA(1, 1, At, B1); PG8_BAR; PG8_SCHED;
	s_add_i32 s60, s90, s67
	v_lshl_add_u64 v[136:137], v[220:221], 0, s[18:19]
	s_mov_b32 m0, s60
	ds_read_b128 v[188:191], v170 offset:49152
	ds_read_b128 v[192:195], v170 offset:50176
	ds_read_b128 v[196:199], v170 offset:51200
	ds_read_b128 v[200:203], v170 offset:52224
	ds_read_b128 v[204:207], v170 offset:53248
	ds_read_b128 v[208:211], v170 offset:54272
	ds_read_b128 v[212:215], v170 offset:55296
	ds_read_b128 v[216:219], v170 offset:56320
	global_load_lds_dwordx4 v[136:137], off
	s_add_i32 m0, s60, 0x2000
	s_add_u32 s58, s58, 0x40080
	v_lshl_add_u64 v[136:137], v[222:223], 0, s[18:19]
	s_addc_u32 s59, s59, 0
	s_add_i32 s60, s91, s67
	global_load_lds_dwordx4 v[136:137], off
	v_lshl_add_u64 v[136:137], s[58:59], 0, v[150:151]
	s_mov_b32 m0, s60
	s_nop 0
	global_load_lds_dwordx4 v[136:137], off
	v_lshl_add_u64 v[136:137], s[58:59], 0, v[146:147]
	s_add_i32 m0, s60, 0x2000
	s_nop 0
	global_load_lds_dwordx4 v[136:137], off
	v_lshl_add_u64 v[136:137], v[224:225], 0, s[18:19]
	s_mov_b32 m0, s78
	s_nop 0
	global_load_lds_dwordx4 v[136:137], off
	v_lshl_add_u64 v[136:137], v[226:227], 0, s[18:19]
	s_mov_b32 m0, s79
	s_nop 0
	global_load_lds_dwordx4 v[136:137], off
	s_waitcnt vmcnt(8)
	s_waitcnt lgkmcnt(0)
	s_barrier
	s_setprio 1
	s_waitcnt lgkmcnt(0)
	v_mfma_f32_16x16x32_bf16 v[62:65], v[124:127], v[188:191], v[62:65]
	v_mfma_f32_16x16x32_bf16 v[58:61], v[132:135], v[188:191], v[58:61]
	v_mfma_f32_16x16x32_bf16 v[54:57], v[124:127], v[196:199], v[54:57]
	v_mfma_f32_16x16x32_bf16 v[42:45], v[132:135], v[196:199], v[42:45]
	v_mfma_f32_16x16x32_bf16 v[38:41], v[124:127], v[204:207], v[38:41]
	v_mfma_f32_16x16x32_bf16 v[26:29], v[132:135], v[204:207], v[26:29]
	v_mfma_f32_16x16x32_bf16 v[22:25], v[124:127], v[212:215], v[22:25]
	v_mfma_f32_16x16x32_bf16 v[10:13], v[132:135], v[212:215], v[10:13]
	v_mfma_f32_16x16x32_bf16 v[62:65], v[128:131], v[192:195], v[62:65]
	v_mfma_f32_16x16x32_bf16 v[58:61], v[164:167], v[192:195], v[58:61]
	v_mfma_f32_16x16x32_bf16 v[54:57], v[128:131], v[200:203], v[54:57]
	v_mfma_f32_16x16x32_bf16 v[42:45], v[164:167], v[200:203], v[42:45]
	v_mfma_f32_16x16x32_bf16 v[38:41], v[128:131], v[208:211], v[38:41]
	v_mfma_f32_16x16x32_bf16 v[26:29], v[164:167], v[208:211], v[26:29]
	v_mfma_f32_16x16x32_bf16 v[22:25], v[128:131], v[216:219], v[22:25]
	v_mfma_f32_16x16x32_bf16 v[10:13], v[164:167], v[216:219], v[10:13]
	s_setprio 0
	s_setprio 1
	v_mfma_f32_16x16x32_bf16 v[50:53], v[172:175], v[188:191], v[50:53]
	v_mfma_f32_16x16x32_bf16 v[46:49], v[180:183], v[188:191], v[46:49]
	v_mfma_f32_16x16x32_bf16 v[34:37], v[172:175], v[196:199], v[34:37]
	v_mfma_f32_16x16x32_bf16 v[30:33], v[180:183], v[196:199], v[30:33]
	v_mfma_f32_16x16x32_bf16 v[18:21], v[172:175], v[204:207], v[18:21]
	v_mfma_f32_16x16x32_bf16 v[14:17], v[180:183], v[204:207], v[14:17]
	v_mfma_f32_16x16x32_bf16 v[6:9], v[172:175], v[212:215], v[6:9]
	v_mfma_f32_16x16x32_bf16 v[2:5], v[180:183], v[212:215], v[2:5]
	v_mfma_f32_16x16x32_bf16 v[50:53], v[176:179], v[192:195], v[50:53]
	v_mfma_f32_16x16x32_bf16 v[46:49], v[184:187], v[192:195], v[46:49]
	v_mfma_f32_16x16x32_bf16 v[34:37], v[176:179], v[200:203], v[34:37]
	v_mfma_f32_16x16x32_bf16 v[30:33], v[184:187], v[200:203], v[30:33]
	v_mfma_f32_16x16x32_bf16 v[18:21], v[176:179], v[208:211], v[18:21]
	v_mfma_f32_16x16x32_bf16 v[14:17], v[184:187], v[208:211], v[14:17]
	v_mfma_f32_16x16x32_bf16 v[6:9], v[176:179], v[216:219], v[6:9]
	v_mfma_f32_16x16x32_bf16 v[2:5], v[184:187], v[216:219], v[2:5]
	s_setprio 0
	s_add_i32 s89, s89, 2
	s_add_u32 s56, s56, 0x100
	s_addc_u32 s57, s57, 0
	s_add_u32 s55, s55, 0x100
	s_addc_u32 s88, s88, 0
	s_cmp_gt_u32 s89, 13
	s_cbranch_scc1 .Lrot592_exit
	s_cmp_lg_u32 s89, 12
	s_cselect_b64 s[58:59], -1, 0
	s_or_b64 s[60:61], s[58:59], s[20:21]
	s_and_b64 vcc, exec, s[60:61]
	s_cbranch_vccnz .Lrot592_head
	s_barrier

; #define PG8_STAGE(bufoff, gbase, voff) do { _Pragma("unroll") for (int _i = 0; _i < 2; ++_i) \
;         __builtin_amdgcn_global_load_lds((const unsigned*)((const char*)(gbase) + (voff)[_i]), (PG8_LAS unsigned*)(lds + (bufoff) + ldsw + _i * 8192), 16, 0, 0); } while (0)
; #define PG8_STAGE_A(bufoff, kbase, h, gv) do { if constexpr (GATHER) { PG8_STAGE(bufoff, kbase, (gv)[h]); } else { PG8_STAGE(bufoff, (kbase) + (h) * hstep, voffA); } } while (0)
; #define PG8_WAIT_V(n) asm volatile("s_waitcnt vmcnt(" #n ")" ::: "memory")
; #define PG8_WAIT_L(n) asm volatile("s_waitcnt lgkmcnt(" #n ")" ::: "memory")
; #define PG8_BAR __builtin_amdgcn_s_barrier()
; template <class Epi, class Sched, bool ALIGN_EPI = false, bool SP2 = false, bool FP8 = false, bool GATHER = false>
; __device__ __forceinline__ void gemm_phase(PG8_LAS unsigned char* lds, const Gemm g, const Sched& S, const Epi& E) {
;     ...
;             const char* a2 = last ? nA : cA + (size_t)(t + 2) * kstep; const char* b2 = last ? nB : cB + (size_t)(t + 2) * kstep;
;             const char* a3 = a2 + kstep; const char* b3 = b2 + kstep;
;             if (last && has_next) S.a_ready(nxt);
;             if (last) E.pre(cur, wid, lane);
;             if constexpr (GATHER) { if (t == nt - 4 && has_next) { _Pragma("unroll") for (int h_ = 0; h_ < 2; ++h_) _Pragma("unroll") for (int i_ = 0; i_ < 2; ++i_)
;                 asm volatile("global_load_dword %0, %1, off" : "+v"(graw[h_][i_]) : "v"(S.rowtok + (nxt.pm * BM + h_ * HALF + gR[i_])) : "memory"); } }
;             unsigned gsel[2][2];
;             if constexpr (GATHER) { _Pragma("unroll") for (int h_ = 0; h_ < 2; ++h_) _Pragma("unroll") for (int i_ = 0; i_ < 2; ++i_) { if (last && has_next) gnxt[h_][i_] = graw[h_][i_] * (unsigned)(K * 2) + gC[i_]; gsel[h_][i_] = (last && has_next) ? gnxt[h_][i_] : gcur[h_][i_]; } }
;             if constexpr (SP2) {
;             PG8_LDB(B0, 0, 0); PG8_LDB(B1, 0, 1); PG8_SCHED; PG8_LDA(At, 0, 0); PG8_STAGE_A(PG8_SA(1, 1), a1, 1, gcur);
;             PG8_WAIT_V(8); PG8_WAIT_L(0); PG8_BAR; PG8_MMA(0, 0, At, B0); PG8_MMA(0, 1, At, B1); PG8_BAR; PG8_SCHED;
;             PG8_LDA(At, 0, 1); PG8_STAGE(PG8_SB(0, 0), b2, voffB); PG8_STAGE(PG8_SB(0, 1), b2 + hstep, voffB); PG8_STAGE_A(PG8_SA(0, 0), a2, 0, gsel);
;             PG8_WAIT_V(8); PG8_WAIT_L(0); PG8_BAR; PG8_MMA(1, 0, At, B0); PG8_MMA(1, 1, At, B1); PG8_BAR; PG8_SCHED;
.Lpeel878_body:
	s_add_u32 s52, s8, s48
	s_addc_u32 s53, s9, s49
	s_add_u32 s54, s52, 0x19200100
	s_addc_u32 s55, s53, 0
	s_and_b64 s[52:53], s[56:57], exec
	s_cselect_b32 s55, s11, s55
	s_cselect_b32 s54, s10, s54
	s_add_u32 s86, s22, s48
	s_addc_u32 s87, s84, s49
	s_and_b64 s[52:53], s[56:57], exec
	s_cselect_b32 s53, s45, s87
	s_cselect_b32 s52, s44, s86
	v_lshl_add_u32 v2, v213, 10, v1
	s_and_b64 vcc, s[46:47], s[56:57]
	v_cndmask_b32_e32 v209, v209, v2, vcc
	v_cndmask_b32_e32 v170, v217, v2, vcc
	v_lshl_add_u32 v2, v214, 10, v204
	v_cndmask_b32_e32 v210, v210, v2, vcc
	v_cndmask_b32_e32 v200, v180, v2, vcc
	v_add_u32_e32 v2, s76, v206
	v_add_u32_e32 v14, s77, v206
	ds_read_b128 v[18:21], v2
	ds_read_b128 v[22:25], v2 offset:1024
	ds_read_b128 v[26:29], v2 offset:2048
	ds_read_b128 v[30:33], v2 offset:3072
	ds_read_b128 v[2:5], v14
	ds_read_b128 v[6:9], v14 offset:1024
	ds_read_b128 v[10:13], v14 offset:2048
	ds_read_b128 v[14:17], v14 offset:3072
	v_lshl_add_u32 v177, v215, 10, v1
	v_lshl_add_u32 v179, v216, 10, v204
	v_cndmask_b32_e32 v211, v211, v177, vcc
	v_cndmask_b32_e32 v212, v212, v179, vcc
	v_cndmask_b32_e32 v177, v178, v177, vcc
	v_cndmask_b32_e32 v179, v176, v179, vcc
	v_lshl_add_u64 v[196:197], v[194:195], 0, s[48:49]
	s_add_i32 m0, s63, 0xc000
	ds_read_b128 v[218:221], v207
	ds_read_b128 v[222:225], v207 offset:1024
	ds_read_b128 v[226:229], v207 offset:2048
	ds_read_b128 v[230:233], v207 offset:3072
	ds_read_b128 v[234:237], v207 offset:4096
	ds_read_b128 v[238:241], v207 offset:5120
	ds_read_b128 v[242:245], v207 offset:6144
	ds_read_b128 v[246:249], v207 offset:7168
	global_load_lds_dwordx4 v[196:197], off
	v_lshl_add_u64 v[196:197], v[192:193], 0, s[48:49]
	s_add_i32 m0, s63, 0xe000
	s_nop 0
	global_load_lds_dwordx4 v[196:197], off
	s_waitcnt vmcnt(8)
	s_waitcnt lgkmcnt(0)
	s_barrier
	s_setprio 1
	s_waitcnt lgkmcnt(0)
	v_mfma_f32_16x16x128_f8f6f4 v[158:161], v[18:25], v[218:225], 0
	v_mfma_f32_16x16x128_f8f6f4 v[150:153], v[26:33], v[218:225], 0
	v_mfma_f32_16x16x128_f8f6f4 v[142:145], v[18:25], v[226:233], 0
	v_mfma_f32_16x16x128_f8f6f4 v[134:137], v[26:33], v[226:233], 0
	v_mfma_f32_16x16x128_f8f6f4 v[126:129], v[18:25], v[234:241], 0
	v_mfma_f32_16x16x128_f8f6f4 v[118:121], v[26:33], v[234:241], 0
	v_mfma_f32_16x16x128_f8f6f4 v[110:113], v[18:25], v[242:249], 0
	v_mfma_f32_16x16x128_f8f6f4 v[102:105], v[26:33], v[242:249], 0
	s_setprio 0
	s_setprio 1
	v_mfma_f32_16x16x128_f8f6f4 v[154:157], v[2:9], v[218:225], 0
	v_mfma_f32_16x16x128_f8f6f4 v[146:149], v[10:17], v[218:225], 0
	v_mfma_f32_16x16x128_f8f6f4 v[138:141], v[2:9], v[226:233], 0
	v_mfma_f32_16x16x128_f8f6f4 v[130:133], v[10:17], v[226:233], 0
	v_mfma_f32_16x16x128_f8f6f4 v[122:125], v[2:9], v[234:241], 0
	v_mfma_f32_16x16x128_f8f6f4 v[114:117], v[10:17], v[234:241], 0
	v_mfma_f32_16x16x128_f8f6f4 v[106:109], v[2:9], v[242:249], 0
	v_mfma_f32_16x16x128_f8f6f4 v[98:101], v[10:17], v[242:249], 0
	s_setprio 0
	s_barrier
	s_add_i32 s56, s76, s60
	v_lshl_add_u64 v[196:197], s[52:53], 0, v[168:169]
	s_mov_b32 m0, s56
	ds_read_b128 v[218:221], v207 offset:16384
	ds_read_b128 v[222:225], v207 offset:17408
	ds_read_b128 v[226:229], v207 offset:18432
	ds_read_b128 v[230:233], v207 offset:19456
	ds_read_b128 v[234:237], v207 offset:20480
	ds_read_b128 v[238:241], v207 offset:21504
	ds_read_b128 v[242:245], v207 offset:22528
	ds_read_b128 v[246:249], v207 offset:23552
	global_load_lds_dwordx4 v[196:197], off
	s_add_i32 m0, s56, 0x2000
	s_add_u32 s56, s52, 0x20000
	v_lshl_add_u64 v[198:199], s[52:53], 0, v[166:167]
	s_addc_u32 s57, s53, 0
	s_add_i32 s86, s77, s60
	global_load_lds_dwordx4 v[198:199], off
	v_lshl_add_u64 v[202:203], s[56:57], 0, v[168:169]
	s_mov_b32 m0, s86
	v_mov_b32_e32 v201, v171
	global_load_lds_dwordx4 v[202:203], off
	v_lshl_add_u64 v[202:203], s[56:57], 0, v[166:167]
	s_add_i32 m0, s86, 0x2000
	s_nop 0
	global_load_lds_dwordx4 v[202:203], off
	s_mov_b32 m0, s63
	v_lshl_add_u64 v[202:203], s[54:55], 0, v[170:171]
	global_load_lds_dwordx4 v170, s[54:55]
	s_mov_b32 m0, s65
	s_nop 0
	global_load_lds_dwordx4 v200, s[54:55]
	s_waitcnt vmcnt(8)
	s_waitcnt lgkmcnt(0)
	v_lshl_add_u64 v[200:201], s[54:55], 0, v[200:201]
	s_barrier
	s_setprio 1
	s_waitcnt lgkmcnt(0)
	v_mfma_f32_16x16x128_f8f6f4 v[94:97], v[18:25], v[218:225], 0
	v_mfma_f32_16x16x128_f8f6f4 v[86:89], v[26:33], v[218:225], 0
	v_mfma_f32_16x16x128_f8f6f4 v[78:81], v[18:25], v[226:233], 0
	v_mfma_f32_16x16x128_f8f6f4 v[70:73], v[26:33], v[226:233], 0
	v_mfma_f32_16x16x128_f8f6f4 v[62:65], v[18:25], v[234:241], 0
	v_mfma_f32_16x16x128_f8f6f4 v[54:57], v[26:33], v[234:241], 0
	v_mfma_f32_16x16x128_f8f6f4 v[46:49], v[18:25], v[242:249], 0
	v_mfma_f32_16x16x128_f8f6f4 v[38:41], v[26:33], v[242:249], 0
	s_setprio 0
	s_setprio 1
	v_mfma_f32_16x16x128_f8f6f4 v[90:93], v[2:9], v[218:225], 0
	v_mfma_f32_16x16x128_f8f6f4 v[82:85], v[10:17], v[218:225], 0
	v_mfma_f32_16x16x128_f8f6f4 v[74:77], v[2:9], v[226:233], 0
	v_mfma_f32_16x16x128_f8f6f4 v[66:69], v[10:17], v[226:233], 0
	v_mfma_f32_16x16x128_f8f6f4 v[58:61], v[2:9], v[234:241], 0
	v_mfma_f32_16x16x128_f8f6f4 v[50:53], v[10:17], v[234:241], 0
	v_mfma_f32_16x16x128_f8f6f4 v[42:45], v[2:9], v[242:249], 0
	v_mfma_f32_16x16x128_f8f6f4 v[34:37], v[10:17], v[242:249], 0
	s_setprio 0
	s_barrier
; #define PG8_STAGE(bufoff, gbase, voff) do { _Pragma("unroll") for (int _i = 0; _i < 2; ++_i) \
;         __builtin_amdgcn_global_load_lds((const unsigned*)((const char*)(gbase) + (voff)[_i]), (PG8_LAS unsigned*)(lds + (bufoff) + ldsw + _i * 8192), 16, 0, 0); } while (0)
; #define PG8_STAGE_A(bufoff, kbase, h, gv) do { if constexpr (GATHER) { PG8_STAGE(bufoff, kbase, (gv)[h]); } else { PG8_STAGE(bufoff, (kbase) + (h) * hstep, voffA); } } while (0)
; #define PG8_WAIT_V(n) asm volatile("s_waitcnt vmcnt(" #n ")" ::: "memory")
; template <class Epi, class Sched, bool ALIGN_EPI = false, bool SP2 = false, bool FP8 = false, bool GATHER = false>
; __device__ __forceinline__ void gemm_phase(PG8_LAS unsigned char* lds, const Gemm g, const Sched& S, const Epi& E) {
;     ...
;         for (int t = 0; t < nt; t += 2) {
;             const bool last = (t == nt - 2);
;             const char* a1 = cA + (size_t)(t + 1) * kstep;
;             const char* a2 = last ? nA : cA + (size_t)(t + 2) * kstep; const char* b2 = last ? nB : cB + (size_t)(t + 2) * kstep;
;             const char* a3 = a2 + kstep; const char* b3 = b2 + kstep;
;             if (last && has_next) S.a_ready(nxt);
;             if (last) E.pre(cur, wid, lane);
;             if constexpr (GATHER) { if (t == nt - 4 && has_next) { _Pragma("unroll") for (int h_ = 0; h_ < 2; ++h_) _Pragma("unroll") for (int i_ = 0; i_ < 2; ++i_)
;                 asm volatile("global_load_dword %0, %1, off" : "+v"(graw[h_][i_]) : "v"(S.rowtok + (nxt.pm * BM + h_ * HALF + gR[i_])) : "memory"); } }
;             unsigned gsel[2][2];
;             if constexpr (GATHER) { _Pragma("unroll") for (int h_ = 0; h_ < 2; ++h_) _Pragma("unroll") for (int i_ = 0; i_ < 2; ++i_) { if (last && has_next) gnxt[h_][i_] = graw[h_][i_] * (unsigned)(K * 2) + gC[i_]; gsel[h_][i_] = (last && has_next) ? gnxt[h_][i_] : gcur[h_][i_]; } }
;     ...
;             PG8_LDB(B0, 1, 0); PG8_LDB(B1, 1, 1); PG8_SCHED; PG8_LDA(At, 1, 0); PG8_STAGE_A(PG8_SA(0, 1), a2, 1, gsel);
;             PG8_WAIT_V(8); PG8_WAIT_L(0); PG8_BAR; PG8_MMA(0, 0, At, B0); PG8_MMA(0, 1, At, B1); PG8_BAR; PG8_SCHED;
;             PG8_LDA(At, 1, 1); PG8_STAGE(PG8_SB(1, 0), b3, voffB); PG8_STAGE(PG8_SB(1, 1), b3 + hstep, voffB); PG8_STAGE_A(PG8_SA(1, 0), a3, 0, gsel);
;             PG8_WAIT_V(8); PG8_WAIT_L(0); PG8_BAR; PG8_MMA(1, 0, At, B0); PG8_MMA(1, 1, At, B1); PG8_BAR; PG8_SCHED;
	s_add_i32 s56, 0, 0x18000
	s_add_i32 s57, 0, 0x1c000
	v_add_u32_e32 v14, s56, v206
	v_add_u32_e32 v30, s57, v206
	ds_read_b128 v[2:5], v14
	ds_read_b128 v[6:9], v14 offset:1024
	ds_read_b128 v[10:13], v14 offset:2048
	ds_read_b128 v[14:17], v14 offset:3072
	ds_read_b128 v[18:21], v30
	ds_read_b128 v[22:25], v30 offset:1024
	ds_read_b128 v[26:29], v30 offset:2048
	ds_read_b128 v[30:33], v30 offset:3072
	s_mov_b32 m0, s66
	ds_read_b128 v[218:221], v207 offset:32768
	ds_read_b128 v[222:225], v207 offset:33792
	ds_read_b128 v[226:229], v207 offset:34816
	ds_read_b128 v[230:233], v207 offset:35840
	ds_read_b128 v[234:237], v207 offset:36864
	ds_read_b128 v[238:241], v207 offset:37888
	ds_read_b128 v[242:245], v207 offset:38912
	ds_read_b128 v[246:249], v207 offset:39936
	global_load_lds_dwordx4 v177, s[54:55]
	s_mov_b32 m0, s67
	s_nop 0
	global_load_lds_dwordx4 v179, s[54:55]
	s_waitcnt vmcnt(8)
	s_waitcnt lgkmcnt(0)
	s_barrier
	s_setprio 1
	s_waitcnt lgkmcnt(0)
	v_mfma_f32_16x16x128_f8f6f4 v[158:161], v[2:9], v[218:225], v[158:161]
	v_mfma_f32_16x16x128_f8f6f4 v[150:153], v[10:17], v[218:225], v[150:153]
	v_mfma_f32_16x16x128_f8f6f4 v[142:145], v[2:9], v[226:233], v[142:145]
	v_mfma_f32_16x16x128_f8f6f4 v[134:137], v[10:17], v[226:233], v[134:137]
	v_mfma_f32_16x16x128_f8f6f4 v[126:129], v[2:9], v[234:241], v[126:129]
	v_mfma_f32_16x16x128_f8f6f4 v[118:121], v[10:17], v[234:241], v[118:121]
	v_mfma_f32_16x16x128_f8f6f4 v[110:113], v[2:9], v[242:249], v[110:113]
	v_mfma_f32_16x16x128_f8f6f4 v[102:105], v[10:17], v[242:249], v[102:105]
	s_setprio 0
	s_setprio 1
	v_mfma_f32_16x16x128_f8f6f4 v[154:157], v[18:25], v[218:225], v[154:157]
	v_mfma_f32_16x16x128_f8f6f4 v[146:149], v[26:33], v[218:225], v[146:149]
	v_mfma_f32_16x16x128_f8f6f4 v[138:141], v[18:25], v[226:233], v[138:141]
	v_mfma_f32_16x16x128_f8f6f4 v[130:133], v[26:33], v[226:233], v[130:133]
	v_mfma_f32_16x16x128_f8f6f4 v[122:125], v[18:25], v[234:241], v[122:125]
	v_mfma_f32_16x16x128_f8f6f4 v[114:117], v[26:33], v[234:241], v[114:117]
	v_mfma_f32_16x16x128_f8f6f4 v[106:109], v[18:25], v[242:249], v[106:109]
	v_mfma_f32_16x16x128_f8f6f4 v[98:101], v[26:33], v[242:249], v[98:101]
	s_setprio 0
	s_barrier
	s_add_i32 s54, s56, s60
	v_lshl_add_u64 v[196:197], v[196:197], 0, s[18:19]
	s_mov_b32 m0, s54
	ds_read_b128 v[218:221], v207 offset:49152
	ds_read_b128 v[222:225], v207 offset:50176
	ds_read_b128 v[226:229], v207 offset:51200
	ds_read_b128 v[230:233], v207 offset:52224
	ds_read_b128 v[234:237], v207 offset:53248
	ds_read_b128 v[238:241], v207 offset:54272
	ds_read_b128 v[242:245], v207 offset:55296
	ds_read_b128 v[246:249], v207 offset:56320
	global_load_lds_dwordx4 v[196:197], off
	s_add_i32 m0, s54, 0x2000
	s_add_u32 s52, s52, 0x20080
	v_lshl_add_u64 v[196:197], v[198:199], 0, s[18:19]
	s_addc_u32 s53, s53, 0
	s_add_i32 s54, s57, s60
	global_load_lds_dwordx4 v[196:197], off
	v_lshl_add_u64 v[196:197], s[52:53], 0, v[168:169]
	s_mov_b32 m0, s54
	s_nop 0
	global_load_lds_dwordx4 v[196:197], off
	v_lshl_add_u64 v[196:197], s[52:53], 0, v[166:167]
	s_add_i32 m0, s54, 0x2000
	s_nop 0
	global_load_lds_dwordx4 v[196:197], off
	v_lshl_add_u64 v[196:197], v[202:203], 0, s[18:19]
	s_mov_b32 m0, s70
	s_nop 0
	global_load_lds_dwordx4 v[196:197], off
	v_lshl_add_u64 v[196:197], v[200:201], 0, s[18:19]
	s_mov_b32 m0, s71
	s_nop 0
	global_load_lds_dwordx4 v[196:197], off
	s_waitcnt vmcnt(8)
	s_waitcnt lgkmcnt(0)
	s_barrier
	s_setprio 1
	s_waitcnt lgkmcnt(0)
	v_mfma_f32_16x16x128_f8f6f4 v[94:97], v[2:9], v[218:225], v[94:97]
	v_mfma_f32_16x16x128_f8f6f4 v[86:89], v[10:17], v[218:225], v[86:89]
	v_mfma_f32_16x16x128_f8f6f4 v[78:81], v[2:9], v[226:233], v[78:81]
	v_mfma_f32_16x16x128_f8f6f4 v[70:73], v[10:17], v[226:233], v[70:73]
	v_mfma_f32_16x16x128_f8f6f4 v[62:65], v[2:9], v[234:241], v[62:65]
	v_mfma_f32_16x16x128_f8f6f4 v[54:57], v[10:17], v[234:241], v[54:57]
	v_mfma_f32_16x16x128_f8f6f4 v[46:49], v[2:9], v[242:249], v[46:49]
	v_mfma_f32_16x16x128_f8f6f4 v[38:41], v[10:17], v[242:249], v[38:41]
	s_setprio 0
	s_setprio 1
	v_mfma_f32_16x16x128_f8f6f4 v[90:93], v[18:25], v[218:225], v[90:93]
	v_mfma_f32_16x16x128_f8f6f4 v[82:85], v[26:33], v[218:225], v[82:85]
	v_mfma_f32_16x16x128_f8f6f4 v[74:77], v[18:25], v[226:233], v[74:77]
	v_mfma_f32_16x16x128_f8f6f4 v[66:69], v[26:33], v[226:233], v[66:69]
	v_mfma_f32_16x16x128_f8f6f4 v[58:61], v[18:25], v[234:241], v[58:61]
	v_mfma_f32_16x16x128_f8f6f4 v[50:53], v[26:33], v[234:241], v[50:53]
	v_mfma_f32_16x16x128_f8f6f4 v[42:45], v[18:25], v[242:249], v[42:45]
	v_mfma_f32_16x16x128_f8f6f4 v[34:37], v[26:33], v[242:249], v[34:37]
	s_setprio 0
	s_add_i32 s85, s85, 2
	s_add_u32 s48, s48, 0x100
	s_addc_u32 s49, s49, 0
	s_cmp_gt_u32 s85, 5
	s_cbranch_scc1 .Lrot878_exit
	s_cmpk_eq_i32 s48, 0x300
	s_cselect_b64 s[56:57], -1, 0
	s_and_b64 s[52:53], s[56:57], s[24:25]
	s_andn2_b64 vcc, exec, s[52:53]
	s_cbranch_vccz .Lrot878_rare0
	s_cmpk_lg_i32 s48, 0x200
	s_cselect_b64 s[52:53], -1, 0
	s_or_b64 s[52:53], s[50:51], s[52:53]
	s_and_b64 vcc, exec, s[52:53]
	s_cbranch_vccnz .Lrot878_head
.Lrot878_rare0:
	s_barrier
	s_branch .LBB0_879

; #define PG8_STAGE(bufoff, gbase, voff) do { _Pragma("unroll") for (int _i = 0; _i < 2; ++_i) \
;         __builtin_amdgcn_global_load_lds((const unsigned*)((const char*)(gbase) + (voff)[_i]), (PG8_LAS unsigned*)(lds + (bufoff) + ldsw + _i * 8192), 16, 0, 0); } while (0)
; #define PG8_STAGE_A(bufoff, kbase, h, gv) do { if constexpr (GATHER) { PG8_STAGE(bufoff, kbase, (gv)[h]); } else { PG8_STAGE(bufoff, (kbase) + (h) * hstep, voffA); } } while (0)
; #define PG8_WAIT_V(n) asm volatile("s_waitcnt vmcnt(" #n ")" ::: "memory")
; #define PG8_WAIT_L(n) asm volatile("s_waitcnt lgkmcnt(" #n ")" ::: "memory")
; #define PG8_BAR __builtin_amdgcn_s_barrier()
; template <class Epi, class Sched, bool ALIGN_EPI = false, bool SP2 = false, bool FP8 = false, bool GATHER = false>
; __device__ __forceinline__ void gemm_phase(PG8_LAS unsigned char* lds, const Gemm g, const Sched& S, const Epi& E) {
;     ...
;             const char* a2 = last ? nA : cA + (size_t)(t + 2) * kstep; const char* b2 = last ? nB : cB + (size_t)(t + 2) * kstep;
;             const char* a3 = a2 + kstep; const char* b3 = b2 + kstep;
;             if (last && has_next) S.a_ready(nxt);
;             if (last) E.pre(cur, wid, lane);
;             if constexpr (GATHER) { if (t == nt - 4 && has_next) { _Pragma("unroll") for (int h_ = 0; h_ < 2; ++h_) _Pragma("unroll") for (int i_ = 0; i_ < 2; ++i_)
;                 asm volatile("global_load_dword %0, %1, off" : "+v"(graw[h_][i_]) : "v"(S.rowtok + (nxt.pm * BM + h_ * HALF + gR[i_])) : "memory"); } }
;             unsigned gsel[2][2];
;             if constexpr (GATHER) { _Pragma("unroll") for (int h_ = 0; h_ < 2; ++h_) _Pragma("unroll") for (int i_ = 0; i_ < 2; ++i_) { if (last && has_next) gnxt[h_][i_] = graw[h_][i_] * (unsigned)(K * 2) + gC[i_]; gsel[h_][i_] = (last && has_next) ? gnxt[h_][i_] : gcur[h_][i_]; } }
;             if constexpr (SP2) {
;             PG8_LDB(B0, 0, 0); PG8_LDB(B1, 0, 1); PG8_SCHED; PG8_LDA(At, 0, 0); PG8_STAGE_A(PG8_SA(1, 1), a1, 1, gcur);
;             PG8_WAIT_V(8); PG8_WAIT_L(0); PG8_BAR; PG8_MMA(0, 0, At, B0); PG8_MMA(0, 1, At, B1); PG8_BAR; PG8_SCHED;
;             PG8_LDA(At, 0, 1); PG8_STAGE(PG8_SB(0, 0), b2, voffB); PG8_STAGE(PG8_SB(0, 1), b2 + hstep, voffB); PG8_STAGE_A(PG8_SA(0, 0), a2, 0, gsel);
;             PG8_WAIT_V(8); PG8_WAIT_L(0); PG8_BAR; PG8_MMA(1, 0, At, B0); PG8_MMA(1, 1, At, B1); PG8_BAR; PG8_SCHED;
.LBB0_878:
	s_add_u32 s52, s8, s48
	s_addc_u32 s53, s9, s49
	s_add_u32 s54, s52, 0x19200100
	s_addc_u32 s55, s53, 0
	s_and_b64 s[52:53], s[56:57], exec
	s_cselect_b32 s55, s11, s55
	s_cselect_b32 s54, s10, s54
	s_add_u32 s86, s22, s48
	s_addc_u32 s87, s84, s49
	s_and_b64 s[52:53], s[56:57], exec
	s_cselect_b32 s53, s45, s87
	s_cselect_b32 s52, s44, s86
	v_lshl_add_u32 v2, v213, 10, v1
	s_and_b64 vcc, s[46:47], s[56:57]
	v_cndmask_b32_e32 v209, v209, v2, vcc
	v_cndmask_b32_e32 v170, v217, v2, vcc
	v_lshl_add_u32 v2, v214, 10, v204
	v_cndmask_b32_e32 v210, v210, v2, vcc
	v_cndmask_b32_e32 v200, v180, v2, vcc
	v_add_u32_e32 v2, s76, v206
	v_add_u32_e32 v14, s77, v206
	ds_read_b128 v[18:21], v2
	ds_read_b128 v[22:25], v2 offset:1024
	ds_read_b128 v[26:29], v2 offset:2048
	ds_read_b128 v[30:33], v2 offset:3072
	ds_read_b128 v[2:5], v14
	ds_read_b128 v[6:9], v14 offset:1024
	ds_read_b128 v[10:13], v14 offset:2048
	ds_read_b128 v[14:17], v14 offset:3072
	v_lshl_add_u32 v177, v215, 10, v1
	v_lshl_add_u32 v179, v216, 10, v204
	v_cndmask_b32_e32 v211, v211, v177, vcc
	v_cndmask_b32_e32 v212, v212, v179, vcc
	v_cndmask_b32_e32 v177, v178, v177, vcc
	v_cndmask_b32_e32 v179, v176, v179, vcc
	v_lshl_add_u64 v[196:197], v[194:195], 0, s[48:49]
	s_add_i32 m0, s63, 0xc000
	ds_read_b128 v[218:221], v207
	ds_read_b128 v[222:225], v207 offset:1024
	ds_read_b128 v[226:229], v207 offset:2048
	ds_read_b128 v[230:233], v207 offset:3072
	ds_read_b128 v[234:237], v207 offset:4096
	ds_read_b128 v[238:241], v207 offset:5120
	ds_read_b128 v[242:245], v207 offset:6144
	ds_read_b128 v[246:249], v207 offset:7168
	global_load_lds_dwordx4 v[196:197], off
	v_lshl_add_u64 v[196:197], v[192:193], 0, s[48:49]
	s_add_i32 m0, s63, 0xe000
	s_nop 0
	global_load_lds_dwordx4 v[196:197], off
	s_waitcnt vmcnt(8)
	s_waitcnt lgkmcnt(0)
	s_barrier
	s_setprio 1
	s_waitcnt lgkmcnt(0)
	v_mfma_f32_16x16x128_f8f6f4 v[158:161], v[18:25], v[218:225], v[158:161]
	v_mfma_f32_16x16x128_f8f6f4 v[150:153], v[26:33], v[218:225], v[150:153]
	v_mfma_f32_16x16x128_f8f6f4 v[142:145], v[18:25], v[226:233], v[142:145]
	v_mfma_f32_16x16x128_f8f6f4 v[134:137], v[26:33], v[226:233], v[134:137]
	v_mfma_f32_16x16x128_f8f6f4 v[126:129], v[18:25], v[234:241], v[126:129]
	v_mfma_f32_16x16x128_f8f6f4 v[118:121], v[26:33], v[234:241], v[118:121]
	v_mfma_f32_16x16x128_f8f6f4 v[110:113], v[18:25], v[242:249], v[110:113]
	v_mfma_f32_16x16x128_f8f6f4 v[102:105], v[26:33], v[242:249], v[102:105]
	s_setprio 0
	s_setprio 1
	v_mfma_f32_16x16x128_f8f6f4 v[154:157], v[2:9], v[218:225], v[154:157]
	v_mfma_f32_16x16x128_f8f6f4 v[146:149], v[10:17], v[218:225], v[146:149]
	v_mfma_f32_16x16x128_f8f6f4 v[138:141], v[2:9], v[226:233], v[138:141]
	v_mfma_f32_16x16x128_f8f6f4 v[130:133], v[10:17], v[226:233], v[130:133]
	v_mfma_f32_16x16x128_f8f6f4 v[122:125], v[2:9], v[234:241], v[122:125]
	v_mfma_f32_16x16x128_f8f6f4 v[114:117], v[10:17], v[234:241], v[114:117]
	v_mfma_f32_16x16x128_f8f6f4 v[106:109], v[2:9], v[242:249], v[106:109]
	v_mfma_f32_16x16x128_f8f6f4 v[98:101], v[10:17], v[242:249], v[98:101]
	s_setprio 0
	s_barrier
	s_add_i32 s56, s76, s60
	v_lshl_add_u64 v[196:197], s[52:53], 0, v[168:169]
	s_mov_b32 m0, s56
	ds_read_b128 v[218:221], v207 offset:16384
	ds_read_b128 v[222:225], v207 offset:17408
	ds_read_b128 v[226:229], v207 offset:18432
	ds_read_b128 v[230:233], v207 offset:19456
	ds_read_b128 v[234:237], v207 offset:20480
	ds_read_b128 v[238:241], v207 offset:21504
	ds_read_b128 v[242:245], v207 offset:22528
	ds_read_b128 v[246:249], v207 offset:23552
	global_load_lds_dwordx4 v[196:197], off
	s_add_i32 m0, s56, 0x2000
	s_add_u32 s56, s52, 0x20000
	v_lshl_add_u64 v[198:199], s[52:53], 0, v[166:167]
	s_addc_u32 s57, s53, 0
	s_add_i32 s86, s77, s60
	global_load_lds_dwordx4 v[198:199], off
	v_lshl_add_u64 v[202:203], s[56:57], 0, v[168:169]
	s_mov_b32 m0, s86
	v_mov_b32_e32 v201, v171
	global_load_lds_dwordx4 v[202:203], off
	v_lshl_add_u64 v[202:203], s[56:57], 0, v[166:167]
	s_add_i32 m0, s86, 0x2000
	s_nop 0
	global_load_lds_dwordx4 v[202:203], off
	s_mov_b32 m0, s63
	v_lshl_add_u64 v[202:203], s[54:55], 0, v[170:171]
	global_load_lds_dwordx4 v170, s[54:55]
	s_mov_b32 m0, s65
	s_nop 0
	global_load_lds_dwordx4 v200, s[54:55]
	s_waitcnt vmcnt(8)
	s_waitcnt lgkmcnt(0)
	v_lshl_add_u64 v[200:201], s[54:55], 0, v[200:201]
	s_barrier
	s_setprio 1
	s_waitcnt lgkmcnt(0)
	v_mfma_f32_16x16x128_f8f6f4 v[94:97], v[18:25], v[218:225], v[94:97]
	v_mfma_f32_16x16x128_f8f6f4 v[86:89], v[26:33], v[218:225], v[86:89]
	v_mfma_f32_16x16x128_f8f6f4 v[78:81], v[18:25], v[226:233], v[78:81]
	v_mfma_f32_16x16x128_f8f6f4 v[70:73], v[26:33], v[226:233], v[70:73]
	v_mfma_f32_16x16x128_f8f6f4 v[62:65], v[18:25], v[234:241], v[62:65]
	v_mfma_f32_16x16x128_f8f6f4 v[54:57], v[26:33], v[234:241], v[54:57]
	v_mfma_f32_16x16x128_f8f6f4 v[46:49], v[18:25], v[242:249], v[46:49]
	v_mfma_f32_16x16x128_f8f6f4 v[38:41], v[26:33], v[242:249], v[38:41]
	s_setprio 0
	s_setprio 1
	v_mfma_f32_16x16x128_f8f6f4 v[90:93], v[2:9], v[218:225], v[90:93]
	v_mfma_f32_16x16x128_f8f6f4 v[82:85], v[10:17], v[218:225], v[82:85]
	v_mfma_f32_16x16x128_f8f6f4 v[74:77], v[2:9], v[226:233], v[74:77]
	v_mfma_f32_16x16x128_f8f6f4 v[66:69], v[10:17], v[226:233], v[66:69]
	v_mfma_f32_16x16x128_f8f6f4 v[58:61], v[2:9], v[234:241], v[58:61]
	v_mfma_f32_16x16x128_f8f6f4 v[50:53], v[10:17], v[234:241], v[50:53]
	v_mfma_f32_16x16x128_f8f6f4 v[42:45], v[2:9], v[242:249], v[42:45]
	v_mfma_f32_16x16x128_f8f6f4 v[34:37], v[10:17], v[242:249], v[34:37]
	s_setprio 0
	s_barrier
; #define PG8_STAGE(bufoff, gbase, voff) do { _Pragma("unroll") for (int _i = 0; _i < 2; ++_i) \
;         __builtin_amdgcn_global_load_lds((const unsigned*)((const char*)(gbase) + (voff)[_i]), (PG8_LAS unsigned*)(lds + (bufoff) + ldsw + _i * 8192), 16, 0, 0); } while (0)
; #define PG8_STAGE_A(bufoff, kbase, h, gv) do { if constexpr (GATHER) { PG8_STAGE(bufoff, kbase, (gv)[h]); } else { PG8_STAGE(bufoff, (kbase) + (h) * hstep, voffA); } } while (0)
; #define PG8_WAIT_V(n) asm volatile("s_waitcnt vmcnt(" #n ")" ::: "memory")
; #define PG8_WAIT_L(n) asm volatile("s_waitcnt lgkmcnt(" #n ")" ::: "memory")
; #define PG8_BAR __builtin_amdgcn_s_barrier()
; #define PG8_SCHED __builtin_amdgcn_sched_barrier(0)
; template <class Epi, class Sched, bool ALIGN_EPI = false, bool SP2 = false, bool FP8 = false, bool GATHER = false>
; __device__ __forceinline__ void gemm_phase(PG8_LAS unsigned char* lds, const Gemm g, const Sched& S, const Epi& E) {
;     ...
;             PG8_LDB(B0, 1, 0); PG8_LDB(B1, 1, 1); PG8_SCHED; PG8_LDA(At, 1, 0); PG8_STAGE_A(PG8_SA(0, 1), a2, 1, gsel);
;             PG8_WAIT_V(8); PG8_WAIT_L(0); PG8_BAR; PG8_MMA(0, 0, At, B0); PG8_MMA(0, 1, At, B1); PG8_BAR; PG8_SCHED;
;             PG8_LDA(At, 1, 1); PG8_STAGE(PG8_SB(1, 0), b3, voffB); PG8_STAGE(PG8_SB(1, 1), b3 + hstep, voffB); PG8_STAGE_A(PG8_SA(1, 0), a3, 0, gsel);
;             PG8_WAIT_V(8); PG8_WAIT_L(0); PG8_BAR; PG8_MMA(1, 0, At, B0); PG8_MMA(1, 1, At, B1); PG8_BAR; PG8_SCHED;
;     __device__ __forceinline__ void pre(const pg8::Unit& u, int wid, int lane) const {
;         if (wid == 0) lds_dma16(bias + (size_t)(u.pn >> 8) * 2048 + (lane >> 5) * 1024 + (u.pn & 255) * 128 + (lane & 31) * 4, (unsigned)(uintptr_t)(lds + LDS_EPI)); }
	s_add_i32 s56, 0, 0x18000
	s_add_i32 s57, 0, 0x1c000
	v_add_u32_e32 v14, s56, v206
	v_add_u32_e32 v30, s57, v206
	ds_read_b128 v[2:5], v14
	ds_read_b128 v[6:9], v14 offset:1024
	ds_read_b128 v[10:13], v14 offset:2048
	ds_read_b128 v[14:17], v14 offset:3072
	ds_read_b128 v[18:21], v30
	ds_read_b128 v[22:25], v30 offset:1024
	ds_read_b128 v[26:29], v30 offset:2048
	ds_read_b128 v[30:33], v30 offset:3072
	s_mov_b32 m0, s66
	ds_read_b128 v[218:221], v207 offset:32768
	ds_read_b128 v[222:225], v207 offset:33792
	ds_read_b128 v[226:229], v207 offset:34816
	ds_read_b128 v[230:233], v207 offset:35840
	ds_read_b128 v[234:237], v207 offset:36864
	ds_read_b128 v[238:241], v207 offset:37888
	ds_read_b128 v[242:245], v207 offset:38912
	ds_read_b128 v[246:249], v207 offset:39936
	global_load_lds_dwordx4 v177, s[54:55]
	s_mov_b32 m0, s67
	s_nop 0
	global_load_lds_dwordx4 v179, s[54:55]
	s_waitcnt vmcnt(8)
	s_waitcnt lgkmcnt(0)
	s_barrier
	s_setprio 1
	s_waitcnt lgkmcnt(0)
	v_mfma_f32_16x16x128_f8f6f4 v[158:161], v[2:9], v[218:225], v[158:161]
	v_mfma_f32_16x16x128_f8f6f4 v[150:153], v[10:17], v[218:225], v[150:153]
	v_mfma_f32_16x16x128_f8f6f4 v[142:145], v[2:9], v[226:233], v[142:145]
	v_mfma_f32_16x16x128_f8f6f4 v[134:137], v[10:17], v[226:233], v[134:137]
	v_mfma_f32_16x16x128_f8f6f4 v[126:129], v[2:9], v[234:241], v[126:129]
	v_mfma_f32_16x16x128_f8f6f4 v[118:121], v[10:17], v[234:241], v[118:121]
	v_mfma_f32_16x16x128_f8f6f4 v[110:113], v[2:9], v[242:249], v[110:113]
	v_mfma_f32_16x16x128_f8f6f4 v[102:105], v[10:17], v[242:249], v[102:105]
	s_setprio 0
	s_setprio 1
	v_mfma_f32_16x16x128_f8f6f4 v[154:157], v[18:25], v[218:225], v[154:157]
	v_mfma_f32_16x16x128_f8f6f4 v[146:149], v[26:33], v[218:225], v[146:149]
	v_mfma_f32_16x16x128_f8f6f4 v[138:141], v[18:25], v[226:233], v[138:141]
	v_mfma_f32_16x16x128_f8f6f4 v[130:133], v[26:33], v[226:233], v[130:133]
	v_mfma_f32_16x16x128_f8f6f4 v[122:125], v[18:25], v[234:241], v[122:125]
	v_mfma_f32_16x16x128_f8f6f4 v[114:117], v[26:33], v[234:241], v[114:117]
	v_mfma_f32_16x16x128_f8f6f4 v[106:109], v[18:25], v[242:249], v[106:109]
	v_mfma_f32_16x16x128_f8f6f4 v[98:101], v[26:33], v[242:249], v[98:101]
	s_setprio 0
	s_barrier
	s_add_i32 s54, s56, s60
	v_lshl_add_u64 v[196:197], v[196:197], 0, s[18:19]
	s_mov_b32 m0, s54
	ds_read_b128 v[218:221], v207 offset:49152
	ds_read_b128 v[222:225], v207 offset:50176
	ds_read_b128 v[226:229], v207 offset:51200
	ds_read_b128 v[230:233], v207 offset:52224
	ds_read_b128 v[234:237], v207 offset:53248
	ds_read_b128 v[238:241], v207 offset:54272
	ds_read_b128 v[242:245], v207 offset:55296
	ds_read_b128 v[246:249], v207 offset:56320
	global_load_lds_dwordx4 v[196:197], off
	s_add_i32 m0, s54, 0x2000
	s_add_u32 s52, s52, 0x20080
	v_lshl_add_u64 v[196:197], v[198:199], 0, s[18:19]
	s_addc_u32 s53, s53, 0
	s_add_i32 s54, s57, s60
	global_load_lds_dwordx4 v[196:197], off
	v_lshl_add_u64 v[196:197], s[52:53], 0, v[168:169]
	s_mov_b32 m0, s54
	s_nop 0
	global_load_lds_dwordx4 v[196:197], off
	v_lshl_add_u64 v[196:197], s[52:53], 0, v[166:167]
	s_add_i32 m0, s54, 0x2000
	s_nop 0
	global_load_lds_dwordx4 v[196:197], off
	v_lshl_add_u64 v[196:197], v[202:203], 0, s[18:19]
	s_mov_b32 m0, s70
	s_nop 0
	global_load_lds_dwordx4 v[196:197], off
	v_lshl_add_u64 v[196:197], v[200:201], 0, s[18:19]
	s_mov_b32 m0, s71
	s_nop 0
	global_load_lds_dwordx4 v[196:197], off
	s_waitcnt vmcnt(8)
	s_waitcnt lgkmcnt(0)
	s_barrier
	s_setprio 1
	s_waitcnt lgkmcnt(0)
	v_mfma_f32_16x16x128_f8f6f4 v[94:97], v[2:9], v[218:225], v[94:97]
	v_mfma_f32_16x16x128_f8f6f4 v[86:89], v[10:17], v[218:225], v[86:89]
	v_mfma_f32_16x16x128_f8f6f4 v[78:81], v[2:9], v[226:233], v[78:81]
	v_mfma_f32_16x16x128_f8f6f4 v[70:73], v[10:17], v[226:233], v[70:73]
	v_mfma_f32_16x16x128_f8f6f4 v[62:65], v[2:9], v[234:241], v[62:65]
	v_mfma_f32_16x16x128_f8f6f4 v[54:57], v[10:17], v[234:241], v[54:57]
	v_mfma_f32_16x16x128_f8f6f4 v[46:49], v[2:9], v[242:249], v[46:49]
	v_mfma_f32_16x16x128_f8f6f4 v[38:41], v[10:17], v[242:249], v[38:41]
	s_setprio 0
	s_setprio 1
	v_mfma_f32_16x16x128_f8f6f4 v[90:93], v[18:25], v[218:225], v[90:93]
	v_mfma_f32_16x16x128_f8f6f4 v[82:85], v[26:33], v[218:225], v[82:85]
	v_mfma_f32_16x16x128_f8f6f4 v[74:77], v[18:25], v[226:233], v[74:77]
	v_mfma_f32_16x16x128_f8f6f4 v[66:69], v[26:33], v[226:233], v[66:69]
	v_mfma_f32_16x16x128_f8f6f4 v[58:61], v[18:25], v[234:241], v[58:61]
	v_mfma_f32_16x16x128_f8f6f4 v[50:53], v[26:33], v[234:241], v[50:53]
	v_mfma_f32_16x16x128_f8f6f4 v[42:45], v[18:25], v[242:249], v[42:45]
	v_mfma_f32_16x16x128_f8f6f4 v[34:37], v[26:33], v[242:249], v[34:37]
	s_setprio 0
	s_add_i32 s85, s85, 2
	s_add_u32 s48, s48, 0x100
	s_addc_u32 s49, s49, 0
	s_cmp_gt_u32 s85, 5
	s_cbranch_scc1 .Lrot878_exit
	s_cmpk_eq_i32 s48, 0x300
	s_cselect_b64 s[56:57], -1, 0
	s_and_b64 s[52:53], s[56:57], s[24:25]
	s_andn2_b64 vcc, exec, s[52:53]
	s_cbranch_vccz .Lrot878_rare1
	s_cmpk_lg_i32 s48, 0x200
	s_cselect_b64 s[52:53], -1, 0
	s_or_b64 s[52:53], s[50:51], s[52:53]
	s_and_b64 vcc, exec, s[52:53]
	s_cbranch_vccnz .Lrot878_head
.Lrot878_rare1:
	s_barrier
.LBB0_879:
	s_cmpk_eq_i32 s48, 0x300
	s_cselect_b64 s[56:57], -1, 0
	s_and_b64 s[52:53], s[56:57], s[24:25]
	s_andn2_b64 vcc, exec, s[52:53]
	s_cbranch_vccnz .LBB0_881
	s_add_i32 s52, 0, 0x20000
	s_mov_b32 s53, m0
	s_mov_b32 m0, s52
	s_nop 0
	global_load_lds_dwordx4 v[182:183], off
	s_mov_b32 m0, s53

; #define PG8_STAGE(bufoff, gbase, voff) do { _Pragma("unroll") for (int _i = 0; _i < 2; ++_i) \
;         __builtin_amdgcn_global_load_lds((const unsigned*)((const char*)(gbase) + (voff)[_i]), (PG8_LAS unsigned*)(lds + (bufoff) + ldsw + _i * 8192), 16, 0, 0); } while (0)
; #define PG8_STAGE_A(bufoff, kbase, h, gv) do { if constexpr (GATHER) { PG8_STAGE(bufoff, kbase, (gv)[h]); } else { PG8_STAGE(bufoff, (kbase) + (h) * hstep, voffA); } } while (0)
; #define PG8_WAIT_V(n) asm volatile("s_waitcnt vmcnt(" #n ")" ::: "memory")
; #define PG8_WAIT_L(n) asm volatile("s_waitcnt lgkmcnt(" #n ")" ::: "memory")
; template <class Epi, class Sched, bool ALIGN_EPI = false, bool SP2 = false, bool FP8 = false, bool GATHER = false>
; __device__ __forceinline__ void gemm_phase(PG8_LAS unsigned char* lds, const Gemm g, const Sched& S, const Epi& E) {
;     ...
;             const char* a1 = cA + (size_t)(t + 1) * kstep;
;             const char* a2 = last ? nA : cA + (size_t)(t + 2) * kstep; const char* b2 = last ? nB : cB + (size_t)(t + 2) * kstep;
;             const char* a3 = a2 + kstep; const char* b3 = b2 + kstep;
;             if (last && has_next) S.a_ready(nxt);
;             if (last) E.pre(cur, wid, lane);
;             if constexpr (GATHER) { if (t == nt - 4 && has_next) { _Pragma("unroll") for (int h_ = 0; h_ < 2; ++h_) _Pragma("unroll") for (int i_ = 0; i_ < 2; ++i_)
;                 asm volatile("global_load_dword %0, %1, off" : "+v"(graw[h_][i_]) : "v"(S.rowtok + (nxt.pm * BM + h_ * HALF + gR[i_])) : "memory"); } }
;             unsigned gsel[2][2];
;             if constexpr (GATHER) { _Pragma("unroll") for (int h_ = 0; h_ < 2; ++h_) _Pragma("unroll") for (int i_ = 0; i_ < 2; ++i_) { if (last && has_next) gnxt[h_][i_] = graw[h_][i_] * (unsigned)(K * 2) + gC[i_]; gsel[h_][i_] = (last && has_next) ? gnxt[h_][i_] : gcur[h_][i_]; } }
;             if constexpr (SP2) {
;             PG8_LDB(B0, 0, 0); PG8_LDB(B1, 0, 1); PG8_SCHED; PG8_LDA(At, 0, 0); PG8_STAGE_A(PG8_SA(1, 1), a1, 1, gcur);
;             PG8_WAIT_V(8); PG8_WAIT_L(0); PG8_BAR; PG8_MMA(0, 0, At, B0); PG8_MMA(0, 1, At, B1); PG8_BAR; PG8_SCHED;
;             PG8_LDA(At, 0, 1); PG8_STAGE(PG8_SB(0, 0), b2, voffB); PG8_STAGE(PG8_SB(0, 1), b2 + hstep, voffB); PG8_STAGE_A(PG8_SA(0, 0), a2, 0, gsel);
;             PG8_WAIT_V(8); PG8_WAIT_L(0); PG8_BAR; PG8_MMA(1, 0, At, B0); PG8_MMA(1, 1, At, B1); PG8_BAR; PG8_SCHED;
.Lpeel953_body:
	v_add_u32_e32 v2, s76, v191
	v_add_u32_e32 v14, s77, v191
	ds_read_b128 v[18:21], v2
	ds_read_b128 v[22:25], v2 offset:1024
	ds_read_b128 v[26:29], v2 offset:2048
	ds_read_b128 v[30:33], v2 offset:3072
	ds_read_b128 v[2:5], v14
	ds_read_b128 v[6:9], v14 offset:1024
	ds_read_b128 v[10:13], v14 offset:2048
	ds_read_b128 v[14:17], v14 offset:3072
	s_add_u32 s52, s48, 0xfffe0080
	s_addc_u32 s53, s49, -1
	s_and_b64 s[50:51], s[50:51], exec
	s_cselect_b32 s53, s80, s53
	s_cselect_b32 s52, s81, s52
	s_cselect_b32 s51, s29, s82
	s_cselect_b32 s50, s28, s47
	v_lshl_add_u64 v[218:219], s[48:49], 0, v[172:173]
	s_add_i32 m0, s62, 0xc000
	ds_read_b128 v[182:185], v192
	ds_read_b128 v[186:189], v192 offset:1024
	ds_read_b128 v[194:197], v192 offset:2048
	ds_read_b128 v[198:201], v192 offset:3072
	ds_read_b128 v[202:205], v192 offset:4096
	ds_read_b128 v[206:209], v192 offset:5120
	ds_read_b128 v[210:213], v192 offset:6144
	ds_read_b128 v[214:217], v192 offset:7168
	global_load_lds_dwordx4 v[218:219], off
	v_lshl_add_u64 v[218:219], s[48:49], 0, v[174:175]
	s_add_i32 m0, s62, 0xe000
	s_nop 0
	global_load_lds_dwordx4 v[218:219], off
	s_waitcnt vmcnt(8)
	s_waitcnt lgkmcnt(0)
	s_barrier
	s_setprio 1
	s_waitcnt lgkmcnt(0)
	v_mfma_f32_16x16x128_f8f6f4 v[158:161], v[18:25], v[182:189], 0
	v_mfma_f32_16x16x128_f8f6f4 v[154:157], v[26:33], v[182:189], 0
	v_mfma_f32_16x16x128_f8f6f4 v[150:153], v[18:25], v[194:201], 0
	v_mfma_f32_16x16x128_f8f6f4 v[146:149], v[26:33], v[194:201], 0
	v_mfma_f32_16x16x128_f8f6f4 v[130:133], v[18:25], v[202:209], 0
	v_mfma_f32_16x16x128_f8f6f4 v[122:125], v[26:33], v[202:209], 0
	v_mfma_f32_16x16x128_f8f6f4 v[118:121], v[18:25], v[210:217], 0
	v_mfma_f32_16x16x128_f8f6f4 v[114:117], v[26:33], v[210:217], 0
	s_setprio 0
	s_setprio 1
	v_mfma_f32_16x16x128_f8f6f4 v[142:145], v[2:9], v[182:189], 0
	v_mfma_f32_16x16x128_f8f6f4 v[138:141], v[10:17], v[182:189], 0
	v_mfma_f32_16x16x128_f8f6f4 v[134:137], v[2:9], v[194:201], 0
	v_mfma_f32_16x16x128_f8f6f4 v[126:129], v[10:17], v[194:201], 0
	v_mfma_f32_16x16x128_f8f6f4 v[110:113], v[2:9], v[202:209], 0
	v_mfma_f32_16x16x128_f8f6f4 v[106:109], v[10:17], v[202:209], 0
	v_mfma_f32_16x16x128_f8f6f4 v[102:105], v[2:9], v[210:217], 0
	v_mfma_f32_16x16x128_f8f6f4 v[98:101], v[10:17], v[210:217], 0
	s_setprio 0
	s_barrier
	s_add_i32 s84, s76, s60
	v_lshl_add_u64 v[182:183], s[50:51], 0, v[166:167]
	s_mov_b32 m0, s84
	ds_read_b128 v[194:197], v192 offset:16384
	ds_read_b128 v[198:201], v192 offset:17408
	ds_read_b128 v[202:205], v192 offset:18432
	ds_read_b128 v[206:209], v192 offset:19456
	ds_read_b128 v[210:213], v192 offset:20480
	ds_read_b128 v[214:217], v192 offset:21504
	ds_read_b128 v[218:221], v192 offset:22528
	ds_read_b128 v[222:225], v192 offset:23552
	global_load_lds_dwordx4 v[182:183], off
	s_add_i32 m0, s84, 0x2000
	s_add_u32 s84, s50, 0x20000
	v_lshl_add_u64 v[184:185], s[50:51], 0, v[162:163]
	s_addc_u32 s85, s51, 0
	s_add_i32 s86, s77, s60
	global_load_lds_dwordx4 v[184:185], off
	v_lshl_add_u64 v[186:187], s[84:85], 0, v[166:167]
	s_mov_b32 m0, s86
	v_lshl_add_u64 v[188:189], s[52:53], 0, v[164:165]
	global_load_lds_dwordx4 v[186:187], off
	v_lshl_add_u64 v[186:187], s[84:85], 0, v[162:163]
	s_add_i32 m0, s86, 0x2000
	s_nop 0
	global_load_lds_dwordx4 v[186:187], off
	v_lshl_add_u64 v[186:187], s[52:53], 0, v[168:169]
	s_mov_b32 m0, s62
	s_nop 0
	global_load_lds_dwordx4 v[186:187], off
	s_mov_b32 m0, s63
	s_nop 0
	global_load_lds_dwordx4 v[188:189], off
	s_waitcnt vmcnt(8)
	s_waitcnt lgkmcnt(0)
	s_barrier
	s_setprio 1
	s_waitcnt lgkmcnt(0)
	v_mfma_f32_16x16x128_f8f6f4 v[94:97], v[18:25], v[194:201], 0
	v_mfma_f32_16x16x128_f8f6f4 v[90:93], v[26:33], v[194:201], 0
	v_mfma_f32_16x16x128_f8f6f4 v[86:89], v[18:25], v[202:209], 0
	v_mfma_f32_16x16x128_f8f6f4 v[82:85], v[26:33], v[202:209], 0
	v_mfma_f32_16x16x128_f8f6f4 v[66:69], v[18:25], v[210:217], 0
	v_mfma_f32_16x16x128_f8f6f4 v[58:61], v[26:33], v[210:217], 0
	v_mfma_f32_16x16x128_f8f6f4 v[54:57], v[18:25], v[218:225], 0
	v_mfma_f32_16x16x128_f8f6f4 v[50:53], v[26:33], v[218:225], 0
	s_setprio 0
	s_setprio 1
	v_mfma_f32_16x16x128_f8f6f4 v[78:81], v[2:9], v[194:201], 0
	v_mfma_f32_16x16x128_f8f6f4 v[74:77], v[10:17], v[194:201], 0
	v_mfma_f32_16x16x128_f8f6f4 v[70:73], v[2:9], v[202:209], 0
	v_mfma_f32_16x16x128_f8f6f4 v[62:65], v[10:17], v[202:209], 0
	v_mfma_f32_16x16x128_f8f6f4 v[46:49], v[2:9], v[210:217], 0
	v_mfma_f32_16x16x128_f8f6f4 v[42:45], v[10:17], v[210:217], 0
	v_mfma_f32_16x16x128_f8f6f4 v[38:41], v[2:9], v[218:225], 0
	v_mfma_f32_16x16x128_f8f6f4 v[34:37], v[10:17], v[218:225], 0
	s_setprio 0
	s_barrier
; #define PG8_STAGE(bufoff, gbase, voff) do { _Pragma("unroll") for (int _i = 0; _i < 2; ++_i) \
;         __builtin_amdgcn_global_load_lds((const unsigned*)((const char*)(gbase) + (voff)[_i]), (PG8_LAS unsigned*)(lds + (bufoff) + ldsw + _i * 8192), 16, 0, 0); } while (0)
; #define PG8_STAGE_A(bufoff, kbase, h, gv) do { if constexpr (GATHER) { PG8_STAGE(bufoff, kbase, (gv)[h]); } else { PG8_STAGE(bufoff, (kbase) + (h) * hstep, voffA); } } while (0)
; #define PG8_WAIT_V(n) asm volatile("s_waitcnt vmcnt(" #n ")" ::: "memory")
; #define PG8_WAIT_L(n) asm volatile("s_waitcnt lgkmcnt(" #n ")" ::: "memory")
; #define PG8_BAR __builtin_amdgcn_s_barrier()
; #define PG8_SCHED __builtin_amdgcn_sched_barrier(0)
; template <class Epi, class Sched, bool ALIGN_EPI = false, bool SP2 = false, bool FP8 = false, bool GATHER = false>
; __device__ __forceinline__ void gemm_phase(PG8_LAS unsigned char* lds, const Gemm g, const Sched& S, const Epi& E) {
;     ...
;         for (int t = 0; t < nt; t += 2) {
;             const bool last = (t == nt - 2);
;             const char* a1 = cA + (size_t)(t + 1) * kstep;
;             const char* a2 = last ? nA : cA + (size_t)(t + 2) * kstep; const char* b2 = last ? nB : cB + (size_t)(t + 2) * kstep;
;             const char* a3 = a2 + kstep; const char* b3 = b2 + kstep;
;     ...
;             PG8_LDB(B0, 1, 0); PG8_LDB(B1, 1, 1); PG8_SCHED; PG8_LDA(At, 1, 0); PG8_STAGE_A(PG8_SA(0, 1), a2, 1, gsel);
;             PG8_WAIT_V(8); PG8_WAIT_L(0); PG8_BAR; PG8_MMA(0, 0, At, B0); PG8_MMA(0, 1, At, B1); PG8_BAR; PG8_SCHED;
;             PG8_LDA(At, 1, 1); PG8_STAGE(PG8_SB(1, 0), b3, voffB); PG8_STAGE(PG8_SB(1, 1), b3 + hstep, voffB); PG8_STAGE_A(PG8_SA(1, 0), a3, 0, gsel);
;             PG8_WAIT_V(8); PG8_WAIT_L(0); PG8_BAR; PG8_MMA(1, 0, At, B0); PG8_MMA(1, 1, At, B1); PG8_BAR; PG8_SCHED;
	s_add_i32 s84, 0, 0x18000
	s_add_i32 s85, 0, 0x1c000
	v_add_u32_e32 v14, s84, v191
	v_add_u32_e32 v30, s85, v191
	ds_read_b128 v[2:5], v14
	ds_read_b128 v[6:9], v14 offset:1024
	ds_read_b128 v[10:13], v14 offset:2048
	ds_read_b128 v[14:17], v14 offset:3072
	ds_read_b128 v[18:21], v30
	ds_read_b128 v[22:25], v30 offset:1024
	ds_read_b128 v[26:29], v30 offset:2048
	ds_read_b128 v[30:33], v30 offset:3072
	s_add_u32 s52, s52, 0x20000
	s_addc_u32 s53, s53, 0
	s_mov_b32 m0, s65
	v_lshl_add_u64 v[226:227], s[52:53], 0, v[168:169]
	ds_read_b128 v[194:197], v192 offset:32768
	ds_read_b128 v[198:201], v192 offset:33792
	ds_read_b128 v[202:205], v192 offset:34816
	ds_read_b128 v[206:209], v192 offset:35840
	ds_read_b128 v[210:213], v192 offset:36864
	ds_read_b128 v[214:217], v192 offset:37888
	ds_read_b128 v[218:221], v192 offset:38912
	ds_read_b128 v[222:225], v192 offset:39936
	global_load_lds_dwordx4 v[226:227], off
	v_lshl_add_u64 v[226:227], s[52:53], 0, v[164:165]
	s_mov_b32 m0, s66
	s_nop 0
	global_load_lds_dwordx4 v[226:227], off
	s_waitcnt vmcnt(8)
	s_waitcnt lgkmcnt(0)
	s_barrier
	s_setprio 1
	s_waitcnt lgkmcnt(0)
	v_mfma_f32_16x16x128_f8f6f4 v[158:161], v[2:9], v[194:201], v[158:161]
	v_mfma_f32_16x16x128_f8f6f4 v[154:157], v[10:17], v[194:201], v[154:157]
	v_mfma_f32_16x16x128_f8f6f4 v[150:153], v[2:9], v[202:209], v[150:153]
	v_mfma_f32_16x16x128_f8f6f4 v[146:149], v[10:17], v[202:209], v[146:149]
	v_mfma_f32_16x16x128_f8f6f4 v[130:133], v[2:9], v[210:217], v[130:133]
	v_mfma_f32_16x16x128_f8f6f4 v[122:125], v[10:17], v[210:217], v[122:125]
	v_mfma_f32_16x16x128_f8f6f4 v[118:121], v[2:9], v[218:225], v[118:121]
	v_mfma_f32_16x16x128_f8f6f4 v[114:117], v[10:17], v[218:225], v[114:117]
	s_setprio 0
	s_setprio 1
	v_mfma_f32_16x16x128_f8f6f4 v[142:145], v[18:25], v[194:201], v[142:145]
	v_mfma_f32_16x16x128_f8f6f4 v[138:141], v[26:33], v[194:201], v[138:141]
	v_mfma_f32_16x16x128_f8f6f4 v[134:137], v[18:25], v[202:209], v[134:137]
	v_mfma_f32_16x16x128_f8f6f4 v[126:129], v[26:33], v[202:209], v[126:129]
	v_mfma_f32_16x16x128_f8f6f4 v[110:113], v[18:25], v[210:217], v[110:113]
	v_mfma_f32_16x16x128_f8f6f4 v[106:109], v[26:33], v[210:217], v[106:109]
	v_mfma_f32_16x16x128_f8f6f4 v[102:105], v[18:25], v[218:225], v[102:105]
	v_mfma_f32_16x16x128_f8f6f4 v[98:101], v[26:33], v[218:225], v[98:101]
	s_setprio 0
	s_barrier
	s_add_i32 s52, s84, s60
	v_lshl_add_u64 v[182:183], v[182:183], 0, s[18:19]
	s_mov_b32 m0, s52
	ds_read_b128 v[194:197], v192 offset:49152
	ds_read_b128 v[198:201], v192 offset:50176
	ds_read_b128 v[202:205], v192 offset:51200
	ds_read_b128 v[206:209], v192 offset:52224
	ds_read_b128 v[210:213], v192 offset:53248
	ds_read_b128 v[214:217], v192 offset:54272
	ds_read_b128 v[218:221], v192 offset:55296
	ds_read_b128 v[222:225], v192 offset:56320
	global_load_lds_dwordx4 v[182:183], off
	s_add_i32 m0, s52, 0x2000
	s_add_u32 s50, s50, 0x20080
	v_lshl_add_u64 v[182:183], v[184:185], 0, s[18:19]
	s_addc_u32 s51, s51, 0
	s_add_i32 s52, s85, s60
	global_load_lds_dwordx4 v[182:183], off
	v_lshl_add_u64 v[182:183], s[50:51], 0, v[166:167]
	s_mov_b32 m0, s52
	s_nop 0
	global_load_lds_dwordx4 v[182:183], off
	v_lshl_add_u64 v[182:183], s[50:51], 0, v[162:163]
	s_add_i32 m0, s52, 0x2000
	s_nop 0
	global_load_lds_dwordx4 v[182:183], off
	v_lshl_add_u64 v[182:183], v[186:187], 0, s[18:19]
	s_mov_b32 m0, s69
	s_nop 0
	global_load_lds_dwordx4 v[182:183], off
	v_lshl_add_u64 v[182:183], v[188:189], 0, s[18:19]
	s_mov_b32 m0, s70
	s_nop 0
	global_load_lds_dwordx4 v[182:183], off
	s_waitcnt vmcnt(8)
	s_waitcnt lgkmcnt(0)
	s_barrier
	s_setprio 1
	s_waitcnt lgkmcnt(0)
	v_mfma_f32_16x16x128_f8f6f4 v[94:97], v[2:9], v[194:201], v[94:97]
	v_mfma_f32_16x16x128_f8f6f4 v[90:93], v[10:17], v[194:201], v[90:93]
	v_mfma_f32_16x16x128_f8f6f4 v[86:89], v[2:9], v[202:209], v[86:89]
	v_mfma_f32_16x16x128_f8f6f4 v[82:85], v[10:17], v[202:209], v[82:85]
	v_mfma_f32_16x16x128_f8f6f4 v[66:69], v[2:9], v[210:217], v[66:69]
	v_mfma_f32_16x16x128_f8f6f4 v[58:61], v[10:17], v[210:217], v[58:61]
	v_mfma_f32_16x16x128_f8f6f4 v[54:57], v[2:9], v[218:225], v[54:57]
	v_mfma_f32_16x16x128_f8f6f4 v[50:53], v[10:17], v[218:225], v[50:53]
	s_setprio 0
	s_setprio 1
	v_mfma_f32_16x16x128_f8f6f4 v[78:81], v[18:25], v[194:201], v[78:81]
	v_mfma_f32_16x16x128_f8f6f4 v[74:77], v[26:33], v[194:201], v[74:77]
	v_mfma_f32_16x16x128_f8f6f4 v[70:73], v[18:25], v[202:209], v[70:73]
	v_mfma_f32_16x16x128_f8f6f4 v[62:65], v[26:33], v[202:209], v[62:65]
	v_mfma_f32_16x16x128_f8f6f4 v[46:49], v[18:25], v[210:217], v[46:49]
	v_mfma_f32_16x16x128_f8f6f4 v[42:45], v[26:33], v[210:217], v[42:45]
	v_mfma_f32_16x16x128_f8f6f4 v[38:41], v[18:25], v[218:225], v[38:41]
	v_mfma_f32_16x16x128_f8f6f4 v[34:37], v[26:33], v[218:225], v[34:37]
	s_setprio 0
	s_add_i32 s83, s83, 2
	s_add_u32 s48, s48, 0x100
	s_addc_u32 s49, s49, 0
	s_add_u32 s47, s47, 0x100
	s_addc_u32 s82, s82, 0
	s_cmp_gt_u32 s83, 5
	s_cbranch_scc1 .Lrot953_exit
	s_cmp_eq_u32 s83, 4
	s_cselect_b64 s[50:51], -1, 0
	s_cmp_lg_u32 s83, 4
	s_cbranch_scc1 .Lrot953_head
	s_barrier
	s_branch .LBB0_954

; #define PG8_STAGE(bufoff, gbase, voff) do { _Pragma("unroll") for (int _i = 0; _i < 2; ++_i) \
;         __builtin_amdgcn_global_load_lds((const unsigned*)((const char*)(gbase) + (voff)[_i]), (PG8_LAS unsigned*)(lds + (bufoff) + ldsw + _i * 8192), 16, 0, 0); } while (0)
; #define PG8_STAGE_A(bufoff, kbase, h, gv) do { if constexpr (GATHER) { PG8_STAGE(bufoff, kbase, (gv)[h]); } else { PG8_STAGE(bufoff, (kbase) + (h) * hstep, voffA); } } while (0)
; #define PG8_WAIT_V(n) asm volatile("s_waitcnt vmcnt(" #n ")" ::: "memory")
; #define PG8_WAIT_L(n) asm volatile("s_waitcnt lgkmcnt(" #n ")" ::: "memory")
; template <class Epi, class Sched, bool ALIGN_EPI = false, bool SP2 = false, bool FP8 = false, bool GATHER = false>
; __device__ __forceinline__ void gemm_phase(PG8_LAS unsigned char* lds, const Gemm g, const Sched& S, const Epi& E) {
;     ...
;             const char* a1 = cA + (size_t)(t + 1) * kstep;
;             const char* a2 = last ? nA : cA + (size_t)(t + 2) * kstep; const char* b2 = last ? nB : cB + (size_t)(t + 2) * kstep;
;             const char* a3 = a2 + kstep; const char* b3 = b2 + kstep;
;             if (last && has_next) S.a_ready(nxt);
;             if (last) E.pre(cur, wid, lane);
;             if constexpr (GATHER) { if (t == nt - 4 && has_next) { _Pragma("unroll") for (int h_ = 0; h_ < 2; ++h_) _Pragma("unroll") for (int i_ = 0; i_ < 2; ++i_)
;                 asm volatile("global_load_dword %0, %1, off" : "+v"(graw[h_][i_]) : "v"(S.rowtok + (nxt.pm * BM + h_ * HALF + gR[i_])) : "memory"); } }
;             unsigned gsel[2][2];
;             if constexpr (GATHER) { _Pragma("unroll") for (int h_ = 0; h_ < 2; ++h_) _Pragma("unroll") for (int i_ = 0; i_ < 2; ++i_) { if (last && has_next) gnxt[h_][i_] = graw[h_][i_] * (unsigned)(K * 2) + gC[i_]; gsel[h_][i_] = (last && has_next) ? gnxt[h_][i_] : gcur[h_][i_]; } }
;             if constexpr (SP2) {
;             PG8_LDB(B0, 0, 0); PG8_LDB(B1, 0, 1); PG8_SCHED; PG8_LDA(At, 0, 0); PG8_STAGE_A(PG8_SA(1, 1), a1, 1, gcur);
;             PG8_WAIT_V(8); PG8_WAIT_L(0); PG8_BAR; PG8_MMA(0, 0, At, B0); PG8_MMA(0, 1, At, B1); PG8_BAR; PG8_SCHED;
;             PG8_LDA(At, 0, 1); PG8_STAGE(PG8_SB(0, 0), b2, voffB); PG8_STAGE(PG8_SB(0, 1), b2 + hstep, voffB); PG8_STAGE_A(PG8_SA(0, 0), a2, 0, gsel);
;             PG8_WAIT_V(8); PG8_WAIT_L(0); PG8_BAR; PG8_MMA(1, 0, At, B0); PG8_MMA(1, 1, At, B1); PG8_BAR; PG8_SCHED;
.LBB0_953:
	v_add_u32_e32 v2, s76, v191
	v_add_u32_e32 v14, s77, v191
	ds_read_b128 v[18:21], v2
	ds_read_b128 v[22:25], v2 offset:1024
	ds_read_b128 v[26:29], v2 offset:2048
	ds_read_b128 v[30:33], v2 offset:3072
	ds_read_b128 v[2:5], v14
	ds_read_b128 v[6:9], v14 offset:1024
	ds_read_b128 v[10:13], v14 offset:2048
	ds_read_b128 v[14:17], v14 offset:3072
	s_add_u32 s52, s48, 0xfffe0080
	s_addc_u32 s53, s49, -1
	s_and_b64 s[50:51], s[50:51], exec
	s_cselect_b32 s53, s80, s53
	s_cselect_b32 s52, s81, s52
	s_cselect_b32 s51, s29, s82
	s_cselect_b32 s50, s28, s47
	v_lshl_add_u64 v[218:219], s[48:49], 0, v[172:173]
	s_add_i32 m0, s62, 0xc000
	ds_read_b128 v[182:185], v192
	ds_read_b128 v[186:189], v192 offset:1024
	ds_read_b128 v[194:197], v192 offset:2048
	ds_read_b128 v[198:201], v192 offset:3072
	ds_read_b128 v[202:205], v192 offset:4096
	ds_read_b128 v[206:209], v192 offset:5120
	ds_read_b128 v[210:213], v192 offset:6144
	ds_read_b128 v[214:217], v192 offset:7168
	global_load_lds_dwordx4 v[218:219], off
	v_lshl_add_u64 v[218:219], s[48:49], 0, v[174:175]
	s_add_i32 m0, s62, 0xe000
	s_nop 0
	global_load_lds_dwordx4 v[218:219], off
	s_waitcnt vmcnt(8)
	s_waitcnt lgkmcnt(0)
	s_barrier
	s_setprio 1
	s_waitcnt lgkmcnt(0)
	v_mfma_f32_16x16x128_f8f6f4 v[158:161], v[18:25], v[182:189], v[158:161]
	v_mfma_f32_16x16x128_f8f6f4 v[154:157], v[26:33], v[182:189], v[154:157]
	v_mfma_f32_16x16x128_f8f6f4 v[150:153], v[18:25], v[194:201], v[150:153]
	v_mfma_f32_16x16x128_f8f6f4 v[146:149], v[26:33], v[194:201], v[146:149]
	v_mfma_f32_16x16x128_f8f6f4 v[130:133], v[18:25], v[202:209], v[130:133]
	v_mfma_f32_16x16x128_f8f6f4 v[122:125], v[26:33], v[202:209], v[122:125]
	v_mfma_f32_16x16x128_f8f6f4 v[118:121], v[18:25], v[210:217], v[118:121]
	v_mfma_f32_16x16x128_f8f6f4 v[114:117], v[26:33], v[210:217], v[114:117]
	s_setprio 0
	s_setprio 1
	v_mfma_f32_16x16x128_f8f6f4 v[142:145], v[2:9], v[182:189], v[142:145]
	v_mfma_f32_16x16x128_f8f6f4 v[138:141], v[10:17], v[182:189], v[138:141]
	v_mfma_f32_16x16x128_f8f6f4 v[134:137], v[2:9], v[194:201], v[134:137]
	v_mfma_f32_16x16x128_f8f6f4 v[126:129], v[10:17], v[194:201], v[126:129]
	v_mfma_f32_16x16x128_f8f6f4 v[110:113], v[2:9], v[202:209], v[110:113]
	v_mfma_f32_16x16x128_f8f6f4 v[106:109], v[10:17], v[202:209], v[106:109]
	v_mfma_f32_16x16x128_f8f6f4 v[102:105], v[2:9], v[210:217], v[102:105]
	v_mfma_f32_16x16x128_f8f6f4 v[98:101], v[10:17], v[210:217], v[98:101]
	s_setprio 0
	s_barrier
	s_add_i32 s84, s76, s60
	v_lshl_add_u64 v[182:183], s[50:51], 0, v[166:167]
	s_mov_b32 m0, s84
	ds_read_b128 v[194:197], v192 offset:16384
	ds_read_b128 v[198:201], v192 offset:17408
	ds_read_b128 v[202:205], v192 offset:18432
	ds_read_b128 v[206:209], v192 offset:19456
	ds_read_b128 v[210:213], v192 offset:20480
	ds_read_b128 v[214:217], v192 offset:21504
	ds_read_b128 v[218:221], v192 offset:22528
	ds_read_b128 v[222:225], v192 offset:23552
	global_load_lds_dwordx4 v[182:183], off
	s_add_i32 m0, s84, 0x2000
	s_add_u32 s84, s50, 0x20000
	v_lshl_add_u64 v[184:185], s[50:51], 0, v[162:163]
	s_addc_u32 s85, s51, 0
	s_add_i32 s86, s77, s60
	global_load_lds_dwordx4 v[184:185], off
	v_lshl_add_u64 v[186:187], s[84:85], 0, v[166:167]
	s_mov_b32 m0, s86
	v_lshl_add_u64 v[188:189], s[52:53], 0, v[164:165]
	global_load_lds_dwordx4 v[186:187], off
	v_lshl_add_u64 v[186:187], s[84:85], 0, v[162:163]
	s_add_i32 m0, s86, 0x2000
	s_nop 0
	global_load_lds_dwordx4 v[186:187], off
	v_lshl_add_u64 v[186:187], s[52:53], 0, v[168:169]
	s_mov_b32 m0, s62
	s_nop 0
	global_load_lds_dwordx4 v[186:187], off
	s_mov_b32 m0, s63
	s_nop 0
	global_load_lds_dwordx4 v[188:189], off
	s_waitcnt vmcnt(8)
	s_waitcnt lgkmcnt(0)
	s_barrier
	s_setprio 1
	s_waitcnt lgkmcnt(0)
	v_mfma_f32_16x16x128_f8f6f4 v[94:97], v[18:25], v[194:201], v[94:97]
	v_mfma_f32_16x16x128_f8f6f4 v[90:93], v[26:33], v[194:201], v[90:93]
	v_mfma_f32_16x16x128_f8f6f4 v[86:89], v[18:25], v[202:209], v[86:89]
	v_mfma_f32_16x16x128_f8f6f4 v[82:85], v[26:33], v[202:209], v[82:85]
	v_mfma_f32_16x16x128_f8f6f4 v[66:69], v[18:25], v[210:217], v[66:69]
	v_mfma_f32_16x16x128_f8f6f4 v[58:61], v[26:33], v[210:217], v[58:61]
	v_mfma_f32_16x16x128_f8f6f4 v[54:57], v[18:25], v[218:225], v[54:57]
	v_mfma_f32_16x16x128_f8f6f4 v[50:53], v[26:33], v[218:225], v[50:53]
	s_setprio 0
	s_setprio 1
	v_mfma_f32_16x16x128_f8f6f4 v[78:81], v[2:9], v[194:201], v[78:81]
	v_mfma_f32_16x16x128_f8f6f4 v[74:77], v[10:17], v[194:201], v[74:77]
	v_mfma_f32_16x16x128_f8f6f4 v[70:73], v[2:9], v[202:209], v[70:73]
	v_mfma_f32_16x16x128_f8f6f4 v[62:65], v[10:17], v[202:209], v[62:65]
	v_mfma_f32_16x16x128_f8f6f4 v[46:49], v[2:9], v[210:217], v[46:49]
	v_mfma_f32_16x16x128_f8f6f4 v[42:45], v[10:17], v[210:217], v[42:45]
	v_mfma_f32_16x16x128_f8f6f4 v[38:41], v[2:9], v[218:225], v[38:41]
	v_mfma_f32_16x16x128_f8f6f4 v[34:37], v[10:17], v[218:225], v[34:37]
	s_setprio 0
	s_barrier
; #define PG8_STAGE(bufoff, gbase, voff) do { _Pragma("unroll") for (int _i = 0; _i < 2; ++_i) \
;         __builtin_amdgcn_global_load_lds((const unsigned*)((const char*)(gbase) + (voff)[_i]), (PG8_LAS unsigned*)(lds + (bufoff) + ldsw + _i * 8192), 16, 0, 0); } while (0)
; #define PG8_STAGE_A(bufoff, kbase, h, gv) do { if constexpr (GATHER) { PG8_STAGE(bufoff, kbase, (gv)[h]); } else { PG8_STAGE(bufoff, (kbase) + (h) * hstep, voffA); } } while (0)
; #define PG8_WAIT_V(n) asm volatile("s_waitcnt vmcnt(" #n ")" ::: "memory")
; #define PG8_WAIT_L(n) asm volatile("s_waitcnt lgkmcnt(" #n ")" ::: "memory")
; #define PG8_BAR __builtin_amdgcn_s_barrier()
; #define PG8_SCHED __builtin_amdgcn_sched_barrier(0)
; template <class Epi, class Sched, bool ALIGN_EPI = false, bool SP2 = false, bool FP8 = false, bool GATHER = false>
; __device__ __forceinline__ void gemm_phase(PG8_LAS unsigned char* lds, const Gemm g, const Sched& S, const Epi& E) {
;     ...
;         for (int t = 0; t < nt; t += 2) {
;             const bool last = (t == nt - 2);
;             const char* a1 = cA + (size_t)(t + 1) * kstep;
;             const char* a2 = last ? nA : cA + (size_t)(t + 2) * kstep; const char* b2 = last ? nB : cB + (size_t)(t + 2) * kstep;
;             const char* a3 = a2 + kstep; const char* b3 = b2 + kstep;
;     ...
;             PG8_LDB(B0, 1, 0); PG8_LDB(B1, 1, 1); PG8_SCHED; PG8_LDA(At, 1, 0); PG8_STAGE_A(PG8_SA(0, 1), a2, 1, gsel);
;             PG8_WAIT_V(8); PG8_WAIT_L(0); PG8_BAR; PG8_MMA(0, 0, At, B0); PG8_MMA(0, 1, At, B1); PG8_BAR; PG8_SCHED;
;             PG8_LDA(At, 1, 1); PG8_STAGE(PG8_SB(1, 0), b3, voffB); PG8_STAGE(PG8_SB(1, 1), b3 + hstep, voffB); PG8_STAGE_A(PG8_SA(1, 0), a3, 0, gsel);
;             PG8_WAIT_V(8); PG8_WAIT_L(0); PG8_BAR; PG8_MMA(1, 0, At, B0); PG8_MMA(1, 1, At, B1); PG8_BAR; PG8_SCHED;
	s_add_i32 s84, 0, 0x18000
	s_add_i32 s85, 0, 0x1c000
	v_add_u32_e32 v14, s84, v191
	v_add_u32_e32 v30, s85, v191
	ds_read_b128 v[2:5], v14
	ds_read_b128 v[6:9], v14 offset:1024
	ds_read_b128 v[10:13], v14 offset:2048
	ds_read_b128 v[14:17], v14 offset:3072
	ds_read_b128 v[18:21], v30
	ds_read_b128 v[22:25], v30 offset:1024
	ds_read_b128 v[26:29], v30 offset:2048
	ds_read_b128 v[30:33], v30 offset:3072
	s_add_u32 s52, s52, 0x20000
	s_addc_u32 s53, s53, 0
	s_mov_b32 m0, s65
	v_lshl_add_u64 v[226:227], s[52:53], 0, v[168:169]
	ds_read_b128 v[194:197], v192 offset:32768
	ds_read_b128 v[198:201], v192 offset:33792
	ds_read_b128 v[202:205], v192 offset:34816
	ds_read_b128 v[206:209], v192 offset:35840
	ds_read_b128 v[210:213], v192 offset:36864
	ds_read_b128 v[214:217], v192 offset:37888
	ds_read_b128 v[218:221], v192 offset:38912
	ds_read_b128 v[222:225], v192 offset:39936
	global_load_lds_dwordx4 v[226:227], off
	v_lshl_add_u64 v[226:227], s[52:53], 0, v[164:165]
	s_mov_b32 m0, s66
	s_nop 0
	global_load_lds_dwordx4 v[226:227], off
	s_waitcnt vmcnt(8)
	s_waitcnt lgkmcnt(0)
	s_barrier
	s_setprio 1
	s_waitcnt lgkmcnt(0)
	v_mfma_f32_16x16x128_f8f6f4 v[158:161], v[2:9], v[194:201], v[158:161]
	v_mfma_f32_16x16x128_f8f6f4 v[154:157], v[10:17], v[194:201], v[154:157]
	v_mfma_f32_16x16x128_f8f6f4 v[150:153], v[2:9], v[202:209], v[150:153]
	v_mfma_f32_16x16x128_f8f6f4 v[146:149], v[10:17], v[202:209], v[146:149]
	v_mfma_f32_16x16x128_f8f6f4 v[130:133], v[2:9], v[210:217], v[130:133]
	v_mfma_f32_16x16x128_f8f6f4 v[122:125], v[10:17], v[210:217], v[122:125]
	v_mfma_f32_16x16x128_f8f6f4 v[118:121], v[2:9], v[218:225], v[118:121]
	v_mfma_f32_16x16x128_f8f6f4 v[114:117], v[10:17], v[218:225], v[114:117]
	s_setprio 0
	s_setprio 1
	v_mfma_f32_16x16x128_f8f6f4 v[142:145], v[18:25], v[194:201], v[142:145]
	v_mfma_f32_16x16x128_f8f6f4 v[138:141], v[26:33], v[194:201], v[138:141]
	v_mfma_f32_16x16x128_f8f6f4 v[134:137], v[18:25], v[202:209], v[134:137]
	v_mfma_f32_16x16x128_f8f6f4 v[126:129], v[26:33], v[202:209], v[126:129]
	v_mfma_f32_16x16x128_f8f6f4 v[110:113], v[18:25], v[210:217], v[110:113]
	v_mfma_f32_16x16x128_f8f6f4 v[106:109], v[26:33], v[210:217], v[106:109]
	v_mfma_f32_16x16x128_f8f6f4 v[102:105], v[18:25], v[218:225], v[102:105]
	v_mfma_f32_16x16x128_f8f6f4 v[98:101], v[26:33], v[218:225], v[98:101]
	s_setprio 0
	s_barrier
	s_add_i32 s52, s84, s60
	v_lshl_add_u64 v[182:183], v[182:183], 0, s[18:19]
	s_mov_b32 m0, s52
	ds_read_b128 v[194:197], v192 offset:49152
	ds_read_b128 v[198:201], v192 offset:50176
	ds_read_b128 v[202:205], v192 offset:51200
	ds_read_b128 v[206:209], v192 offset:52224
	ds_read_b128 v[210:213], v192 offset:53248
	ds_read_b128 v[214:217], v192 offset:54272
	ds_read_b128 v[218:221], v192 offset:55296
	ds_read_b128 v[222:225], v192 offset:56320
	global_load_lds_dwordx4 v[182:183], off
	s_add_i32 m0, s52, 0x2000
	s_add_u32 s50, s50, 0x20080
	v_lshl_add_u64 v[182:183], v[184:185], 0, s[18:19]
	s_addc_u32 s51, s51, 0
	s_add_i32 s52, s85, s60
	global_load_lds_dwordx4 v[182:183], off
	v_lshl_add_u64 v[182:183], s[50:51], 0, v[166:167]
	s_mov_b32 m0, s52
	s_nop 0
	global_load_lds_dwordx4 v[182:183], off
	v_lshl_add_u64 v[182:183], s[50:51], 0, v[162:163]
	s_add_i32 m0, s52, 0x2000
	s_nop 0
	global_load_lds_dwordx4 v[182:183], off
	v_lshl_add_u64 v[182:183], v[186:187], 0, s[18:19]
	s_mov_b32 m0, s69
	s_nop 0
	global_load_lds_dwordx4 v[182:183], off
	v_lshl_add_u64 v[182:183], v[188:189], 0, s[18:19]
	s_mov_b32 m0, s70
	s_nop 0
	global_load_lds_dwordx4 v[182:183], off
	s_waitcnt vmcnt(8)
	s_waitcnt lgkmcnt(0)
	s_barrier
	s_setprio 1
	s_waitcnt lgkmcnt(0)
	v_mfma_f32_16x16x128_f8f6f4 v[94:97], v[2:9], v[194:201], v[94:97]
	v_mfma_f32_16x16x128_f8f6f4 v[90:93], v[10:17], v[194:201], v[90:93]
	v_mfma_f32_16x16x128_f8f6f4 v[86:89], v[2:9], v[202:209], v[86:89]
	v_mfma_f32_16x16x128_f8f6f4 v[82:85], v[10:17], v[202:209], v[82:85]
	v_mfma_f32_16x16x128_f8f6f4 v[66:69], v[2:9], v[210:217], v[66:69]
	v_mfma_f32_16x16x128_f8f6f4 v[58:61], v[10:17], v[210:217], v[58:61]
	v_mfma_f32_16x16x128_f8f6f4 v[54:57], v[2:9], v[218:225], v[54:57]
	v_mfma_f32_16x16x128_f8f6f4 v[50:53], v[10:17], v[218:225], v[50:53]
	s_setprio 0
	s_setprio 1
	v_mfma_f32_16x16x128_f8f6f4 v[78:81], v[18:25], v[194:201], v[78:81]
	v_mfma_f32_16x16x128_f8f6f4 v[74:77], v[26:33], v[194:201], v[74:77]
	v_mfma_f32_16x16x128_f8f6f4 v[70:73], v[18:25], v[202:209], v[70:73]
	v_mfma_f32_16x16x128_f8f6f4 v[62:65], v[26:33], v[202:209], v[62:65]
	v_mfma_f32_16x16x128_f8f6f4 v[46:49], v[18:25], v[210:217], v[46:49]
	v_mfma_f32_16x16x128_f8f6f4 v[42:45], v[26:33], v[210:217], v[42:45]
	v_mfma_f32_16x16x128_f8f6f4 v[38:41], v[18:25], v[218:225], v[38:41]
	v_mfma_f32_16x16x128_f8f6f4 v[34:37], v[26:33], v[218:225], v[34:37]
	s_setprio 0
	s_add_i32 s83, s83, 2
	s_add_u32 s48, s48, 0x100
	s_addc_u32 s49, s49, 0
	s_add_u32 s47, s47, 0x100
	s_addc_u32 s82, s82, 0
	s_cmp_gt_u32 s83, 5
	s_cbranch_scc1 .Lrot953_exit
	s_cmp_eq_u32 s83, 4
	s_cselect_b64 s[50:51], -1, 0
	s_cmp_lg_u32 s83, 4
	s_cbranch_scc1 .Lrot953_head
	s_barrier

;     __device__ __forceinline__ int brow(const pg8::Unit& u) const { return (u.pn >> 8) * Nper + (u.pn & 255) * 256; }
; template <class Epi, class Sched, bool ALIGN_EPI = false, bool SP2 = false, bool FP8 = false, bool GATHER = false>
; __device__ __forceinline__ void gemm_phase(PG8_LAS unsigned char* lds, const Gemm g, const Sched& S, const Epi& E) {
;     ...
;         const bool has_next = S.next(ui + 1, nxt);
;         const char* nA = (has_next && !GATHER) ? (const char*)g.A + (size_t)nxt.pm * tstep : cA; const char* nB = has_next ? (const char*)g.Bt + (size_t)S.brow(nxt) * (size_t)K * 2 : cB;
;     ...
; #pragma unroll
;         for (int a = 0; a < 2; ++a)
; #pragma unroll
;             for (int b = 0; b < 2; ++b)
; #pragma unroll
;                 for (int m = 0; m < 4; ++m)
; #pragma unroll
;                     for (int n = 0; n < 2; ++n) acc[a][b][m][n] = (f32x4){0.f, 0.f, 0.f, 0.f};
;         cur = nxt; cA = nA; cB = nB; ++ui;
.LBB0_1496:
	s_ashr_i32 s45, s44, 31
	s_lshl_b64 s[46:47], s[44:45], 19
	s_add_u32 s46, s61, s46
	s_addc_u32 s47, s62, s47
	s_and_b64 s[48:49], s[4:5], exec
	s_cselect_b32 s45, s47, s55
	s_cselect_b32 s82, s46, s54
	s_lshl_b32 s48, s81, 8
	s_ashr_i32 s49, s48, 31
	s_lshl_b64 s[48:49], s[48:49], 11
	s_add_u32 s48, s63, s48
	s_addc_u32 s49, s65, s49
	s_and_b64 s[58:59], s[4:5], exec
	s_cselect_b32 s83, s49, s57
	s_cselect_b32 s84, s48, s56
	s_lshl_b32 s52, s52, 8
	s_ashr_i32 s58, s50, 4
	s_ashr_i32 s53, s52, 31
	s_cmpk_lt_i32 s50, 0x100
	s_mul_i32 s85, s58, 0x1800
	s_mul_hi_i32 s58, s58, 0x1800
	s_cselect_b32 s59, s58, 0
	s_cselect_b32 s58, s85, 0x18000
	s_lshl_b64 s[58:59], s[58:59], 2
	s_add_u32 s85, s71, s58
	s_addc_u32 s86, s72, s59
	s_lshl_b64 s[58:59], s[52:53], 2
	s_add_u32 s58, s85, s58
	s_addc_u32 s59, s86, s59
	s_add_u32 s54, s54, 0x40080
	s_addc_u32 s55, s55, 0
	s_add_u32 s53, s56, 0x100
	v_mov_b32_e32 v2, 0
	v_lshl_add_u64 v[122:123], s[58:59], 0, v[162:163]
	s_addc_u32 s85, s57, 0
	s_mov_b32 s86, -2
	v_mov_b32_e32 v3, v2
	v_mov_b32_e32 v4, v2
	v_mov_b32_e32 v5, v2
	v_mov_b32_e32 v6, v2
	v_mov_b32_e32 v7, v2
	v_mov_b32_e32 v8, v2
	v_mov_b32_e32 v9, v2
	v_mov_b32_e32 v14, v2
	v_mov_b32_e32 v15, v2
	v_mov_b32_e32 v16, v2
	v_mov_b32_e32 v17, v2
	v_mov_b32_e32 v18, v2
	v_mov_b32_e32 v19, v2
	v_mov_b32_e32 v20, v2
	v_mov_b32_e32 v21, v2
	v_mov_b32_e32 v30, v2
	v_mov_b32_e32 v31, v2
	v_mov_b32_e32 v32, v2
	v_mov_b32_e32 v33, v2
	v_mov_b32_e32 v34, v2
	v_mov_b32_e32 v35, v2
	v_mov_b32_e32 v36, v2
	v_mov_b32_e32 v37, v2
	v_mov_b32_e32 v46, v2
	v_mov_b32_e32 v47, v2
	v_mov_b32_e32 v48, v2
	v_mov_b32_e32 v49, v2
	v_mov_b32_e32 v50, v2
	v_mov_b32_e32 v51, v2
	v_mov_b32_e32 v52, v2
	v_mov_b32_e32 v53, v2
	v_mov_b32_e32 v10, v2
	v_mov_b32_e32 v11, v2
	v_mov_b32_e32 v12, v2
	v_mov_b32_e32 v13, v2
	v_mov_b32_e32 v22, v2
	v_mov_b32_e32 v23, v2
	v_mov_b32_e32 v24, v2
	v_mov_b32_e32 v25, v2
	v_mov_b32_e32 v26, v2
	v_mov_b32_e32 v27, v2
	v_mov_b32_e32 v28, v2
	v_mov_b32_e32 v29, v2
	v_mov_b32_e32 v38, v2
	v_mov_b32_e32 v39, v2
	v_mov_b32_e32 v40, v2
	v_mov_b32_e32 v41, v2
	v_mov_b32_e32 v42, v2
	v_mov_b32_e32 v43, v2
	v_mov_b32_e32 v44, v2
	v_mov_b32_e32 v45, v2
	v_mov_b32_e32 v54, v2
	v_mov_b32_e32 v55, v2
	v_mov_b32_e32 v56, v2
	v_mov_b32_e32 v57, v2
	v_mov_b32_e32 v58, v2
	v_mov_b32_e32 v59, v2
	v_mov_b32_e32 v60, v2
	v_mov_b32_e32 v61, v2
	v_mov_b32_e32 v62, v2
	v_mov_b32_e32 v63, v2
	v_mov_b32_e32 v64, v2
	v_mov_b32_e32 v65, v2
	v_mov_b32_e32 v66, v2
	v_mov_b32_e32 v67, v2
	v_mov_b32_e32 v68, v2
	v_mov_b32_e32 v69, v2
	s_waitcnt vmcnt(0)
	v_mov_b32_e32 v70, v2
	v_mov_b32_e32 v71, v2
	v_mov_b32_e32 v72, v2
	v_mov_b32_e32 v73, v2
	v_mov_b32_e32 v78, v2
	v_mov_b32_e32 v79, v2
	v_mov_b32_e32 v80, v2
	v_mov_b32_e32 v81, v2
	v_mov_b32_e32 v82, v2
	v_mov_b32_e32 v83, v2
	v_mov_b32_e32 v84, v2
	v_mov_b32_e32 v85, v2
	v_mov_b32_e32 v94, v2
	v_mov_b32_e32 v95, v2
	v_mov_b32_e32 v96, v2
	v_mov_b32_e32 v97, v2
	v_mov_b32_e32 v98, v2
	v_mov_b32_e32 v99, v2
	v_mov_b32_e32 v100, v2
	v_mov_b32_e32 v101, v2
	v_mov_b32_e32 v110, v2
	v_mov_b32_e32 v111, v2
	v_mov_b32_e32 v112, v2
	v_mov_b32_e32 v113, v2
	v_mov_b32_e32 v114, v2
	v_mov_b32_e32 v115, v2
	v_mov_b32_e32 v116, v2
	v_mov_b32_e32 v117, v2
	v_mov_b32_e32 v74, v2
	v_mov_b32_e32 v75, v2
	v_mov_b32_e32 v76, v2
	v_mov_b32_e32 v77, v2
	v_mov_b32_e32 v86, v2
	v_mov_b32_e32 v87, v2
	v_mov_b32_e32 v88, v2
	v_mov_b32_e32 v89, v2
	v_mov_b32_e32 v90, v2
	v_mov_b32_e32 v91, v2
	v_mov_b32_e32 v92, v2
	v_mov_b32_e32 v93, v2
	v_mov_b32_e32 v102, v2
	v_mov_b32_e32 v103, v2
	v_mov_b32_e32 v104, v2
	v_mov_b32_e32 v105, v2
	v_mov_b32_e32 v106, v2
	v_mov_b32_e32 v107, v2
	v_mov_b32_e32 v108, v2
	v_mov_b32_e32 v109, v2
	v_mov_b32_e32 v118, v2
	v_mov_b32_e32 v119, v2
	v_mov_b32_e32 v120, v2
	v_mov_b32_e32 v121, v2
	v_mov_b32_e32 v138, v2
	v_mov_b32_e32 v139, v2
	v_mov_b32_e32 v140, v2
	v_mov_b32_e32 v141, v2
	v_mov_b32_e32 v142, v2
	v_mov_b32_e32 v143, v2
	v_mov_b32_e32 v144, v2
	v_mov_b32_e32 v145, v2
	s_branch .LBB0_1498
.Lrot1497_head:
	s_barrier
.LBB0_1497:
	v_add_u32_e32 v136, s79, v169
	ds_read_b128 v[124:127], v136
	ds_read_b128 v[128:131], v136 offset:1024
	ds_read_b128 v[132:135], v136 offset:2048
	ds_read_b128 v[164:167], v136 offset:3072
	v_add_u32_e32 v136, s80, v169
	ds_read_b128 v[172:175], v136
	ds_read_b128 v[176:179], v136 offset:1024
	ds_read_b128 v[180:183], v136 offset:2048
	ds_read_b128 v[184:187], v136 offset:3072
	s_add_u32 s58, s54, 0xfffc0080
	s_addc_u32 s59, s55, -1
	s_and_b64 s[56:57], s[56:57], exec
	s_cselect_b32 s59, s59, s45
	s_cselect_b32 s58, s58, s82
	s_cselect_b32 s57, s85, s83
	s_cselect_b32 s56, s53, s84
	v_lshl_add_u64 v[136:137], s[54:55], 0, v[154:155]
	s_add_i32 m0, s51, 0xc000
	ds_read_b128 v[188:191], v170
	ds_read_b128 v[192:195], v170 offset:1024
	ds_read_b128 v[196:199], v170 offset:2048
	ds_read_b128 v[200:203], v170 offset:3072
	ds_read_b128 v[204:207], v170 offset:4096
	ds_read_b128 v[208:211], v170 offset:5120
	ds_read_b128 v[212:215], v170 offset:6144
	ds_read_b128 v[216:219], v170 offset:7168
	global_load_lds_dwordx4 v[136:137], off
	v_lshl_add_u64 v[136:137], s[54:55], 0, v[156:157]
	s_add_i32 m0, s51, 0xe000
	s_nop 0
	global_load_lds_dwordx4 v[136:137], off
	s_waitcnt vmcnt(8)
	s_waitcnt lgkmcnt(0)
	s_barrier
; #define PG8_STAGE(bufoff, gbase, voff) do { _Pragma("unroll") for (int _i = 0; _i < 2; ++_i) \
;         __builtin_amdgcn_global_load_lds((const unsigned*)((const char*)(gbase) + (voff)[_i]), (PG8_LAS unsigned*)(lds + (bufoff) + ldsw + _i * 8192), 16, 0, 0); } while (0)
; #define PG8_STAGE_A(bufoff, kbase, h, gv) do { if constexpr (GATHER) { PG8_STAGE(bufoff, kbase, (gv)[h]); } else { PG8_STAGE(bufoff, (kbase) + (h) * hstep, voffA); } } while (0)
; #define PG8_WAIT_V(n) asm volatile("s_waitcnt vmcnt(" #n ")" ::: "memory")
; #define PG8_WAIT_L(n) asm volatile("s_waitcnt lgkmcnt(" #n ")" ::: "memory")
; #define PG8_BAR __builtin_amdgcn_s_barrier()
; #define PG8_SCHED __builtin_amdgcn_sched_barrier(0)
; template <class Epi, class Sched, bool ALIGN_EPI = false, bool SP2 = false, bool FP8 = false, bool GATHER = false>
; __device__ __forceinline__ void gemm_phase(PG8_LAS unsigned char* lds, const Gemm g, const Sched& S, const Epi& E) {
;     ...
;             PG8_LDB(B0, 0, 0); PG8_LDB(B1, 0, 1); PG8_SCHED; PG8_LDA(At, 0, 0); PG8_STAGE_A(PG8_SA(1, 1), a1, 1, gcur);
;             PG8_WAIT_V(8); PG8_WAIT_L(0); PG8_BAR; PG8_MMA(0, 0, At, B0); PG8_MMA(0, 1, At, B1); PG8_BAR; PG8_SCHED;
;             PG8_LDA(At, 0, 1); PG8_STAGE(PG8_SB(0, 0), b2, voffB); PG8_STAGE(PG8_SB(0, 1), b2 + hstep, voffB); PG8_STAGE_A(PG8_SA(0, 0), a2, 0, gsel);
;             PG8_WAIT_V(8); PG8_WAIT_L(0); PG8_BAR; PG8_MMA(1, 0, At, B0); PG8_MMA(1, 1, At, B1); PG8_BAR; PG8_SCHED;
	s_setprio 1
	s_waitcnt lgkmcnt(0)
	v_mfma_f32_16x16x32_bf16 v[142:145], v[124:127], v[188:191], v[142:145]
	v_mfma_f32_16x16x32_bf16 v[136:139], v[132:135], v[188:191], v[138:141]
	v_mfma_f32_16x16x32_bf16 v[118:121], v[124:127], v[196:199], v[118:121]
	v_mfma_f32_16x16x32_bf16 v[106:109], v[132:135], v[196:199], v[106:109]
	v_mfma_f32_16x16x32_bf16 v[102:105], v[124:127], v[204:207], v[102:105]
	v_mfma_f32_16x16x32_bf16 v[90:93], v[132:135], v[204:207], v[90:93]
	v_mfma_f32_16x16x32_bf16 v[86:89], v[124:127], v[212:215], v[86:89]
	v_mfma_f32_16x16x32_bf16 v[74:77], v[132:135], v[212:215], v[74:77]
	v_mfma_f32_16x16x32_bf16 v[142:145], v[128:131], v[192:195], v[142:145]
	v_mfma_f32_16x16x32_bf16 v[136:139], v[164:167], v[192:195], v[136:139]
	v_mfma_f32_16x16x32_bf16 v[118:121], v[128:131], v[200:203], v[118:121]
	v_mfma_f32_16x16x32_bf16 v[106:109], v[164:167], v[200:203], v[106:109]
	v_mfma_f32_16x16x32_bf16 v[102:105], v[128:131], v[208:211], v[102:105]
	v_mfma_f32_16x16x32_bf16 v[90:93], v[164:167], v[208:211], v[90:93]
	v_mfma_f32_16x16x32_bf16 v[86:89], v[128:131], v[216:219], v[86:89]
	v_mfma_f32_16x16x32_bf16 v[74:77], v[164:167], v[216:219], v[74:77]
	s_setprio 0
	s_setprio 1
	v_mfma_f32_16x16x32_bf16 v[114:117], v[172:175], v[188:191], v[114:117]
	v_mfma_f32_16x16x32_bf16 v[110:113], v[180:183], v[188:191], v[110:113]
	v_mfma_f32_16x16x32_bf16 v[98:101], v[172:175], v[196:199], v[98:101]
	v_mfma_f32_16x16x32_bf16 v[94:97], v[180:183], v[196:199], v[94:97]
	v_mfma_f32_16x16x32_bf16 v[82:85], v[172:175], v[204:207], v[82:85]
	v_mfma_f32_16x16x32_bf16 v[78:81], v[180:183], v[204:207], v[78:81]
	v_mfma_f32_16x16x32_bf16 v[70:73], v[172:175], v[212:215], v[70:73]
	v_mfma_f32_16x16x32_bf16 v[66:69], v[180:183], v[212:215], v[66:69]
	v_mfma_f32_16x16x32_bf16 v[114:117], v[176:179], v[192:195], v[114:117]
	v_mfma_f32_16x16x32_bf16 v[110:113], v[184:187], v[192:195], v[110:113]
	v_mfma_f32_16x16x32_bf16 v[98:101], v[176:179], v[200:203], v[98:101]
	v_mfma_f32_16x16x32_bf16 v[94:97], v[184:187], v[200:203], v[94:97]
	v_mfma_f32_16x16x32_bf16 v[82:85], v[176:179], v[208:211], v[82:85]
	v_mfma_f32_16x16x32_bf16 v[78:81], v[184:187], v[208:211], v[78:81]
	v_mfma_f32_16x16x32_bf16 v[70:73], v[176:179], v[216:219], v[70:73]
	v_mfma_f32_16x16x32_bf16 v[66:69], v[184:187], v[216:219], v[66:69]
	s_setprio 0
	s_barrier
	s_add_i32 s87, s79, s66
	v_lshl_add_u64 v[220:221], s[56:57], 0, v[148:149]
	s_mov_b32 m0, s87
	ds_read_b128 v[188:191], v170 offset:16384
	ds_read_b128 v[192:195], v170 offset:17408
	ds_read_b128 v[196:199], v170 offset:18432
	ds_read_b128 v[200:203], v170 offset:19456
	ds_read_b128 v[204:207], v170 offset:20480
	ds_read_b128 v[208:211], v170 offset:21504
	ds_read_b128 v[212:215], v170 offset:22528
	ds_read_b128 v[216:219], v170 offset:23552
	global_load_lds_dwordx4 v[220:221], off
	s_add_i32 m0, s87, 0x2000
	s_add_u32 s88, s56, 0x40000
	v_lshl_add_u64 v[222:223], s[56:57], 0, v[152:153]
	s_addc_u32 s89, s57, 0
	s_add_i32 s87, s80, s66
	global_load_lds_dwordx4 v[222:223], off
	v_lshl_add_u64 v[140:141], s[88:89], 0, v[148:149]
	s_mov_b32 m0, s87
	v_lshl_add_u64 v[224:225], s[58:59], 0, v[146:147]
	global_load_lds_dwordx4 v[140:141], off
	v_lshl_add_u64 v[140:141], s[88:89], 0, v[152:153]
	s_add_i32 m0, s87, 0x2000
	v_lshl_add_u64 v[226:227], s[58:59], 0, v[150:151]
	global_load_lds_dwordx4 v[140:141], off
	s_mov_b32 m0, s51
	s_nop 0
	global_load_lds_dwordx4 v[224:225], off
	s_mov_b32 m0, s67
	s_nop 0
	global_load_lds_dwordx4 v[226:227], off
	s_waitcnt vmcnt(8)
	s_waitcnt lgkmcnt(0)
	s_barrier
	s_setprio 1
	s_waitcnt lgkmcnt(0)
	v_mfma_f32_16x16x32_bf16 v[62:65], v[124:127], v[188:191], v[62:65]
	v_mfma_f32_16x16x32_bf16 v[58:61], v[132:135], v[188:191], v[58:61]
	v_mfma_f32_16x16x32_bf16 v[54:57], v[124:127], v[196:199], v[54:57]
	v_mfma_f32_16x16x32_bf16 v[42:45], v[132:135], v[196:199], v[42:45]
	v_mfma_f32_16x16x32_bf16 v[38:41], v[124:127], v[204:207], v[38:41]
	v_mfma_f32_16x16x32_bf16 v[26:29], v[132:135], v[204:207], v[26:29]
	v_mfma_f32_16x16x32_bf16 v[22:25], v[124:127], v[212:215], v[22:25]
	v_mfma_f32_16x16x32_bf16 v[10:13], v[132:135], v[212:215], v[10:13]
	v_mfma_f32_16x16x32_bf16 v[62:65], v[128:131], v[192:195], v[62:65]
	v_mfma_f32_16x16x32_bf16 v[58:61], v[164:167], v[192:195], v[58:61]
	v_mfma_f32_16x16x32_bf16 v[54:57], v[128:131], v[200:203], v[54:57]
	v_mfma_f32_16x16x32_bf16 v[42:45], v[164:167], v[200:203], v[42:45]
	v_mfma_f32_16x16x32_bf16 v[38:41], v[128:131], v[208:211], v[38:41]
	v_mfma_f32_16x16x32_bf16 v[26:29], v[164:167], v[208:211], v[26:29]
	v_mfma_f32_16x16x32_bf16 v[22:25], v[128:131], v[216:219], v[22:25]
	v_mfma_f32_16x16x32_bf16 v[10:13], v[164:167], v[216:219], v[10:13]
	s_setprio 0
	s_setprio 1
	v_mfma_f32_16x16x32_bf16 v[50:53], v[172:175], v[188:191], v[50:53]
	v_mfma_f32_16x16x32_bf16 v[46:49], v[180:183], v[188:191], v[46:49]
	v_mfma_f32_16x16x32_bf16 v[34:37], v[172:175], v[196:199], v[34:37]
	v_mfma_f32_16x16x32_bf16 v[30:33], v[180:183], v[196:199], v[30:33]
	v_mfma_f32_16x16x32_bf16 v[18:21], v[172:175], v[204:207], v[18:21]
	v_mfma_f32_16x16x32_bf16 v[14:17], v[180:183], v[204:207], v[14:17]
	v_mfma_f32_16x16x32_bf16 v[6:9], v[172:175], v[212:215], v[6:9]
	v_mfma_f32_16x16x32_bf16 v[2:5], v[180:183], v[212:215], v[2:5]
	v_mfma_f32_16x16x32_bf16 v[50:53], v[176:179], v[192:195], v[50:53]
	v_mfma_f32_16x16x32_bf16 v[46:49], v[184:187], v[192:195], v[46:49]
	v_mfma_f32_16x16x32_bf16 v[34:37], v[176:179], v[200:203], v[34:37]
	v_mfma_f32_16x16x32_bf16 v[30:33], v[184:187], v[200:203], v[30:33]
	v_mfma_f32_16x16x32_bf16 v[18:21], v[176:179], v[208:211], v[18:21]
	v_mfma_f32_16x16x32_bf16 v[14:17], v[184:187], v[208:211], v[14:17]
	v_mfma_f32_16x16x32_bf16 v[6:9], v[176:179], v[216:219], v[6:9]
	v_mfma_f32_16x16x32_bf16 v[2:5], v[184:187], v[216:219], v[2:5]
	s_setprio 0
	s_barrier
; #define PG8_STAGE_A(bufoff, kbase, h, gv) do { if constexpr (GATHER) { PG8_STAGE(bufoff, kbase, (gv)[h]); } else { PG8_STAGE(bufoff, (kbase) + (h) * hstep, voffA); } } while (0)
; #define PG8_WAIT_V(n) asm volatile("s_waitcnt vmcnt(" #n ")" ::: "memory")
; #define PG8_WAIT_L(n) asm volatile("s_waitcnt lgkmcnt(" #n ")" ::: "memory")
; #define PG8_BAR __builtin_amdgcn_s_barrier()
; #define PG8_SCHED __builtin_amdgcn_sched_barrier(0)
; template <class Epi, class Sched, bool ALIGN_EPI = false, bool SP2 = false, bool FP8 = false, bool GATHER = false>
; __device__ __forceinline__ void gemm_phase(PG8_LAS unsigned char* lds, const Gemm g, const Sched& S, const Epi& E) {
;     ...
;             PG8_LDB(B0, 1, 0); PG8_LDB(B1, 1, 1); PG8_SCHED; PG8_LDA(At, 1, 0); PG8_STAGE_A(PG8_SA(0, 1), a2, 1, gsel);
;             PG8_WAIT_V(8); PG8_WAIT_L(0); PG8_BAR; PG8_MMA(0, 0, At, B0); PG8_MMA(0, 1, At, B1); PG8_BAR; PG8_SCHED;
	s_add_i32 s87, 0, 0x18000
	v_add_u32_e32 v140, s87, v169
	s_add_i32 s88, 0, 0x1c000
	ds_read_b128 v[124:127], v140
	ds_read_b128 v[128:131], v140 offset:1024
	ds_read_b128 v[132:135], v140 offset:2048
	ds_read_b128 v[164:167], v140 offset:3072
	v_add_u32_e32 v140, s88, v169
	ds_read_b128 v[172:175], v140
	ds_read_b128 v[176:179], v140 offset:1024
	ds_read_b128 v[180:183], v140 offset:2048
	ds_read_b128 v[184:187], v140 offset:3072
	s_add_u32 s58, s58, 0x40000
	s_addc_u32 s59, s59, 0
	s_mov_b32 m0, s68
	v_lshl_add_u64 v[140:141], s[58:59], 0, v[146:147]
	ds_read_b128 v[188:191], v170 offset:32768
	ds_read_b128 v[192:195], v170 offset:33792
	ds_read_b128 v[196:199], v170 offset:34816
	ds_read_b128 v[200:203], v170 offset:35840
	ds_read_b128 v[204:207], v170 offset:36864
	ds_read_b128 v[208:211], v170 offset:37888
	ds_read_b128 v[212:215], v170 offset:38912
	ds_read_b128 v[216:219], v170 offset:39936
	global_load_lds_dwordx4 v[140:141], off
	v_lshl_add_u64 v[140:141], s[58:59], 0, v[150:151]
	s_mov_b32 m0, s69
	s_nop 0
	global_load_lds_dwordx4 v[140:141], off
	s_waitcnt vmcnt(8)
	s_waitcnt lgkmcnt(0)
	s_barrier
	s_setprio 1
	s_waitcnt lgkmcnt(0)
	v_mfma_f32_16x16x32_bf16 v[140:143], v[124:127], v[188:191], v[142:145]
	v_mfma_f32_16x16x32_bf16 v[136:139], v[132:135], v[188:191], v[136:139]
	v_mfma_f32_16x16x32_bf16 v[118:121], v[124:127], v[196:199], v[118:121]
	v_mfma_f32_16x16x32_bf16 v[106:109], v[132:135], v[196:199], v[106:109]
	v_mfma_f32_16x16x32_bf16 v[102:105], v[124:127], v[204:207], v[102:105]
	v_mfma_f32_16x16x32_bf16 v[90:93], v[132:135], v[204:207], v[90:93]
	v_mfma_f32_16x16x32_bf16 v[86:89], v[124:127], v[212:215], v[86:89]
	v_mfma_f32_16x16x32_bf16 v[74:77], v[132:135], v[212:215], v[74:77]
	v_mfma_f32_16x16x32_bf16 v[142:145], v[128:131], v[192:195], v[140:143]
	v_mfma_f32_16x16x32_bf16 v[138:141], v[164:167], v[192:195], v[136:139]
	v_mfma_f32_16x16x32_bf16 v[118:121], v[128:131], v[200:203], v[118:121]
	v_mfma_f32_16x16x32_bf16 v[106:109], v[164:167], v[200:203], v[106:109]
	v_mfma_f32_16x16x32_bf16 v[102:105], v[128:131], v[208:211], v[102:105]
	v_mfma_f32_16x16x32_bf16 v[90:93], v[164:167], v[208:211], v[90:93]
	v_mfma_f32_16x16x32_bf16 v[86:89], v[128:131], v[216:219], v[86:89]
	v_mfma_f32_16x16x32_bf16 v[74:77], v[164:167], v[216:219], v[74:77]
	s_setprio 0
	s_setprio 1
	v_mfma_f32_16x16x32_bf16 v[114:117], v[172:175], v[188:191], v[114:117]
	v_mfma_f32_16x16x32_bf16 v[110:113], v[180:183], v[188:191], v[110:113]
	v_mfma_f32_16x16x32_bf16 v[98:101], v[172:175], v[196:199], v[98:101]
	v_mfma_f32_16x16x32_bf16 v[94:97], v[180:183], v[196:199], v[94:97]
	v_mfma_f32_16x16x32_bf16 v[82:85], v[172:175], v[204:207], v[82:85]
	v_mfma_f32_16x16x32_bf16 v[78:81], v[180:183], v[204:207], v[78:81]
	v_mfma_f32_16x16x32_bf16 v[70:73], v[172:175], v[212:215], v[70:73]
	v_mfma_f32_16x16x32_bf16 v[66:69], v[180:183], v[212:215], v[66:69]
	v_mfma_f32_16x16x32_bf16 v[114:117], v[176:179], v[192:195], v[114:117]
	v_mfma_f32_16x16x32_bf16 v[110:113], v[184:187], v[192:195], v[110:113]
	v_mfma_f32_16x16x32_bf16 v[98:101], v[176:179], v[200:203], v[98:101]
	v_mfma_f32_16x16x32_bf16 v[94:97], v[184:187], v[200:203], v[94:97]
	v_mfma_f32_16x16x32_bf16 v[82:85], v[176:179], v[208:211], v[82:85]
	v_mfma_f32_16x16x32_bf16 v[78:81], v[184:187], v[208:211], v[78:81]
	v_mfma_f32_16x16x32_bf16 v[70:73], v[176:179], v[216:219], v[70:73]
	v_mfma_f32_16x16x32_bf16 v[66:69], v[184:187], v[216:219], v[66:69]
	s_setprio 0
	s_barrier
; #define PG8_STAGE(bufoff, gbase, voff) do { _Pragma("unroll") for (int _i = 0; _i < 2; ++_i) \
;         __builtin_amdgcn_global_load_lds((const unsigned*)((const char*)(gbase) + (voff)[_i]), (PG8_LAS unsigned*)(lds + (bufoff) + ldsw + _i * 8192), 16, 0, 0); } while (0)
; #define PG8_STAGE_A(bufoff, kbase, h, gv) do { if constexpr (GATHER) { PG8_STAGE(bufoff, kbase, (gv)[h]); } else { PG8_STAGE(bufoff, (kbase) + (h) * hstep, voffA); } } while (0)
; #define PG8_WAIT_V(n) asm volatile("s_waitcnt vmcnt(" #n ")" ::: "memory")
; #define PG8_WAIT_L(n) asm volatile("s_waitcnt lgkmcnt(" #n ")" ::: "memory")
; #define PG8_BAR __builtin_amdgcn_s_barrier()
; #define PG8_SCHED __builtin_amdgcn_sched_barrier(0)
; template <class Epi, class Sched, bool ALIGN_EPI = false, bool SP2 = false, bool FP8 = false, bool GATHER = false>
; __device__ __forceinline__ void gemm_phase(PG8_LAS unsigned char* lds, const Gemm g, const Sched& S, const Epi& E) {
;     ...
;         for (int t = 0; t < nt; t += 2) {
;             const bool last = (t == nt - 2);
;             const char* a1 = cA + (size_t)(t + 1) * kstep;
;             const char* a2 = last ? nA : cA + (size_t)(t + 2) * kstep; const char* b2 = last ? nB : cB + (size_t)(t + 2) * kstep;
;             const char* a3 = a2 + kstep; const char* b3 = b2 + kstep;
;     ...
;             PG8_LDA(At, 1, 1); PG8_STAGE(PG8_SB(1, 0), b3, voffB); PG8_STAGE(PG8_SB(1, 1), b3 + hstep, voffB); PG8_STAGE_A(PG8_SA(1, 0), a3, 0, gsel);
;             PG8_WAIT_V(8); PG8_WAIT_L(0); PG8_BAR; PG8_MMA(1, 0, At, B0); PG8_MMA(1, 1, At, B1); PG8_BAR; PG8_SCHED;
	s_add_i32 s58, s87, s66
	v_lshl_add_u64 v[136:137], v[220:221], 0, s[16:17]
	s_mov_b32 m0, s58
	ds_read_b128 v[188:191], v170 offset:49152
	ds_read_b128 v[192:195], v170 offset:50176
	ds_read_b128 v[196:199], v170 offset:51200
	ds_read_b128 v[200:203], v170 offset:52224
	ds_read_b128 v[204:207], v170 offset:53248
	ds_read_b128 v[208:211], v170 offset:54272
	ds_read_b128 v[212:215], v170 offset:55296
	ds_read_b128 v[216:219], v170 offset:56320
	global_load_lds_dwordx4 v[136:137], off
	s_add_i32 m0, s58, 0x2000
	s_add_u32 s56, s56, 0x40080
	v_lshl_add_u64 v[136:137], v[222:223], 0, s[16:17]
	s_addc_u32 s57, s57, 0
	s_add_i32 s58, s88, s66
	global_load_lds_dwordx4 v[136:137], off
	v_lshl_add_u64 v[136:137], s[56:57], 0, v[148:149]
	s_mov_b32 m0, s58
	s_nop 0
	global_load_lds_dwordx4 v[136:137], off
	v_lshl_add_u64 v[136:137], s[56:57], 0, v[152:153]
	s_add_i32 m0, s58, 0x2000
	s_nop 0
	global_load_lds_dwordx4 v[136:137], off
	v_lshl_add_u64 v[136:137], v[224:225], 0, s[16:17]
	s_mov_b32 m0, s75
	s_nop 0
	global_load_lds_dwordx4 v[136:137], off
	v_lshl_add_u64 v[136:137], v[226:227], 0, s[16:17]
	s_mov_b32 m0, s76
	s_nop 0
	global_load_lds_dwordx4 v[136:137], off
	s_waitcnt vmcnt(8)
	s_waitcnt lgkmcnt(0)
	s_barrier
	s_setprio 1
	s_waitcnt lgkmcnt(0)
	v_mfma_f32_16x16x32_bf16 v[62:65], v[124:127], v[188:191], v[62:65]
	v_mfma_f32_16x16x32_bf16 v[58:61], v[132:135], v[188:191], v[58:61]
	v_mfma_f32_16x16x32_bf16 v[54:57], v[124:127], v[196:199], v[54:57]
	v_mfma_f32_16x16x32_bf16 v[42:45], v[132:135], v[196:199], v[42:45]
	v_mfma_f32_16x16x32_bf16 v[38:41], v[124:127], v[204:207], v[38:41]
	v_mfma_f32_16x16x32_bf16 v[26:29], v[132:135], v[204:207], v[26:29]
	v_mfma_f32_16x16x32_bf16 v[22:25], v[124:127], v[212:215], v[22:25]
	v_mfma_f32_16x16x32_bf16 v[10:13], v[132:135], v[212:215], v[10:13]
	v_mfma_f32_16x16x32_bf16 v[62:65], v[128:131], v[192:195], v[62:65]
	v_mfma_f32_16x16x32_bf16 v[58:61], v[164:167], v[192:195], v[58:61]
	v_mfma_f32_16x16x32_bf16 v[54:57], v[128:131], v[200:203], v[54:57]
	v_mfma_f32_16x16x32_bf16 v[42:45], v[164:167], v[200:203], v[42:45]
	v_mfma_f32_16x16x32_bf16 v[38:41], v[128:131], v[208:211], v[38:41]
	v_mfma_f32_16x16x32_bf16 v[26:29], v[164:167], v[208:211], v[26:29]
	v_mfma_f32_16x16x32_bf16 v[22:25], v[128:131], v[216:219], v[22:25]
	v_mfma_f32_16x16x32_bf16 v[10:13], v[164:167], v[216:219], v[10:13]
	s_setprio 0
	s_setprio 1
	v_mfma_f32_16x16x32_bf16 v[50:53], v[172:175], v[188:191], v[50:53]
	v_mfma_f32_16x16x32_bf16 v[46:49], v[180:183], v[188:191], v[46:49]
	v_mfma_f32_16x16x32_bf16 v[34:37], v[172:175], v[196:199], v[34:37]
	v_mfma_f32_16x16x32_bf16 v[30:33], v[180:183], v[196:199], v[30:33]
	v_mfma_f32_16x16x32_bf16 v[18:21], v[172:175], v[204:207], v[18:21]
	v_mfma_f32_16x16x32_bf16 v[14:17], v[180:183], v[204:207], v[14:17]
	v_mfma_f32_16x16x32_bf16 v[6:9], v[172:175], v[212:215], v[6:9]
	v_mfma_f32_16x16x32_bf16 v[2:5], v[180:183], v[212:215], v[2:5]
	v_mfma_f32_16x16x32_bf16 v[50:53], v[176:179], v[192:195], v[50:53]
	v_mfma_f32_16x16x32_bf16 v[46:49], v[184:187], v[192:195], v[46:49]
	v_mfma_f32_16x16x32_bf16 v[34:37], v[176:179], v[200:203], v[34:37]
	v_mfma_f32_16x16x32_bf16 v[30:33], v[184:187], v[200:203], v[30:33]
	v_mfma_f32_16x16x32_bf16 v[18:21], v[176:179], v[208:211], v[18:21]
	v_mfma_f32_16x16x32_bf16 v[14:17], v[184:187], v[208:211], v[14:17]
	v_mfma_f32_16x16x32_bf16 v[6:9], v[176:179], v[216:219], v[6:9]
	v_mfma_f32_16x16x32_bf16 v[2:5], v[184:187], v[216:219], v[2:5]
	s_setprio 0
	s_add_i32 s86, s86, 2
	s_add_u32 s54, s54, 0x100
	s_addc_u32 s55, s55, 0
	s_add_u32 s53, s53, 0x100
	s_addc_u32 s85, s85, 0
	s_cmp_gt_u32 s86, 13
	s_cbranch_scc1 .Lrot1497_exit
	s_cmp_lg_u32 s86, 12
	s_cselect_b64 s[56:57], -1, 0
	s_or_b64 s[58:59], s[56:57], s[18:19]
	s_and_b64 vcc, exec, s[58:59]
	s_cbranch_vccnz .Lrot1497_head
	s_barrier

; #define PG8_STAGE(bufoff, gbase, voff) do { _Pragma("unroll") for (int _i = 0; _i < 2; ++_i) \
;         __builtin_amdgcn_global_load_lds((const unsigned*)((const char*)(gbase) + (voff)[_i]), (PG8_LAS unsigned*)(lds + (bufoff) + ldsw + _i * 8192), 16, 0, 0); } while (0)
; #define PG8_STAGE_A(bufoff, kbase, h, gv) do { if constexpr (GATHER) { PG8_STAGE(bufoff, kbase, (gv)[h]); } else { PG8_STAGE(bufoff, (kbase) + (h) * hstep, voffA); } } while (0)
; #define PG8_WAIT_V(n) asm volatile("s_waitcnt vmcnt(" #n ")" ::: "memory")
; #define PG8_WAIT_L(n) asm volatile("s_waitcnt lgkmcnt(" #n ")" ::: "memory")
; #define PG8_BAR __builtin_amdgcn_s_barrier()
; template <class Epi, class Sched, bool ALIGN_EPI = false, bool SP2 = false, bool FP8 = false, bool GATHER = false>
; __device__ __forceinline__ void gemm_phase(PG8_LAS unsigned char* lds, const Gemm g, const Sched& S, const Epi& E) {
;     ...
;             const char* a2 = last ? nA : cA + (size_t)(t + 2) * kstep; const char* b2 = last ? nB : cB + (size_t)(t + 2) * kstep;
;             const char* a3 = a2 + kstep; const char* b3 = b2 + kstep;
;             if (last && has_next) S.a_ready(nxt);
;             if (last) E.pre(cur, wid, lane);
;             if constexpr (GATHER) { if (t == nt - 4 && has_next) { _Pragma("unroll") for (int h_ = 0; h_ < 2; ++h_) _Pragma("unroll") for (int i_ = 0; i_ < 2; ++i_)
;                 asm volatile("global_load_dword %0, %1, off" : "+v"(graw[h_][i_]) : "v"(S.rowtok + (nxt.pm * BM + h_ * HALF + gR[i_])) : "memory"); } }
;             unsigned gsel[2][2];
;             if constexpr (GATHER) { _Pragma("unroll") for (int h_ = 0; h_ < 2; ++h_) _Pragma("unroll") for (int i_ = 0; i_ < 2; ++i_) { if (last && has_next) gnxt[h_][i_] = graw[h_][i_] * (unsigned)(K * 2) + gC[i_]; gsel[h_][i_] = (last && has_next) ? gnxt[h_][i_] : gcur[h_][i_]; } }
;             if constexpr (SP2) {
;             PG8_LDB(B0, 0, 0); PG8_LDB(B1, 0, 1); PG8_SCHED; PG8_LDA(At, 0, 0); PG8_STAGE_A(PG8_SA(1, 1), a1, 1, gcur);
;             PG8_WAIT_V(8); PG8_WAIT_L(0); PG8_BAR; PG8_MMA(0, 0, At, B0); PG8_MMA(0, 1, At, B1); PG8_BAR; PG8_SCHED;
;             PG8_LDA(At, 0, 1); PG8_STAGE(PG8_SB(0, 0), b2, voffB); PG8_STAGE(PG8_SB(0, 1), b2 + hstep, voffB); PG8_STAGE_A(PG8_SA(0, 0), a2, 0, gsel);
;             PG8_WAIT_V(8); PG8_WAIT_L(0); PG8_BAR; PG8_MMA(1, 0, At, B0); PG8_MMA(1, 1, At, B1); PG8_BAR; PG8_SCHED;
.Lpeel1781_body:
	s_add_u32 s50, s6, s46
	s_addc_u32 s51, s7, s47
	s_add_u32 s52, s50, 0x19200100
	s_addc_u32 s53, s51, 0
	s_and_b64 s[50:51], s[54:55], exec
	s_cselect_b32 s53, s9, s53
	s_cselect_b32 s52, s8, s52
	s_add_u32 s84, s20, s46
	s_addc_u32 s85, s82, s47
	s_and_b64 s[50:51], s[54:55], exec
	s_cselect_b32 s51, s35, s85
	s_cselect_b32 s50, s34, s84
	v_lshl_add_u32 v2, v213, 10, v1
	s_and_b64 vcc, s[44:45], s[54:55]
	v_cndmask_b32_e32 v209, v209, v2, vcc
	v_cndmask_b32_e32 v170, v217, v2, vcc
	v_lshl_add_u32 v2, v214, 10, v204
	v_cndmask_b32_e32 v210, v210, v2, vcc
	v_cndmask_b32_e32 v200, v180, v2, vcc
	v_add_u32_e32 v2, s74, v206
	v_add_u32_e32 v14, s75, v206
	ds_read_b128 v[18:21], v2
	ds_read_b128 v[22:25], v2 offset:1024
	ds_read_b128 v[26:29], v2 offset:2048
	ds_read_b128 v[30:33], v2 offset:3072
	ds_read_b128 v[2:5], v14
	ds_read_b128 v[6:9], v14 offset:1024
	ds_read_b128 v[10:13], v14 offset:2048
	ds_read_b128 v[14:17], v14 offset:3072
	v_lshl_add_u32 v177, v215, 10, v1
	v_lshl_add_u32 v179, v216, 10, v204
	v_cndmask_b32_e32 v211, v211, v177, vcc
	v_cndmask_b32_e32 v212, v212, v179, vcc
	v_cndmask_b32_e32 v177, v178, v177, vcc
	v_cndmask_b32_e32 v179, v176, v179, vcc
	v_lshl_add_u64 v[196:197], v[194:195], 0, s[46:47]
	s_add_i32 m0, s61, 0xc000
	ds_read_b128 v[218:221], v207
	ds_read_b128 v[222:225], v207 offset:1024
	ds_read_b128 v[226:229], v207 offset:2048
	ds_read_b128 v[230:233], v207 offset:3072
	ds_read_b128 v[234:237], v207 offset:4096
	ds_read_b128 v[238:241], v207 offset:5120
	ds_read_b128 v[242:245], v207 offset:6144
	ds_read_b128 v[246:249], v207 offset:7168
	global_load_lds_dwordx4 v[196:197], off
	v_lshl_add_u64 v[196:197], v[192:193], 0, s[46:47]
	s_add_i32 m0, s61, 0xe000
	s_nop 0
	global_load_lds_dwordx4 v[196:197], off
	s_waitcnt vmcnt(8)
	s_waitcnt lgkmcnt(0)
	s_barrier
	s_setprio 1
	s_waitcnt lgkmcnt(0)
	v_mfma_f32_16x16x128_f8f6f4 v[158:161], v[18:25], v[218:225], 0
	v_mfma_f32_16x16x128_f8f6f4 v[150:153], v[26:33], v[218:225], 0
	v_mfma_f32_16x16x128_f8f6f4 v[142:145], v[18:25], v[226:233], 0
	v_mfma_f32_16x16x128_f8f6f4 v[134:137], v[26:33], v[226:233], 0
	v_mfma_f32_16x16x128_f8f6f4 v[126:129], v[18:25], v[234:241], 0
	v_mfma_f32_16x16x128_f8f6f4 v[118:121], v[26:33], v[234:241], 0
	v_mfma_f32_16x16x128_f8f6f4 v[110:113], v[18:25], v[242:249], 0
	v_mfma_f32_16x16x128_f8f6f4 v[102:105], v[26:33], v[242:249], 0
	s_setprio 0
	s_setprio 1
	v_mfma_f32_16x16x128_f8f6f4 v[154:157], v[2:9], v[218:225], 0
	v_mfma_f32_16x16x128_f8f6f4 v[146:149], v[10:17], v[218:225], 0
	v_mfma_f32_16x16x128_f8f6f4 v[138:141], v[2:9], v[226:233], 0
	v_mfma_f32_16x16x128_f8f6f4 v[130:133], v[10:17], v[226:233], 0
	v_mfma_f32_16x16x128_f8f6f4 v[122:125], v[2:9], v[234:241], 0
	v_mfma_f32_16x16x128_f8f6f4 v[114:117], v[10:17], v[234:241], 0
	v_mfma_f32_16x16x128_f8f6f4 v[106:109], v[2:9], v[242:249], 0
	v_mfma_f32_16x16x128_f8f6f4 v[98:101], v[10:17], v[242:249], 0
	s_setprio 0
	s_barrier
	s_add_i32 s54, s74, s58
	v_lshl_add_u64 v[196:197], s[50:51], 0, v[168:169]
	s_mov_b32 m0, s54
	ds_read_b128 v[218:221], v207 offset:16384
	ds_read_b128 v[222:225], v207 offset:17408
	ds_read_b128 v[226:229], v207 offset:18432
	ds_read_b128 v[230:233], v207 offset:19456
	ds_read_b128 v[234:237], v207 offset:20480
	ds_read_b128 v[238:241], v207 offset:21504
	ds_read_b128 v[242:245], v207 offset:22528
	ds_read_b128 v[246:249], v207 offset:23552
	global_load_lds_dwordx4 v[196:197], off
	s_add_i32 m0, s54, 0x2000
	s_add_u32 s54, s50, 0x20000
	v_lshl_add_u64 v[198:199], s[50:51], 0, v[166:167]
	s_addc_u32 s55, s51, 0
	s_add_i32 s84, s75, s58
	global_load_lds_dwordx4 v[198:199], off
	v_lshl_add_u64 v[202:203], s[54:55], 0, v[168:169]
	s_mov_b32 m0, s84
	v_mov_b32_e32 v201, v171
	global_load_lds_dwordx4 v[202:203], off
	v_lshl_add_u64 v[202:203], s[54:55], 0, v[166:167]
	s_add_i32 m0, s84, 0x2000
	s_nop 0
	global_load_lds_dwordx4 v[202:203], off
	s_mov_b32 m0, s61
	v_lshl_add_u64 v[202:203], s[52:53], 0, v[170:171]
	global_load_lds_dwordx4 v170, s[52:53]
	s_mov_b32 m0, s62
	s_nop 0
	global_load_lds_dwordx4 v200, s[52:53]
	s_waitcnt vmcnt(8)
	s_waitcnt lgkmcnt(0)
	v_lshl_add_u64 v[200:201], s[52:53], 0, v[200:201]
	s_barrier
	s_setprio 1
	s_waitcnt lgkmcnt(0)
	v_mfma_f32_16x16x128_f8f6f4 v[94:97], v[18:25], v[218:225], 0
	v_mfma_f32_16x16x128_f8f6f4 v[86:89], v[26:33], v[218:225], 0
	v_mfma_f32_16x16x128_f8f6f4 v[78:81], v[18:25], v[226:233], 0
	v_mfma_f32_16x16x128_f8f6f4 v[70:73], v[26:33], v[226:233], 0
	v_mfma_f32_16x16x128_f8f6f4 v[62:65], v[18:25], v[234:241], 0
	v_mfma_f32_16x16x128_f8f6f4 v[54:57], v[26:33], v[234:241], 0
	v_mfma_f32_16x16x128_f8f6f4 v[46:49], v[18:25], v[242:249], 0
	v_mfma_f32_16x16x128_f8f6f4 v[38:41], v[26:33], v[242:249], 0
	s_setprio 0
	s_setprio 1
	v_mfma_f32_16x16x128_f8f6f4 v[90:93], v[2:9], v[218:225], 0
	v_mfma_f32_16x16x128_f8f6f4 v[82:85], v[10:17], v[218:225], 0
	v_mfma_f32_16x16x128_f8f6f4 v[74:77], v[2:9], v[226:233], 0
	v_mfma_f32_16x16x128_f8f6f4 v[66:69], v[10:17], v[226:233], 0
	v_mfma_f32_16x16x128_f8f6f4 v[58:61], v[2:9], v[234:241], 0
	v_mfma_f32_16x16x128_f8f6f4 v[50:53], v[10:17], v[234:241], 0
	v_mfma_f32_16x16x128_f8f6f4 v[42:45], v[2:9], v[242:249], 0
	v_mfma_f32_16x16x128_f8f6f4 v[34:37], v[10:17], v[242:249], 0
	s_setprio 0
	s_barrier
; #define PG8_STAGE(bufoff, gbase, voff) do { _Pragma("unroll") for (int _i = 0; _i < 2; ++_i) \
;         __builtin_amdgcn_global_load_lds((const unsigned*)((const char*)(gbase) + (voff)[_i]), (PG8_LAS unsigned*)(lds + (bufoff) + ldsw + _i * 8192), 16, 0, 0); } while (0)
; #define PG8_STAGE_A(bufoff, kbase, h, gv) do { if constexpr (GATHER) { PG8_STAGE(bufoff, kbase, (gv)[h]); } else { PG8_STAGE(bufoff, (kbase) + (h) * hstep, voffA); } } while (0)
; #define PG8_WAIT_V(n) asm volatile("s_waitcnt vmcnt(" #n ")" ::: "memory")
; template <class Epi, class Sched, bool ALIGN_EPI = false, bool SP2 = false, bool FP8 = false, bool GATHER = false>
; __device__ __forceinline__ void gemm_phase(PG8_LAS unsigned char* lds, const Gemm g, const Sched& S, const Epi& E) {
;     ...
;         for (int t = 0; t < nt; t += 2) {
;             const bool last = (t == nt - 2);
;             const char* a1 = cA + (size_t)(t + 1) * kstep;
;             const char* a2 = last ? nA : cA + (size_t)(t + 2) * kstep; const char* b2 = last ? nB : cB + (size_t)(t + 2) * kstep;
;             const char* a3 = a2 + kstep; const char* b3 = b2 + kstep;
;             if (last && has_next) S.a_ready(nxt);
;             if (last) E.pre(cur, wid, lane);
;             if constexpr (GATHER) { if (t == nt - 4 && has_next) { _Pragma("unroll") for (int h_ = 0; h_ < 2; ++h_) _Pragma("unroll") for (int i_ = 0; i_ < 2; ++i_)
;                 asm volatile("global_load_dword %0, %1, off" : "+v"(graw[h_][i_]) : "v"(S.rowtok + (nxt.pm * BM + h_ * HALF + gR[i_])) : "memory"); } }
;             unsigned gsel[2][2];
;             if constexpr (GATHER) { _Pragma("unroll") for (int h_ = 0; h_ < 2; ++h_) _Pragma("unroll") for (int i_ = 0; i_ < 2; ++i_) { if (last && has_next) gnxt[h_][i_] = graw[h_][i_] * (unsigned)(K * 2) + gC[i_]; gsel[h_][i_] = (last && has_next) ? gnxt[h_][i_] : gcur[h_][i_]; } }
;     ...
;             PG8_LDB(B0, 1, 0); PG8_LDB(B1, 1, 1); PG8_SCHED; PG8_LDA(At, 1, 0); PG8_STAGE_A(PG8_SA(0, 1), a2, 1, gsel);
;             PG8_WAIT_V(8); PG8_WAIT_L(0); PG8_BAR; PG8_MMA(0, 0, At, B0); PG8_MMA(0, 1, At, B1); PG8_BAR; PG8_SCHED;
;             PG8_LDA(At, 1, 1); PG8_STAGE(PG8_SB(1, 0), b3, voffB); PG8_STAGE(PG8_SB(1, 1), b3 + hstep, voffB); PG8_STAGE_A(PG8_SA(1, 0), a3, 0, gsel);
;             PG8_WAIT_V(8); PG8_WAIT_L(0); PG8_BAR; PG8_MMA(1, 0, At, B0); PG8_MMA(1, 1, At, B1); PG8_BAR; PG8_SCHED;
	s_add_i32 s54, 0, 0x18000
	s_add_i32 s55, 0, 0x1c000
	v_add_u32_e32 v14, s54, v206
	v_add_u32_e32 v30, s55, v206
	ds_read_b128 v[2:5], v14
	ds_read_b128 v[6:9], v14 offset:1024
	ds_read_b128 v[10:13], v14 offset:2048
	ds_read_b128 v[14:17], v14 offset:3072
	ds_read_b128 v[18:21], v30
	ds_read_b128 v[22:25], v30 offset:1024
	ds_read_b128 v[26:29], v30 offset:2048
	ds_read_b128 v[30:33], v30 offset:3072
	s_mov_b32 m0, s63
	ds_read_b128 v[218:221], v207 offset:32768
	ds_read_b128 v[222:225], v207 offset:33792
	ds_read_b128 v[226:229], v207 offset:34816
	ds_read_b128 v[230:233], v207 offset:35840
	ds_read_b128 v[234:237], v207 offset:36864
	ds_read_b128 v[238:241], v207 offset:37888
	ds_read_b128 v[242:245], v207 offset:38912
	ds_read_b128 v[246:249], v207 offset:39936
	global_load_lds_dwordx4 v177, s[52:53]
	s_mov_b32 m0, s65
	s_nop 0
	global_load_lds_dwordx4 v179, s[52:53]
	s_waitcnt vmcnt(8)
	s_waitcnt lgkmcnt(0)
	s_barrier
	s_setprio 1
	s_waitcnt lgkmcnt(0)
	v_mfma_f32_16x16x128_f8f6f4 v[158:161], v[2:9], v[218:225], v[158:161]
	v_mfma_f32_16x16x128_f8f6f4 v[150:153], v[10:17], v[218:225], v[150:153]
	v_mfma_f32_16x16x128_f8f6f4 v[142:145], v[2:9], v[226:233], v[142:145]
	v_mfma_f32_16x16x128_f8f6f4 v[134:137], v[10:17], v[226:233], v[134:137]
	v_mfma_f32_16x16x128_f8f6f4 v[126:129], v[2:9], v[234:241], v[126:129]
	v_mfma_f32_16x16x128_f8f6f4 v[118:121], v[10:17], v[234:241], v[118:121]
	v_mfma_f32_16x16x128_f8f6f4 v[110:113], v[2:9], v[242:249], v[110:113]
	v_mfma_f32_16x16x128_f8f6f4 v[102:105], v[10:17], v[242:249], v[102:105]
	s_setprio 0
	s_setprio 1
	v_mfma_f32_16x16x128_f8f6f4 v[154:157], v[18:25], v[218:225], v[154:157]
	v_mfma_f32_16x16x128_f8f6f4 v[146:149], v[26:33], v[218:225], v[146:149]
	v_mfma_f32_16x16x128_f8f6f4 v[138:141], v[18:25], v[226:233], v[138:141]
	v_mfma_f32_16x16x128_f8f6f4 v[130:133], v[26:33], v[226:233], v[130:133]
	v_mfma_f32_16x16x128_f8f6f4 v[122:125], v[18:25], v[234:241], v[122:125]
	v_mfma_f32_16x16x128_f8f6f4 v[114:117], v[26:33], v[234:241], v[114:117]
	v_mfma_f32_16x16x128_f8f6f4 v[106:109], v[18:25], v[242:249], v[106:109]
	v_mfma_f32_16x16x128_f8f6f4 v[98:101], v[26:33], v[242:249], v[98:101]
	s_setprio 0
	s_barrier
	s_add_i32 s52, s54, s58
	v_lshl_add_u64 v[196:197], v[196:197], 0, s[16:17]
	s_mov_b32 m0, s52
	ds_read_b128 v[218:221], v207 offset:49152
	ds_read_b128 v[222:225], v207 offset:50176
	ds_read_b128 v[226:229], v207 offset:51200
	ds_read_b128 v[230:233], v207 offset:52224
	ds_read_b128 v[234:237], v207 offset:53248
	ds_read_b128 v[238:241], v207 offset:54272
	ds_read_b128 v[242:245], v207 offset:55296
	ds_read_b128 v[246:249], v207 offset:56320
	global_load_lds_dwordx4 v[196:197], off
	s_add_i32 m0, s52, 0x2000
	s_add_u32 s50, s50, 0x20080
	v_lshl_add_u64 v[196:197], v[198:199], 0, s[16:17]
	s_addc_u32 s51, s51, 0
	s_add_i32 s52, s55, s58
	global_load_lds_dwordx4 v[196:197], off
	v_lshl_add_u64 v[196:197], s[50:51], 0, v[168:169]
	s_mov_b32 m0, s52
	s_nop 0
	global_load_lds_dwordx4 v[196:197], off
	v_lshl_add_u64 v[196:197], s[50:51], 0, v[166:167]
	s_add_i32 m0, s52, 0x2000
	s_nop 0
	global_load_lds_dwordx4 v[196:197], off
	v_lshl_add_u64 v[196:197], v[202:203], 0, s[16:17]
	s_mov_b32 m0, s68
	s_nop 0
	global_load_lds_dwordx4 v[196:197], off
	v_lshl_add_u64 v[196:197], v[200:201], 0, s[16:17]
	s_mov_b32 m0, s69
	s_nop 0
	global_load_lds_dwordx4 v[196:197], off
	s_waitcnt vmcnt(8)
	s_waitcnt lgkmcnt(0)
	s_barrier
	s_setprio 1
	s_waitcnt lgkmcnt(0)
	v_mfma_f32_16x16x128_f8f6f4 v[94:97], v[2:9], v[218:225], v[94:97]
	v_mfma_f32_16x16x128_f8f6f4 v[86:89], v[10:17], v[218:225], v[86:89]
	v_mfma_f32_16x16x128_f8f6f4 v[78:81], v[2:9], v[226:233], v[78:81]
	v_mfma_f32_16x16x128_f8f6f4 v[70:73], v[10:17], v[226:233], v[70:73]
	v_mfma_f32_16x16x128_f8f6f4 v[62:65], v[2:9], v[234:241], v[62:65]
	v_mfma_f32_16x16x128_f8f6f4 v[54:57], v[10:17], v[234:241], v[54:57]
	v_mfma_f32_16x16x128_f8f6f4 v[46:49], v[2:9], v[242:249], v[46:49]
	v_mfma_f32_16x16x128_f8f6f4 v[38:41], v[10:17], v[242:249], v[38:41]
	s_setprio 0
	s_setprio 1
	v_mfma_f32_16x16x128_f8f6f4 v[90:93], v[18:25], v[218:225], v[90:93]
	v_mfma_f32_16x16x128_f8f6f4 v[82:85], v[26:33], v[218:225], v[82:85]
	v_mfma_f32_16x16x128_f8f6f4 v[74:77], v[18:25], v[226:233], v[74:77]
	v_mfma_f32_16x16x128_f8f6f4 v[66:69], v[26:33], v[226:233], v[66:69]
	v_mfma_f32_16x16x128_f8f6f4 v[58:61], v[18:25], v[234:241], v[58:61]
	v_mfma_f32_16x16x128_f8f6f4 v[50:53], v[26:33], v[234:241], v[50:53]
	v_mfma_f32_16x16x128_f8f6f4 v[42:45], v[18:25], v[242:249], v[42:45]
	v_mfma_f32_16x16x128_f8f6f4 v[34:37], v[26:33], v[242:249], v[34:37]
	s_setprio 0
	s_add_i32 s83, s83, 2
	s_add_u32 s46, s46, 0x100
	s_addc_u32 s47, s47, 0
	s_cmp_gt_u32 s83, 5
	s_cbranch_scc1 .Lrot1781_exit
	s_cmpk_eq_i32 s46, 0x300
	s_cselect_b64 s[54:55], -1, 0
	s_and_b64 s[50:51], s[54:55], s[22:23]
	s_andn2_b64 vcc, exec, s[50:51]
	s_cbranch_vccz .Lrot1781_rare0
	s_cmpk_lg_i32 s46, 0x200
	s_cselect_b64 s[50:51], -1, 0
	s_or_b64 s[50:51], s[48:49], s[50:51]
	s_and_b64 vcc, exec, s[50:51]
	s_cbranch_vccnz .Lrot1781_head

; #define PG8_STAGE(bufoff, gbase, voff) do { _Pragma("unroll") for (int _i = 0; _i < 2; ++_i) \
;         __builtin_amdgcn_global_load_lds((const unsigned*)((const char*)(gbase) + (voff)[_i]), (PG8_LAS unsigned*)(lds + (bufoff) + ldsw + _i * 8192), 16, 0, 0); } while (0)
; #define PG8_STAGE_A(bufoff, kbase, h, gv) do { if constexpr (GATHER) { PG8_STAGE(bufoff, kbase, (gv)[h]); } else { PG8_STAGE(bufoff, (kbase) + (h) * hstep, voffA); } } while (0)
; #define PG8_WAIT_V(n) asm volatile("s_waitcnt vmcnt(" #n ")" ::: "memory")
; #define PG8_WAIT_L(n) asm volatile("s_waitcnt lgkmcnt(" #n ")" ::: "memory")
; #define PG8_BAR __builtin_amdgcn_s_barrier()
; template <class Epi, class Sched, bool ALIGN_EPI = false, bool SP2 = false, bool FP8 = false, bool GATHER = false>
; __device__ __forceinline__ void gemm_phase(PG8_LAS unsigned char* lds, const Gemm g, const Sched& S, const Epi& E) {
;     ...
;             const char* a2 = last ? nA : cA + (size_t)(t + 2) * kstep; const char* b2 = last ? nB : cB + (size_t)(t + 2) * kstep;
;             const char* a3 = a2 + kstep; const char* b3 = b2 + kstep;
;             if (last && has_next) S.a_ready(nxt);
;             if (last) E.pre(cur, wid, lane);
;             if constexpr (GATHER) { if (t == nt - 4 && has_next) { _Pragma("unroll") for (int h_ = 0; h_ < 2; ++h_) _Pragma("unroll") for (int i_ = 0; i_ < 2; ++i_)
;                 asm volatile("global_load_dword %0, %1, off" : "+v"(graw[h_][i_]) : "v"(S.rowtok + (nxt.pm * BM + h_ * HALF + gR[i_])) : "memory"); } }
;             unsigned gsel[2][2];
;             if constexpr (GATHER) { _Pragma("unroll") for (int h_ = 0; h_ < 2; ++h_) _Pragma("unroll") for (int i_ = 0; i_ < 2; ++i_) { if (last && has_next) gnxt[h_][i_] = graw[h_][i_] * (unsigned)(K * 2) + gC[i_]; gsel[h_][i_] = (last && has_next) ? gnxt[h_][i_] : gcur[h_][i_]; } }
;             if constexpr (SP2) {
;             PG8_LDB(B0, 0, 0); PG8_LDB(B1, 0, 1); PG8_SCHED; PG8_LDA(At, 0, 0); PG8_STAGE_A(PG8_SA(1, 1), a1, 1, gcur);
;             PG8_WAIT_V(8); PG8_WAIT_L(0); PG8_BAR; PG8_MMA(0, 0, At, B0); PG8_MMA(0, 1, At, B1); PG8_BAR; PG8_SCHED;
;             PG8_LDA(At, 0, 1); PG8_STAGE(PG8_SB(0, 0), b2, voffB); PG8_STAGE(PG8_SB(0, 1), b2 + hstep, voffB); PG8_STAGE_A(PG8_SA(0, 0), a2, 0, gsel);
;             PG8_WAIT_V(8); PG8_WAIT_L(0); PG8_BAR; PG8_MMA(1, 0, At, B0); PG8_MMA(1, 1, At, B1); PG8_BAR; PG8_SCHED;
.LBB0_1781:
	s_add_u32 s50, s6, s46
	s_addc_u32 s51, s7, s47
	s_add_u32 s52, s50, 0x19200100
	s_addc_u32 s53, s51, 0
	s_and_b64 s[50:51], s[54:55], exec
	s_cselect_b32 s53, s9, s53
	s_cselect_b32 s52, s8, s52
	s_add_u32 s84, s20, s46
	s_addc_u32 s85, s82, s47
	s_and_b64 s[50:51], s[54:55], exec
	s_cselect_b32 s51, s35, s85
	s_cselect_b32 s50, s34, s84
	v_lshl_add_u32 v2, v213, 10, v1
	s_and_b64 vcc, s[44:45], s[54:55]
	v_cndmask_b32_e32 v209, v209, v2, vcc
	v_cndmask_b32_e32 v170, v217, v2, vcc
	v_lshl_add_u32 v2, v214, 10, v204
	v_cndmask_b32_e32 v210, v210, v2, vcc
	v_cndmask_b32_e32 v200, v180, v2, vcc
	v_add_u32_e32 v2, s74, v206
	v_add_u32_e32 v14, s75, v206
	ds_read_b128 v[18:21], v2
	ds_read_b128 v[22:25], v2 offset:1024
	ds_read_b128 v[26:29], v2 offset:2048
	ds_read_b128 v[30:33], v2 offset:3072
	ds_read_b128 v[2:5], v14
	ds_read_b128 v[6:9], v14 offset:1024
	ds_read_b128 v[10:13], v14 offset:2048
	ds_read_b128 v[14:17], v14 offset:3072
	v_lshl_add_u32 v177, v215, 10, v1
	v_lshl_add_u32 v179, v216, 10, v204
	v_cndmask_b32_e32 v211, v211, v177, vcc
	v_cndmask_b32_e32 v212, v212, v179, vcc
	v_cndmask_b32_e32 v177, v178, v177, vcc
	v_cndmask_b32_e32 v179, v176, v179, vcc
	v_lshl_add_u64 v[196:197], v[194:195], 0, s[46:47]
	s_add_i32 m0, s61, 0xc000
	ds_read_b128 v[218:221], v207
	ds_read_b128 v[222:225], v207 offset:1024
	ds_read_b128 v[226:229], v207 offset:2048
	ds_read_b128 v[230:233], v207 offset:3072
	ds_read_b128 v[234:237], v207 offset:4096
	ds_read_b128 v[238:241], v207 offset:5120
	ds_read_b128 v[242:245], v207 offset:6144
	ds_read_b128 v[246:249], v207 offset:7168
	global_load_lds_dwordx4 v[196:197], off
	v_lshl_add_u64 v[196:197], v[192:193], 0, s[46:47]
	s_add_i32 m0, s61, 0xe000
	s_nop 0
	global_load_lds_dwordx4 v[196:197], off
	s_waitcnt vmcnt(8)
	s_waitcnt lgkmcnt(0)
	s_barrier
	s_setprio 1
	s_waitcnt lgkmcnt(0)
	v_mfma_f32_16x16x128_f8f6f4 v[158:161], v[18:25], v[218:225], v[158:161]
	v_mfma_f32_16x16x128_f8f6f4 v[150:153], v[26:33], v[218:225], v[150:153]
	v_mfma_f32_16x16x128_f8f6f4 v[142:145], v[18:25], v[226:233], v[142:145]
	v_mfma_f32_16x16x128_f8f6f4 v[134:137], v[26:33], v[226:233], v[134:137]
	v_mfma_f32_16x16x128_f8f6f4 v[126:129], v[18:25], v[234:241], v[126:129]
	v_mfma_f32_16x16x128_f8f6f4 v[118:121], v[26:33], v[234:241], v[118:121]
	v_mfma_f32_16x16x128_f8f6f4 v[110:113], v[18:25], v[242:249], v[110:113]
	v_mfma_f32_16x16x128_f8f6f4 v[102:105], v[26:33], v[242:249], v[102:105]
	s_setprio 0
	s_setprio 1
	v_mfma_f32_16x16x128_f8f6f4 v[154:157], v[2:9], v[218:225], v[154:157]
	v_mfma_f32_16x16x128_f8f6f4 v[146:149], v[10:17], v[218:225], v[146:149]
	v_mfma_f32_16x16x128_f8f6f4 v[138:141], v[2:9], v[226:233], v[138:141]
	v_mfma_f32_16x16x128_f8f6f4 v[130:133], v[10:17], v[226:233], v[130:133]
	v_mfma_f32_16x16x128_f8f6f4 v[122:125], v[2:9], v[234:241], v[122:125]
	v_mfma_f32_16x16x128_f8f6f4 v[114:117], v[10:17], v[234:241], v[114:117]
	v_mfma_f32_16x16x128_f8f6f4 v[106:109], v[2:9], v[242:249], v[106:109]
	v_mfma_f32_16x16x128_f8f6f4 v[98:101], v[10:17], v[242:249], v[98:101]
	s_setprio 0
	s_barrier
	s_add_i32 s54, s74, s58
	v_lshl_add_u64 v[196:197], s[50:51], 0, v[168:169]
	s_mov_b32 m0, s54
	ds_read_b128 v[218:221], v207 offset:16384
	ds_read_b128 v[222:225], v207 offset:17408
	ds_read_b128 v[226:229], v207 offset:18432
	ds_read_b128 v[230:233], v207 offset:19456
	ds_read_b128 v[234:237], v207 offset:20480
	ds_read_b128 v[238:241], v207 offset:21504
	ds_read_b128 v[242:245], v207 offset:22528
	ds_read_b128 v[246:249], v207 offset:23552
	global_load_lds_dwordx4 v[196:197], off
	s_add_i32 m0, s54, 0x2000
	s_add_u32 s54, s50, 0x20000
	v_lshl_add_u64 v[198:199], s[50:51], 0, v[166:167]
	s_addc_u32 s55, s51, 0
	s_add_i32 s84, s75, s58
	global_load_lds_dwordx4 v[198:199], off
	v_lshl_add_u64 v[202:203], s[54:55], 0, v[168:169]
	s_mov_b32 m0, s84
	v_mov_b32_e32 v201, v171
	global_load_lds_dwordx4 v[202:203], off
	v_lshl_add_u64 v[202:203], s[54:55], 0, v[166:167]
	s_add_i32 m0, s84, 0x2000
	s_nop 0
	global_load_lds_dwordx4 v[202:203], off
	s_mov_b32 m0, s61
	v_lshl_add_u64 v[202:203], s[52:53], 0, v[170:171]
	global_load_lds_dwordx4 v170, s[52:53]
	s_mov_b32 m0, s62
	s_nop 0
	global_load_lds_dwordx4 v200, s[52:53]
	s_waitcnt vmcnt(8)
	s_waitcnt lgkmcnt(0)
	v_lshl_add_u64 v[200:201], s[52:53], 0, v[200:201]
	s_barrier
	s_setprio 1
	s_waitcnt lgkmcnt(0)
	v_mfma_f32_16x16x128_f8f6f4 v[94:97], v[18:25], v[218:225], v[94:97]
	v_mfma_f32_16x16x128_f8f6f4 v[86:89], v[26:33], v[218:225], v[86:89]
	v_mfma_f32_16x16x128_f8f6f4 v[78:81], v[18:25], v[226:233], v[78:81]
	v_mfma_f32_16x16x128_f8f6f4 v[70:73], v[26:33], v[226:233], v[70:73]
	v_mfma_f32_16x16x128_f8f6f4 v[62:65], v[18:25], v[234:241], v[62:65]
	v_mfma_f32_16x16x128_f8f6f4 v[54:57], v[26:33], v[234:241], v[54:57]
	v_mfma_f32_16x16x128_f8f6f4 v[46:49], v[18:25], v[242:249], v[46:49]
	v_mfma_f32_16x16x128_f8f6f4 v[38:41], v[26:33], v[242:249], v[38:41]
	s_setprio 0
	s_setprio 1
	v_mfma_f32_16x16x128_f8f6f4 v[90:93], v[2:9], v[218:225], v[90:93]
	v_mfma_f32_16x16x128_f8f6f4 v[82:85], v[10:17], v[218:225], v[82:85]
	v_mfma_f32_16x16x128_f8f6f4 v[74:77], v[2:9], v[226:233], v[74:77]
	v_mfma_f32_16x16x128_f8f6f4 v[66:69], v[10:17], v[226:233], v[66:69]
	v_mfma_f32_16x16x128_f8f6f4 v[58:61], v[2:9], v[234:241], v[58:61]
	v_mfma_f32_16x16x128_f8f6f4 v[50:53], v[10:17], v[234:241], v[50:53]
	v_mfma_f32_16x16x128_f8f6f4 v[42:45], v[2:9], v[242:249], v[42:45]
	v_mfma_f32_16x16x128_f8f6f4 v[34:37], v[10:17], v[242:249], v[34:37]
	s_setprio 0
	s_barrier
; #define PG8_STAGE(bufoff, gbase, voff) do { _Pragma("unroll") for (int _i = 0; _i < 2; ++_i) \
;         __builtin_amdgcn_global_load_lds((const unsigned*)((const char*)(gbase) + (voff)[_i]), (PG8_LAS unsigned*)(lds + (bufoff) + ldsw + _i * 8192), 16, 0, 0); } while (0)
; #define PG8_STAGE_A(bufoff, kbase, h, gv) do { if constexpr (GATHER) { PG8_STAGE(bufoff, kbase, (gv)[h]); } else { PG8_STAGE(bufoff, (kbase) + (h) * hstep, voffA); } } while (0)
; #define PG8_WAIT_V(n) asm volatile("s_waitcnt vmcnt(" #n ")" ::: "memory")
; #define PG8_WAIT_L(n) asm volatile("s_waitcnt lgkmcnt(" #n ")" ::: "memory")
; #define PG8_BAR __builtin_amdgcn_s_barrier()
; #define PG8_SCHED __builtin_amdgcn_sched_barrier(0)
; template <class Epi, class Sched, bool ALIGN_EPI = false, bool SP2 = false, bool FP8 = false, bool GATHER = false>
; __device__ __forceinline__ void gemm_phase(PG8_LAS unsigned char* lds, const Gemm g, const Sched& S, const Epi& E) {
;     ...
;             PG8_LDB(B0, 1, 0); PG8_LDB(B1, 1, 1); PG8_SCHED; PG8_LDA(At, 1, 0); PG8_STAGE_A(PG8_SA(0, 1), a2, 1, gsel);
;             PG8_WAIT_V(8); PG8_WAIT_L(0); PG8_BAR; PG8_MMA(0, 0, At, B0); PG8_MMA(0, 1, At, B1); PG8_BAR; PG8_SCHED;
;             PG8_LDA(At, 1, 1); PG8_STAGE(PG8_SB(1, 0), b3, voffB); PG8_STAGE(PG8_SB(1, 1), b3 + hstep, voffB); PG8_STAGE_A(PG8_SA(1, 0), a3, 0, gsel);
;             PG8_WAIT_V(8); PG8_WAIT_L(0); PG8_BAR; PG8_MMA(1, 0, At, B0); PG8_MMA(1, 1, At, B1); PG8_BAR; PG8_SCHED;
;     __device__ __forceinline__ void pre(const pg8::Unit& u, int wid, int lane) const {
;         if (wid == 0) lds_dma16(bias + (size_t)(u.pn >> 8) * 2048 + (lane >> 5) * 1024 + (u.pn & 255) * 128 + (lane & 31) * 4, (unsigned)(uintptr_t)(lds + LDS_EPI)); }
	s_add_i32 s54, 0, 0x18000
	s_add_i32 s55, 0, 0x1c000
	v_add_u32_e32 v14, s54, v206
	v_add_u32_e32 v30, s55, v206
	ds_read_b128 v[2:5], v14
	ds_read_b128 v[6:9], v14 offset:1024
	ds_read_b128 v[10:13], v14 offset:2048
	ds_read_b128 v[14:17], v14 offset:3072
	ds_read_b128 v[18:21], v30
	ds_read_b128 v[22:25], v30 offset:1024
	ds_read_b128 v[26:29], v30 offset:2048
	ds_read_b128 v[30:33], v30 offset:3072
	s_mov_b32 m0, s63
	ds_read_b128 v[218:221], v207 offset:32768
	ds_read_b128 v[222:225], v207 offset:33792
	ds_read_b128 v[226:229], v207 offset:34816
	ds_read_b128 v[230:233], v207 offset:35840
	ds_read_b128 v[234:237], v207 offset:36864
	ds_read_b128 v[238:241], v207 offset:37888
	ds_read_b128 v[242:245], v207 offset:38912
	ds_read_b128 v[246:249], v207 offset:39936
	global_load_lds_dwordx4 v177, s[52:53]
	s_mov_b32 m0, s65
	s_nop 0
	global_load_lds_dwordx4 v179, s[52:53]
	s_waitcnt vmcnt(8)
	s_waitcnt lgkmcnt(0)
	s_barrier
	s_setprio 1
	s_waitcnt lgkmcnt(0)
	v_mfma_f32_16x16x128_f8f6f4 v[158:161], v[2:9], v[218:225], v[158:161]
	v_mfma_f32_16x16x128_f8f6f4 v[150:153], v[10:17], v[218:225], v[150:153]
	v_mfma_f32_16x16x128_f8f6f4 v[142:145], v[2:9], v[226:233], v[142:145]
	v_mfma_f32_16x16x128_f8f6f4 v[134:137], v[10:17], v[226:233], v[134:137]
	v_mfma_f32_16x16x128_f8f6f4 v[126:129], v[2:9], v[234:241], v[126:129]
	v_mfma_f32_16x16x128_f8f6f4 v[118:121], v[10:17], v[234:241], v[118:121]
	v_mfma_f32_16x16x128_f8f6f4 v[110:113], v[2:9], v[242:249], v[110:113]
	v_mfma_f32_16x16x128_f8f6f4 v[102:105], v[10:17], v[242:249], v[102:105]
	s_setprio 0
	s_setprio 1
	v_mfma_f32_16x16x128_f8f6f4 v[154:157], v[18:25], v[218:225], v[154:157]
	v_mfma_f32_16x16x128_f8f6f4 v[146:149], v[26:33], v[218:225], v[146:149]
	v_mfma_f32_16x16x128_f8f6f4 v[138:141], v[18:25], v[226:233], v[138:141]
	v_mfma_f32_16x16x128_f8f6f4 v[130:133], v[26:33], v[226:233], v[130:133]
	v_mfma_f32_16x16x128_f8f6f4 v[122:125], v[18:25], v[234:241], v[122:125]
	v_mfma_f32_16x16x128_f8f6f4 v[114:117], v[26:33], v[234:241], v[114:117]
	v_mfma_f32_16x16x128_f8f6f4 v[106:109], v[18:25], v[242:249], v[106:109]
	v_mfma_f32_16x16x128_f8f6f4 v[98:101], v[26:33], v[242:249], v[98:101]
	s_setprio 0
	s_barrier
	s_add_i32 s52, s54, s58
	v_lshl_add_u64 v[196:197], v[196:197], 0, s[16:17]
	s_mov_b32 m0, s52
	ds_read_b128 v[218:221], v207 offset:49152
	ds_read_b128 v[222:225], v207 offset:50176
	ds_read_b128 v[226:229], v207 offset:51200
	ds_read_b128 v[230:233], v207 offset:52224
	ds_read_b128 v[234:237], v207 offset:53248
	ds_read_b128 v[238:241], v207 offset:54272
	ds_read_b128 v[242:245], v207 offset:55296
	ds_read_b128 v[246:249], v207 offset:56320
	global_load_lds_dwordx4 v[196:197], off
	s_add_i32 m0, s52, 0x2000
	s_add_u32 s50, s50, 0x20080
	v_lshl_add_u64 v[196:197], v[198:199], 0, s[16:17]
	s_addc_u32 s51, s51, 0
	s_add_i32 s52, s55, s58
	global_load_lds_dwordx4 v[196:197], off
	v_lshl_add_u64 v[196:197], s[50:51], 0, v[168:169]
	s_mov_b32 m0, s52
	s_nop 0
	global_load_lds_dwordx4 v[196:197], off
	v_lshl_add_u64 v[196:197], s[50:51], 0, v[166:167]
	s_add_i32 m0, s52, 0x2000
	s_nop 0
	global_load_lds_dwordx4 v[196:197], off
	v_lshl_add_u64 v[196:197], v[202:203], 0, s[16:17]
	s_mov_b32 m0, s68
	s_nop 0
	global_load_lds_dwordx4 v[196:197], off
	v_lshl_add_u64 v[196:197], v[200:201], 0, s[16:17]
	s_mov_b32 m0, s69
	s_nop 0
	global_load_lds_dwordx4 v[196:197], off
	s_waitcnt vmcnt(8)
	s_waitcnt lgkmcnt(0)
	s_barrier
	s_setprio 1
	s_waitcnt lgkmcnt(0)
	v_mfma_f32_16x16x128_f8f6f4 v[94:97], v[2:9], v[218:225], v[94:97]
	v_mfma_f32_16x16x128_f8f6f4 v[86:89], v[10:17], v[218:225], v[86:89]
	v_mfma_f32_16x16x128_f8f6f4 v[78:81], v[2:9], v[226:233], v[78:81]
	v_mfma_f32_16x16x128_f8f6f4 v[70:73], v[10:17], v[226:233], v[70:73]
	v_mfma_f32_16x16x128_f8f6f4 v[62:65], v[2:9], v[234:241], v[62:65]
	v_mfma_f32_16x16x128_f8f6f4 v[54:57], v[10:17], v[234:241], v[54:57]
	v_mfma_f32_16x16x128_f8f6f4 v[46:49], v[2:9], v[242:249], v[46:49]
	v_mfma_f32_16x16x128_f8f6f4 v[38:41], v[10:17], v[242:249], v[38:41]
	s_setprio 0
	s_setprio 1
	v_mfma_f32_16x16x128_f8f6f4 v[90:93], v[18:25], v[218:225], v[90:93]
	v_mfma_f32_16x16x128_f8f6f4 v[82:85], v[26:33], v[218:225], v[82:85]
	v_mfma_f32_16x16x128_f8f6f4 v[74:77], v[18:25], v[226:233], v[74:77]
	v_mfma_f32_16x16x128_f8f6f4 v[66:69], v[26:33], v[226:233], v[66:69]
	v_mfma_f32_16x16x128_f8f6f4 v[58:61], v[18:25], v[234:241], v[58:61]
	v_mfma_f32_16x16x128_f8f6f4 v[50:53], v[26:33], v[234:241], v[50:53]
	v_mfma_f32_16x16x128_f8f6f4 v[42:45], v[18:25], v[242:249], v[42:45]
	v_mfma_f32_16x16x128_f8f6f4 v[34:37], v[26:33], v[242:249], v[34:37]
	s_setprio 0
	s_add_i32 s83, s83, 2
	s_add_u32 s46, s46, 0x100
	s_addc_u32 s47, s47, 0
	s_cmp_gt_u32 s83, 5
	s_cbranch_scc1 .Lrot1781_exit
	s_cmpk_eq_i32 s46, 0x300
	s_cselect_b64 s[54:55], -1, 0
	s_and_b64 s[50:51], s[54:55], s[22:23]
	s_andn2_b64 vcc, exec, s[50:51]
	s_cbranch_vccz .Lrot1781_rare1
	s_cmpk_lg_i32 s46, 0x200
	s_cselect_b64 s[50:51], -1, 0
	s_or_b64 s[50:51], s[48:49], s[50:51]
	s_and_b64 vcc, exec, s[50:51]
	s_cbranch_vccnz .Lrot1781_head
.Lrot1781_rare1:
	s_barrier
.LBB0_1782:
	s_cmpk_eq_i32 s46, 0x300
	s_cselect_b64 s[54:55], -1, 0
	s_and_b64 s[50:51], s[54:55], s[22:23]
	s_andn2_b64 vcc, exec, s[50:51]
	s_cbranch_vccnz .LBB0_1784
	s_add_i32 s50, 0, 0x20000
	s_mov_b32 s51, m0
	s_mov_b32 m0, s50
	s_nop 0
	global_load_lds_dwordx4 v[182:183], off
	s_mov_b32 m0, s51

; #define PG8_STAGE(bufoff, gbase, voff) do { _Pragma("unroll") for (int _i = 0; _i < 2; ++_i) \
;         __builtin_amdgcn_global_load_lds((const unsigned*)((const char*)(gbase) + (voff)[_i]), (PG8_LAS unsigned*)(lds + (bufoff) + ldsw + _i * 8192), 16, 0, 0); } while (0)
; #define PG8_STAGE_A(bufoff, kbase, h, gv) do { if constexpr (GATHER) { PG8_STAGE(bufoff, kbase, (gv)[h]); } else { PG8_STAGE(bufoff, (kbase) + (h) * hstep, voffA); } } while (0)
; #define PG8_WAIT_V(n) asm volatile("s_waitcnt vmcnt(" #n ")" ::: "memory")
; #define PG8_WAIT_L(n) asm volatile("s_waitcnt lgkmcnt(" #n ")" ::: "memory")
; template <class Epi, class Sched, bool ALIGN_EPI = false, bool SP2 = false, bool FP8 = false, bool GATHER = false>
; __device__ __forceinline__ void gemm_phase(PG8_LAS unsigned char* lds, const Gemm g, const Sched& S, const Epi& E) {
;     ...
;             const char* a1 = cA + (size_t)(t + 1) * kstep;
;             const char* a2 = last ? nA : cA + (size_t)(t + 2) * kstep; const char* b2 = last ? nB : cB + (size_t)(t + 2) * kstep;
;             const char* a3 = a2 + kstep; const char* b3 = b2 + kstep;
;             if (last && has_next) S.a_ready(nxt);
;             if (last) E.pre(cur, wid, lane);
;             if constexpr (GATHER) { if (t == nt - 4 && has_next) { _Pragma("unroll") for (int h_ = 0; h_ < 2; ++h_) _Pragma("unroll") for (int i_ = 0; i_ < 2; ++i_)
;                 asm volatile("global_load_dword %0, %1, off" : "+v"(graw[h_][i_]) : "v"(S.rowtok + (nxt.pm * BM + h_ * HALF + gR[i_])) : "memory"); } }
;             unsigned gsel[2][2];
;             if constexpr (GATHER) { _Pragma("unroll") for (int h_ = 0; h_ < 2; ++h_) _Pragma("unroll") for (int i_ = 0; i_ < 2; ++i_) { if (last && has_next) gnxt[h_][i_] = graw[h_][i_] * (unsigned)(K * 2) + gC[i_]; gsel[h_][i_] = (last && has_next) ? gnxt[h_][i_] : gcur[h_][i_]; } }
;             if constexpr (SP2) {
;             PG8_LDB(B0, 0, 0); PG8_LDB(B1, 0, 1); PG8_SCHED; PG8_LDA(At, 0, 0); PG8_STAGE_A(PG8_SA(1, 1), a1, 1, gcur);
;             PG8_WAIT_V(8); PG8_WAIT_L(0); PG8_BAR; PG8_MMA(0, 0, At, B0); PG8_MMA(0, 1, At, B1); PG8_BAR; PG8_SCHED;
;             PG8_LDA(At, 0, 1); PG8_STAGE(PG8_SB(0, 0), b2, voffB); PG8_STAGE(PG8_SB(0, 1), b2 + hstep, voffB); PG8_STAGE_A(PG8_SA(0, 0), a2, 0, gsel);
;             PG8_WAIT_V(8); PG8_WAIT_L(0); PG8_BAR; PG8_MMA(1, 0, At, B0); PG8_MMA(1, 1, At, B1); PG8_BAR; PG8_SCHED;
.Lpeel1856_body:
	v_add_u32_e32 v2, s74, v191
	v_add_u32_e32 v14, s75, v191
	ds_read_b128 v[18:21], v2
	ds_read_b128 v[22:25], v2 offset:1024
	ds_read_b128 v[26:29], v2 offset:2048
	ds_read_b128 v[30:33], v2 offset:3072
	ds_read_b128 v[2:5], v14
	ds_read_b128 v[6:9], v14 offset:1024
	ds_read_b128 v[10:13], v14 offset:2048
	ds_read_b128 v[14:17], v14 offset:3072
	s_add_u32 s48, s44, 0xfffe0080
	s_addc_u32 s49, s45, -1
	s_and_b64 s[46:47], s[46:47], exec
	s_cselect_b32 s49, s78, s49
	s_cselect_b32 s48, s79, s48
	s_cselect_b32 s47, s25, s80
	s_cselect_b32 s46, s24, s35
	v_lshl_add_u64 v[218:219], s[44:45], 0, v[172:173]
	s_add_i32 m0, s58, 0xc000
	ds_read_b128 v[182:185], v192
	ds_read_b128 v[186:189], v192 offset:1024
	ds_read_b128 v[194:197], v192 offset:2048
	ds_read_b128 v[198:201], v192 offset:3072
	ds_read_b128 v[202:205], v192 offset:4096
	ds_read_b128 v[206:209], v192 offset:5120
	ds_read_b128 v[210:213], v192 offset:6144
	ds_read_b128 v[214:217], v192 offset:7168
	global_load_lds_dwordx4 v[218:219], off
	v_lshl_add_u64 v[218:219], s[44:45], 0, v[174:175]
	s_add_i32 m0, s58, 0xe000
	s_nop 0
	global_load_lds_dwordx4 v[218:219], off
	s_waitcnt vmcnt(8)
	s_waitcnt lgkmcnt(0)
	s_barrier
	s_setprio 1
	s_waitcnt lgkmcnt(0)
	v_mfma_f32_16x16x128_f8f6f4 v[158:161], v[18:25], v[182:189], 0
	v_mfma_f32_16x16x128_f8f6f4 v[154:157], v[26:33], v[182:189], 0
	v_mfma_f32_16x16x128_f8f6f4 v[150:153], v[18:25], v[194:201], 0
	v_mfma_f32_16x16x128_f8f6f4 v[146:149], v[26:33], v[194:201], 0
	v_mfma_f32_16x16x128_f8f6f4 v[130:133], v[18:25], v[202:209], 0
	v_mfma_f32_16x16x128_f8f6f4 v[122:125], v[26:33], v[202:209], 0
	v_mfma_f32_16x16x128_f8f6f4 v[118:121], v[18:25], v[210:217], 0
	v_mfma_f32_16x16x128_f8f6f4 v[114:117], v[26:33], v[210:217], 0
	s_setprio 0
	s_setprio 1
	v_mfma_f32_16x16x128_f8f6f4 v[142:145], v[2:9], v[182:189], 0
	v_mfma_f32_16x16x128_f8f6f4 v[138:141], v[10:17], v[182:189], 0
	v_mfma_f32_16x16x128_f8f6f4 v[134:137], v[2:9], v[194:201], 0
	v_mfma_f32_16x16x128_f8f6f4 v[126:129], v[10:17], v[194:201], 0
	v_mfma_f32_16x16x128_f8f6f4 v[110:113], v[2:9], v[202:209], 0
	v_mfma_f32_16x16x128_f8f6f4 v[106:109], v[10:17], v[202:209], 0
	v_mfma_f32_16x16x128_f8f6f4 v[102:105], v[2:9], v[210:217], 0
	v_mfma_f32_16x16x128_f8f6f4 v[98:101], v[10:17], v[210:217], 0
	s_setprio 0
	s_barrier
	s_add_i32 s82, s74, s56
	v_lshl_add_u64 v[182:183], s[46:47], 0, v[166:167]
	s_mov_b32 m0, s82
	ds_read_b128 v[194:197], v192 offset:16384
	ds_read_b128 v[198:201], v192 offset:17408
	ds_read_b128 v[202:205], v192 offset:18432
	ds_read_b128 v[206:209], v192 offset:19456
	ds_read_b128 v[210:213], v192 offset:20480
	ds_read_b128 v[214:217], v192 offset:21504
	ds_read_b128 v[218:221], v192 offset:22528
	ds_read_b128 v[222:225], v192 offset:23552
	global_load_lds_dwordx4 v[182:183], off
	s_add_i32 m0, s82, 0x2000
	s_add_u32 s82, s46, 0x20000
	v_lshl_add_u64 v[184:185], s[46:47], 0, v[162:163]
	s_addc_u32 s83, s47, 0
	s_add_i32 s84, s75, s56
	global_load_lds_dwordx4 v[184:185], off
	v_lshl_add_u64 v[186:187], s[82:83], 0, v[166:167]
	s_mov_b32 m0, s84
	v_lshl_add_u64 v[188:189], s[48:49], 0, v[164:165]
	global_load_lds_dwordx4 v[186:187], off
	v_lshl_add_u64 v[186:187], s[82:83], 0, v[162:163]
	s_add_i32 m0, s84, 0x2000
	s_nop 0
	global_load_lds_dwordx4 v[186:187], off
	v_lshl_add_u64 v[186:187], s[48:49], 0, v[168:169]
	s_mov_b32 m0, s58
	s_nop 0
	global_load_lds_dwordx4 v[186:187], off
	s_mov_b32 m0, s59
	s_nop 0
	global_load_lds_dwordx4 v[188:189], off
	s_waitcnt vmcnt(8)
	s_waitcnt lgkmcnt(0)
	s_barrier
	s_setprio 1
	s_waitcnt lgkmcnt(0)
	v_mfma_f32_16x16x128_f8f6f4 v[94:97], v[18:25], v[194:201], 0
	v_mfma_f32_16x16x128_f8f6f4 v[90:93], v[26:33], v[194:201], 0
	v_mfma_f32_16x16x128_f8f6f4 v[86:89], v[18:25], v[202:209], 0
	v_mfma_f32_16x16x128_f8f6f4 v[82:85], v[26:33], v[202:209], 0
	v_mfma_f32_16x16x128_f8f6f4 v[66:69], v[18:25], v[210:217], 0
	v_mfma_f32_16x16x128_f8f6f4 v[58:61], v[26:33], v[210:217], 0
	v_mfma_f32_16x16x128_f8f6f4 v[54:57], v[18:25], v[218:225], 0
	v_mfma_f32_16x16x128_f8f6f4 v[50:53], v[26:33], v[218:225], 0
	s_setprio 0
	s_setprio 1
	v_mfma_f32_16x16x128_f8f6f4 v[78:81], v[2:9], v[194:201], 0
	v_mfma_f32_16x16x128_f8f6f4 v[74:77], v[10:17], v[194:201], 0
	v_mfma_f32_16x16x128_f8f6f4 v[70:73], v[2:9], v[202:209], 0
	v_mfma_f32_16x16x128_f8f6f4 v[62:65], v[10:17], v[202:209], 0
	v_mfma_f32_16x16x128_f8f6f4 v[46:49], v[2:9], v[210:217], 0
	v_mfma_f32_16x16x128_f8f6f4 v[42:45], v[10:17], v[210:217], 0
	v_mfma_f32_16x16x128_f8f6f4 v[38:41], v[2:9], v[218:225], 0
	v_mfma_f32_16x16x128_f8f6f4 v[34:37], v[10:17], v[218:225], 0
	s_setprio 0
	s_barrier
; #define PG8_STAGE(bufoff, gbase, voff) do { _Pragma("unroll") for (int _i = 0; _i < 2; ++_i) \
;         __builtin_amdgcn_global_load_lds((const unsigned*)((const char*)(gbase) + (voff)[_i]), (PG8_LAS unsigned*)(lds + (bufoff) + ldsw + _i * 8192), 16, 0, 0); } while (0)
; #define PG8_STAGE_A(bufoff, kbase, h, gv) do { if constexpr (GATHER) { PG8_STAGE(bufoff, kbase, (gv)[h]); } else { PG8_STAGE(bufoff, (kbase) + (h) * hstep, voffA); } } while (0)
; #define PG8_WAIT_V(n) asm volatile("s_waitcnt vmcnt(" #n ")" ::: "memory")
; #define PG8_WAIT_L(n) asm volatile("s_waitcnt lgkmcnt(" #n ")" ::: "memory")
; #define PG8_BAR __builtin_amdgcn_s_barrier()
; #define PG8_SCHED __builtin_amdgcn_sched_barrier(0)
; template <class Epi, class Sched, bool ALIGN_EPI = false, bool SP2 = false, bool FP8 = false, bool GATHER = false>
; __device__ __forceinline__ void gemm_phase(PG8_LAS unsigned char* lds, const Gemm g, const Sched& S, const Epi& E) {
;     ...
;         for (int t = 0; t < nt; t += 2) {
;             const bool last = (t == nt - 2);
;             const char* a1 = cA + (size_t)(t + 1) * kstep;
;             const char* a2 = last ? nA : cA + (size_t)(t + 2) * kstep; const char* b2 = last ? nB : cB + (size_t)(t + 2) * kstep;
;             const char* a3 = a2 + kstep; const char* b3 = b2 + kstep;
;     ...
;             PG8_LDB(B0, 1, 0); PG8_LDB(B1, 1, 1); PG8_SCHED; PG8_LDA(At, 1, 0); PG8_STAGE_A(PG8_SA(0, 1), a2, 1, gsel);
;             PG8_WAIT_V(8); PG8_WAIT_L(0); PG8_BAR; PG8_MMA(0, 0, At, B0); PG8_MMA(0, 1, At, B1); PG8_BAR; PG8_SCHED;
;             PG8_LDA(At, 1, 1); PG8_STAGE(PG8_SB(1, 0), b3, voffB); PG8_STAGE(PG8_SB(1, 1), b3 + hstep, voffB); PG8_STAGE_A(PG8_SA(1, 0), a3, 0, gsel);
;             PG8_WAIT_V(8); PG8_WAIT_L(0); PG8_BAR; PG8_MMA(1, 0, At, B0); PG8_MMA(1, 1, At, B1); PG8_BAR; PG8_SCHED;
	s_add_i32 s82, 0, 0x18000
	s_add_i32 s83, 0, 0x1c000
	v_add_u32_e32 v14, s82, v191
	v_add_u32_e32 v30, s83, v191
	ds_read_b128 v[2:5], v14
	ds_read_b128 v[6:9], v14 offset:1024
	ds_read_b128 v[10:13], v14 offset:2048
	ds_read_b128 v[14:17], v14 offset:3072
	ds_read_b128 v[18:21], v30
	ds_read_b128 v[22:25], v30 offset:1024
	ds_read_b128 v[26:29], v30 offset:2048
	ds_read_b128 v[30:33], v30 offset:3072
	s_add_u32 s48, s48, 0x20000
	s_addc_u32 s49, s49, 0
	s_mov_b32 m0, s60
	v_lshl_add_u64 v[226:227], s[48:49], 0, v[168:169]
	ds_read_b128 v[194:197], v192 offset:32768
	ds_read_b128 v[198:201], v192 offset:33792
	ds_read_b128 v[202:205], v192 offset:34816
	ds_read_b128 v[206:209], v192 offset:35840
	ds_read_b128 v[210:213], v192 offset:36864
	ds_read_b128 v[214:217], v192 offset:37888
	ds_read_b128 v[218:221], v192 offset:38912
	ds_read_b128 v[222:225], v192 offset:39936
	global_load_lds_dwordx4 v[226:227], off
	v_lshl_add_u64 v[226:227], s[48:49], 0, v[164:165]
	s_mov_b32 m0, s61
	s_nop 0
	global_load_lds_dwordx4 v[226:227], off
	s_waitcnt vmcnt(8)
	s_waitcnt lgkmcnt(0)
	s_barrier
	s_setprio 1
	s_waitcnt lgkmcnt(0)
	v_mfma_f32_16x16x128_f8f6f4 v[158:161], v[2:9], v[194:201], v[158:161]
	v_mfma_f32_16x16x128_f8f6f4 v[154:157], v[10:17], v[194:201], v[154:157]
	v_mfma_f32_16x16x128_f8f6f4 v[150:153], v[2:9], v[202:209], v[150:153]
	v_mfma_f32_16x16x128_f8f6f4 v[146:149], v[10:17], v[202:209], v[146:149]
	v_mfma_f32_16x16x128_f8f6f4 v[130:133], v[2:9], v[210:217], v[130:133]
	v_mfma_f32_16x16x128_f8f6f4 v[122:125], v[10:17], v[210:217], v[122:125]
	v_mfma_f32_16x16x128_f8f6f4 v[118:121], v[2:9], v[218:225], v[118:121]
	v_mfma_f32_16x16x128_f8f6f4 v[114:117], v[10:17], v[218:225], v[114:117]
	s_setprio 0
	s_setprio 1
	v_mfma_f32_16x16x128_f8f6f4 v[142:145], v[18:25], v[194:201], v[142:145]
	v_mfma_f32_16x16x128_f8f6f4 v[138:141], v[26:33], v[194:201], v[138:141]
	v_mfma_f32_16x16x128_f8f6f4 v[134:137], v[18:25], v[202:209], v[134:137]
	v_mfma_f32_16x16x128_f8f6f4 v[126:129], v[26:33], v[202:209], v[126:129]
	v_mfma_f32_16x16x128_f8f6f4 v[110:113], v[18:25], v[210:217], v[110:113]
	v_mfma_f32_16x16x128_f8f6f4 v[106:109], v[26:33], v[210:217], v[106:109]
	v_mfma_f32_16x16x128_f8f6f4 v[102:105], v[18:25], v[218:225], v[102:105]
	v_mfma_f32_16x16x128_f8f6f4 v[98:101], v[26:33], v[218:225], v[98:101]
	s_setprio 0
	s_barrier
	s_add_i32 s48, s82, s56
	v_lshl_add_u64 v[182:183], v[182:183], 0, s[14:15]
	s_mov_b32 m0, s48
	ds_read_b128 v[194:197], v192 offset:49152
	ds_read_b128 v[198:201], v192 offset:50176
	ds_read_b128 v[202:205], v192 offset:51200
	ds_read_b128 v[206:209], v192 offset:52224
	ds_read_b128 v[210:213], v192 offset:53248
	ds_read_b128 v[214:217], v192 offset:54272
	ds_read_b128 v[218:221], v192 offset:55296
	ds_read_b128 v[222:225], v192 offset:56320
	global_load_lds_dwordx4 v[182:183], off
	s_add_i32 m0, s48, 0x2000
	s_add_u32 s46, s46, 0x20080
	v_lshl_add_u64 v[182:183], v[184:185], 0, s[14:15]
	s_addc_u32 s47, s47, 0
	s_add_i32 s48, s83, s56
	global_load_lds_dwordx4 v[182:183], off
	v_lshl_add_u64 v[182:183], s[46:47], 0, v[166:167]
	s_mov_b32 m0, s48
	s_nop 0
	global_load_lds_dwordx4 v[182:183], off
	v_lshl_add_u64 v[182:183], s[46:47], 0, v[162:163]
	s_add_i32 m0, s48, 0x2000
	s_nop 0
	global_load_lds_dwordx4 v[182:183], off
	v_lshl_add_u64 v[182:183], v[186:187], 0, s[14:15]
	s_mov_b32 m0, s67
	s_nop 0
	global_load_lds_dwordx4 v[182:183], off
	v_lshl_add_u64 v[182:183], v[188:189], 0, s[14:15]
	s_mov_b32 m0, s68
	s_nop 0
	global_load_lds_dwordx4 v[182:183], off
	s_waitcnt vmcnt(8)
	s_waitcnt lgkmcnt(0)
	s_barrier
	s_setprio 1
	s_waitcnt lgkmcnt(0)
	v_mfma_f32_16x16x128_f8f6f4 v[94:97], v[2:9], v[194:201], v[94:97]
	v_mfma_f32_16x16x128_f8f6f4 v[90:93], v[10:17], v[194:201], v[90:93]
	v_mfma_f32_16x16x128_f8f6f4 v[86:89], v[2:9], v[202:209], v[86:89]
	v_mfma_f32_16x16x128_f8f6f4 v[82:85], v[10:17], v[202:209], v[82:85]
	v_mfma_f32_16x16x128_f8f6f4 v[66:69], v[2:9], v[210:217], v[66:69]
	v_mfma_f32_16x16x128_f8f6f4 v[58:61], v[10:17], v[210:217], v[58:61]
	v_mfma_f32_16x16x128_f8f6f4 v[54:57], v[2:9], v[218:225], v[54:57]
	v_mfma_f32_16x16x128_f8f6f4 v[50:53], v[10:17], v[218:225], v[50:53]
	s_setprio 0
	s_setprio 1
	v_mfma_f32_16x16x128_f8f6f4 v[78:81], v[18:25], v[194:201], v[78:81]
	v_mfma_f32_16x16x128_f8f6f4 v[74:77], v[26:33], v[194:201], v[74:77]
	v_mfma_f32_16x16x128_f8f6f4 v[70:73], v[18:25], v[202:209], v[70:73]
	v_mfma_f32_16x16x128_f8f6f4 v[62:65], v[26:33], v[202:209], v[62:65]
	v_mfma_f32_16x16x128_f8f6f4 v[46:49], v[18:25], v[210:217], v[46:49]
	v_mfma_f32_16x16x128_f8f6f4 v[42:45], v[26:33], v[210:217], v[42:45]
	v_mfma_f32_16x16x128_f8f6f4 v[38:41], v[18:25], v[218:225], v[38:41]
	v_mfma_f32_16x16x128_f8f6f4 v[34:37], v[26:33], v[218:225], v[34:37]
	s_setprio 0
	s_add_i32 s81, s81, 2
	s_add_u32 s44, s44, 0x100
	s_addc_u32 s45, s45, 0
	s_add_u32 s35, s35, 0x100
	s_addc_u32 s80, s80, 0
	s_cmp_gt_u32 s81, 5
	s_cbranch_scc1 .Lrot1856_exit
	s_cmp_eq_u32 s81, 4
	s_cselect_b64 s[46:47], -1, 0
	s_cmp_lg_u32 s81, 4
	s_cbranch_scc1 .Lrot1856_head
	s_barrier
	s_branch .LBB0_1857

; #define PG8_STAGE(bufoff, gbase, voff) do { _Pragma("unroll") for (int _i = 0; _i < 2; ++_i) \
;         __builtin_amdgcn_global_load_lds((const unsigned*)((const char*)(gbase) + (voff)[_i]), (PG8_LAS unsigned*)(lds + (bufoff) + ldsw + _i * 8192), 16, 0, 0); } while (0)
; #define PG8_STAGE_A(bufoff, kbase, h, gv) do { if constexpr (GATHER) { PG8_STAGE(bufoff, kbase, (gv)[h]); } else { PG8_STAGE(bufoff, (kbase) + (h) * hstep, voffA); } } while (0)
; #define PG8_WAIT_V(n) asm volatile("s_waitcnt vmcnt(" #n ")" ::: "memory")
; #define PG8_WAIT_L(n) asm volatile("s_waitcnt lgkmcnt(" #n ")" ::: "memory")
; #define PG8_BAR __builtin_amdgcn_s_barrier()
; #define PG8_SCHED __builtin_amdgcn_sched_barrier(0)
; template <class Epi, class Sched, bool ALIGN_EPI = false, bool SP2 = false, bool FP8 = false, bool GATHER = false>
; __device__ __forceinline__ void gemm_phase(PG8_LAS unsigned char* lds, const Gemm g, const Sched& S, const Epi& E) {
;     ...
;             PG8_LDB(B0, 0, 0); PG8_LDB(B1, 0, 1); PG8_SCHED; PG8_LDA(At, 0, 0); PG8_STAGE_A(PG8_SA(1, 1), a1, 1, gcur);
;             PG8_WAIT_V(8); PG8_WAIT_L(0); PG8_BAR; PG8_MMA(0, 0, At, B0); PG8_MMA(0, 1, At, B1); PG8_BAR; PG8_SCHED;
;             PG8_LDA(At, 0, 1); PG8_STAGE(PG8_SB(0, 0), b2, voffB); PG8_STAGE(PG8_SB(0, 1), b2 + hstep, voffB); PG8_STAGE_A(PG8_SA(0, 0), a2, 0, gsel);
;             PG8_WAIT_V(8); PG8_WAIT_L(0); PG8_BAR; PG8_MMA(1, 0, At, B0); PG8_MMA(1, 1, At, B1); PG8_BAR; PG8_SCHED;
.LBB0_1856:
	v_add_u32_e32 v2, s74, v191
	v_add_u32_e32 v14, s75, v191
	ds_read_b128 v[18:21], v2
	ds_read_b128 v[22:25], v2 offset:1024
	ds_read_b128 v[26:29], v2 offset:2048
	ds_read_b128 v[30:33], v2 offset:3072
	ds_read_b128 v[2:5], v14
	ds_read_b128 v[6:9], v14 offset:1024
	ds_read_b128 v[10:13], v14 offset:2048
	ds_read_b128 v[14:17], v14 offset:3072
	s_add_u32 s48, s44, 0xfffe0080
	s_addc_u32 s49, s45, -1
	s_and_b64 s[46:47], s[46:47], exec
	s_cselect_b32 s49, s78, s49
	s_cselect_b32 s48, s79, s48
	s_cselect_b32 s47, s25, s80
	s_cselect_b32 s46, s24, s35
	v_lshl_add_u64 v[218:219], s[44:45], 0, v[172:173]
	s_add_i32 m0, s58, 0xc000
	ds_read_b128 v[182:185], v192
	ds_read_b128 v[186:189], v192 offset:1024
	ds_read_b128 v[194:197], v192 offset:2048
	ds_read_b128 v[198:201], v192 offset:3072
	ds_read_b128 v[202:205], v192 offset:4096
	ds_read_b128 v[206:209], v192 offset:5120
	ds_read_b128 v[210:213], v192 offset:6144
	ds_read_b128 v[214:217], v192 offset:7168
	global_load_lds_dwordx4 v[218:219], off
	v_lshl_add_u64 v[218:219], s[44:45], 0, v[174:175]
	s_add_i32 m0, s58, 0xe000
	s_nop 0
	global_load_lds_dwordx4 v[218:219], off
	s_waitcnt vmcnt(8)
	s_waitcnt lgkmcnt(0)
	s_barrier
	s_setprio 1
	s_waitcnt lgkmcnt(0)
	v_mfma_f32_16x16x128_f8f6f4 v[158:161], v[18:25], v[182:189], v[158:161]
	v_mfma_f32_16x16x128_f8f6f4 v[154:157], v[26:33], v[182:189], v[154:157]
	v_mfma_f32_16x16x128_f8f6f4 v[150:153], v[18:25], v[194:201], v[150:153]
	v_mfma_f32_16x16x128_f8f6f4 v[146:149], v[26:33], v[194:201], v[146:149]
	v_mfma_f32_16x16x128_f8f6f4 v[130:133], v[18:25], v[202:209], v[130:133]
	v_mfma_f32_16x16x128_f8f6f4 v[122:125], v[26:33], v[202:209], v[122:125]
	v_mfma_f32_16x16x128_f8f6f4 v[118:121], v[18:25], v[210:217], v[118:121]
	v_mfma_f32_16x16x128_f8f6f4 v[114:117], v[26:33], v[210:217], v[114:117]
	s_setprio 0
	s_setprio 1
	v_mfma_f32_16x16x128_f8f6f4 v[142:145], v[2:9], v[182:189], v[142:145]
	v_mfma_f32_16x16x128_f8f6f4 v[138:141], v[10:17], v[182:189], v[138:141]
	v_mfma_f32_16x16x128_f8f6f4 v[134:137], v[2:9], v[194:201], v[134:137]
	v_mfma_f32_16x16x128_f8f6f4 v[126:129], v[10:17], v[194:201], v[126:129]
	v_mfma_f32_16x16x128_f8f6f4 v[110:113], v[2:9], v[202:209], v[110:113]
	v_mfma_f32_16x16x128_f8f6f4 v[106:109], v[10:17], v[202:209], v[106:109]
	v_mfma_f32_16x16x128_f8f6f4 v[102:105], v[2:9], v[210:217], v[102:105]
	v_mfma_f32_16x16x128_f8f6f4 v[98:101], v[10:17], v[210:217], v[98:101]
	s_setprio 0
	s_barrier
	s_add_i32 s82, s74, s56
	v_lshl_add_u64 v[182:183], s[46:47], 0, v[166:167]
	s_mov_b32 m0, s82
	ds_read_b128 v[194:197], v192 offset:16384
	ds_read_b128 v[198:201], v192 offset:17408
	ds_read_b128 v[202:205], v192 offset:18432
	ds_read_b128 v[206:209], v192 offset:19456
	ds_read_b128 v[210:213], v192 offset:20480
	ds_read_b128 v[214:217], v192 offset:21504
	ds_read_b128 v[218:221], v192 offset:22528
	ds_read_b128 v[222:225], v192 offset:23552
	global_load_lds_dwordx4 v[182:183], off
	s_add_i32 m0, s82, 0x2000
	s_add_u32 s82, s46, 0x20000
	v_lshl_add_u64 v[184:185], s[46:47], 0, v[162:163]
	s_addc_u32 s83, s47, 0
	s_add_i32 s84, s75, s56
	global_load_lds_dwordx4 v[184:185], off
	v_lshl_add_u64 v[186:187], s[82:83], 0, v[166:167]
	s_mov_b32 m0, s84
	v_lshl_add_u64 v[188:189], s[48:49], 0, v[164:165]
	global_load_lds_dwordx4 v[186:187], off
	v_lshl_add_u64 v[186:187], s[82:83], 0, v[162:163]
	s_add_i32 m0, s84, 0x2000
	s_nop 0
	global_load_lds_dwordx4 v[186:187], off
	v_lshl_add_u64 v[186:187], s[48:49], 0, v[168:169]
	s_mov_b32 m0, s58
	s_nop 0
	global_load_lds_dwordx4 v[186:187], off
	s_mov_b32 m0, s59
	s_nop 0
	global_load_lds_dwordx4 v[188:189], off
	s_waitcnt vmcnt(8)
	s_waitcnt lgkmcnt(0)
	s_barrier
	s_setprio 1
	s_waitcnt lgkmcnt(0)
	v_mfma_f32_16x16x128_f8f6f4 v[94:97], v[18:25], v[194:201], v[94:97]
	v_mfma_f32_16x16x128_f8f6f4 v[90:93], v[26:33], v[194:201], v[90:93]
	v_mfma_f32_16x16x128_f8f6f4 v[86:89], v[18:25], v[202:209], v[86:89]
	v_mfma_f32_16x16x128_f8f6f4 v[82:85], v[26:33], v[202:209], v[82:85]
	v_mfma_f32_16x16x128_f8f6f4 v[66:69], v[18:25], v[210:217], v[66:69]
	v_mfma_f32_16x16x128_f8f6f4 v[58:61], v[26:33], v[210:217], v[58:61]
	v_mfma_f32_16x16x128_f8f6f4 v[54:57], v[18:25], v[218:225], v[54:57]
	v_mfma_f32_16x16x128_f8f6f4 v[50:53], v[26:33], v[218:225], v[50:53]
	s_setprio 0
	s_setprio 1
	v_mfma_f32_16x16x128_f8f6f4 v[78:81], v[2:9], v[194:201], v[78:81]
	v_mfma_f32_16x16x128_f8f6f4 v[74:77], v[10:17], v[194:201], v[74:77]
	v_mfma_f32_16x16x128_f8f6f4 v[70:73], v[2:9], v[202:209], v[70:73]
	v_mfma_f32_16x16x128_f8f6f4 v[62:65], v[10:17], v[202:209], v[62:65]
	v_mfma_f32_16x16x128_f8f6f4 v[46:49], v[2:9], v[210:217], v[46:49]
	v_mfma_f32_16x16x128_f8f6f4 v[42:45], v[10:17], v[210:217], v[42:45]
	v_mfma_f32_16x16x128_f8f6f4 v[38:41], v[2:9], v[218:225], v[38:41]
	v_mfma_f32_16x16x128_f8f6f4 v[34:37], v[10:17], v[218:225], v[34:37]
	s_setprio 0
	s_barrier
; #define PG8_STAGE(bufoff, gbase, voff) do { _Pragma("unroll") for (int _i = 0; _i < 2; ++_i) \
;         __builtin_amdgcn_global_load_lds((const unsigned*)((const char*)(gbase) + (voff)[_i]), (PG8_LAS unsigned*)(lds + (bufoff) + ldsw + _i * 8192), 16, 0, 0); } while (0)
; #define PG8_STAGE_A(bufoff, kbase, h, gv) do { if constexpr (GATHER) { PG8_STAGE(bufoff, kbase, (gv)[h]); } else { PG8_STAGE(bufoff, (kbase) + (h) * hstep, voffA); } } while (0)
; #define PG8_WAIT_V(n) asm volatile("s_waitcnt vmcnt(" #n ")" ::: "memory")
; #define PG8_WAIT_L(n) asm volatile("s_waitcnt lgkmcnt(" #n ")" ::: "memory")
; #define PG8_BAR __builtin_amdgcn_s_barrier()
; #define PG8_SCHED __builtin_amdgcn_sched_barrier(0)
; template <class Epi, class Sched, bool ALIGN_EPI = false, bool SP2 = false, bool FP8 = false, bool GATHER = false>
; __device__ __forceinline__ void gemm_phase(PG8_LAS unsigned char* lds, const Gemm g, const Sched& S, const Epi& E) {
;     ...
;         for (int t = 0; t < nt; t += 2) {
;             const bool last = (t == nt - 2);
;             const char* a1 = cA + (size_t)(t + 1) * kstep;
;             const char* a2 = last ? nA : cA + (size_t)(t + 2) * kstep; const char* b2 = last ? nB : cB + (size_t)(t + 2) * kstep;
;             const char* a3 = a2 + kstep; const char* b3 = b2 + kstep;
;             if (last && has_next) S.a_ready(nxt);
;     ...
;             PG8_LDB(B0, 1, 0); PG8_LDB(B1, 1, 1); PG8_SCHED; PG8_LDA(At, 1, 0); PG8_STAGE_A(PG8_SA(0, 1), a2, 1, gsel);
;             PG8_WAIT_V(8); PG8_WAIT_L(0); PG8_BAR; PG8_MMA(0, 0, At, B0); PG8_MMA(0, 1, At, B1); PG8_BAR; PG8_SCHED;
;             PG8_LDA(At, 1, 1); PG8_STAGE(PG8_SB(1, 0), b3, voffB); PG8_STAGE(PG8_SB(1, 1), b3 + hstep, voffB); PG8_STAGE_A(PG8_SA(1, 0), a3, 0, gsel);
;             PG8_WAIT_V(8); PG8_WAIT_L(0); PG8_BAR; PG8_MMA(1, 0, At, B0); PG8_MMA(1, 1, At, B1); PG8_BAR; PG8_SCHED;
	s_add_i32 s82, 0, 0x18000
	s_add_i32 s83, 0, 0x1c000
	v_add_u32_e32 v14, s82, v191
	v_add_u32_e32 v30, s83, v191
	ds_read_b128 v[2:5], v14
	ds_read_b128 v[6:9], v14 offset:1024
	ds_read_b128 v[10:13], v14 offset:2048
	ds_read_b128 v[14:17], v14 offset:3072
	ds_read_b128 v[18:21], v30
	ds_read_b128 v[22:25], v30 offset:1024
	ds_read_b128 v[26:29], v30 offset:2048
	ds_read_b128 v[30:33], v30 offset:3072
	s_add_u32 s48, s48, 0x20000
	s_addc_u32 s49, s49, 0
	s_mov_b32 m0, s60
	v_lshl_add_u64 v[226:227], s[48:49], 0, v[168:169]
	ds_read_b128 v[194:197], v192 offset:32768
	ds_read_b128 v[198:201], v192 offset:33792
	ds_read_b128 v[202:205], v192 offset:34816
	ds_read_b128 v[206:209], v192 offset:35840
	ds_read_b128 v[210:213], v192 offset:36864
	ds_read_b128 v[214:217], v192 offset:37888
	ds_read_b128 v[218:221], v192 offset:38912
	ds_read_b128 v[222:225], v192 offset:39936
	global_load_lds_dwordx4 v[226:227], off
	v_lshl_add_u64 v[226:227], s[48:49], 0, v[164:165]
	s_mov_b32 m0, s61
	s_nop 0
	global_load_lds_dwordx4 v[226:227], off
	s_waitcnt vmcnt(8)
	s_waitcnt lgkmcnt(0)
	s_barrier
	s_setprio 1
	s_waitcnt lgkmcnt(0)
	v_mfma_f32_16x16x128_f8f6f4 v[158:161], v[2:9], v[194:201], v[158:161]
	v_mfma_f32_16x16x128_f8f6f4 v[154:157], v[10:17], v[194:201], v[154:157]
	v_mfma_f32_16x16x128_f8f6f4 v[150:153], v[2:9], v[202:209], v[150:153]
	v_mfma_f32_16x16x128_f8f6f4 v[146:149], v[10:17], v[202:209], v[146:149]
	v_mfma_f32_16x16x128_f8f6f4 v[130:133], v[2:9], v[210:217], v[130:133]
	v_mfma_f32_16x16x128_f8f6f4 v[122:125], v[10:17], v[210:217], v[122:125]
	v_mfma_f32_16x16x128_f8f6f4 v[118:121], v[2:9], v[218:225], v[118:121]
	v_mfma_f32_16x16x128_f8f6f4 v[114:117], v[10:17], v[218:225], v[114:117]
	s_setprio 0
	s_setprio 1
	v_mfma_f32_16x16x128_f8f6f4 v[142:145], v[18:25], v[194:201], v[142:145]
	v_mfma_f32_16x16x128_f8f6f4 v[138:141], v[26:33], v[194:201], v[138:141]
	v_mfma_f32_16x16x128_f8f6f4 v[134:137], v[18:25], v[202:209], v[134:137]
	v_mfma_f32_16x16x128_f8f6f4 v[126:129], v[26:33], v[202:209], v[126:129]
	v_mfma_f32_16x16x128_f8f6f4 v[110:113], v[18:25], v[210:217], v[110:113]
	v_mfma_f32_16x16x128_f8f6f4 v[106:109], v[26:33], v[210:217], v[106:109]
	v_mfma_f32_16x16x128_f8f6f4 v[102:105], v[18:25], v[218:225], v[102:105]
	v_mfma_f32_16x16x128_f8f6f4 v[98:101], v[26:33], v[218:225], v[98:101]
	s_setprio 0
	s_barrier
	s_add_i32 s48, s82, s56
	v_lshl_add_u64 v[182:183], v[182:183], 0, s[14:15]
	s_mov_b32 m0, s48
	ds_read_b128 v[194:197], v192 offset:49152
	ds_read_b128 v[198:201], v192 offset:50176
	ds_read_b128 v[202:205], v192 offset:51200
	ds_read_b128 v[206:209], v192 offset:52224
	ds_read_b128 v[210:213], v192 offset:53248
	ds_read_b128 v[214:217], v192 offset:54272
	ds_read_b128 v[218:221], v192 offset:55296
	ds_read_b128 v[222:225], v192 offset:56320
	global_load_lds_dwordx4 v[182:183], off
	s_add_i32 m0, s48, 0x2000
	s_add_u32 s46, s46, 0x20080
	v_lshl_add_u64 v[182:183], v[184:185], 0, s[14:15]
	s_addc_u32 s47, s47, 0
	s_add_i32 s48, s83, s56
	global_load_lds_dwordx4 v[182:183], off
	v_lshl_add_u64 v[182:183], s[46:47], 0, v[166:167]
	s_mov_b32 m0, s48
	s_nop 0
	global_load_lds_dwordx4 v[182:183], off
	v_lshl_add_u64 v[182:183], s[46:47], 0, v[162:163]
	s_add_i32 m0, s48, 0x2000
	s_nop 0
	global_load_lds_dwordx4 v[182:183], off
	v_lshl_add_u64 v[182:183], v[186:187], 0, s[14:15]
	s_mov_b32 m0, s67
	s_nop 0
	global_load_lds_dwordx4 v[182:183], off
	v_lshl_add_u64 v[182:183], v[188:189], 0, s[14:15]
	s_mov_b32 m0, s68
	s_nop 0
	global_load_lds_dwordx4 v[182:183], off
	s_waitcnt vmcnt(8)
	s_waitcnt lgkmcnt(0)
	s_barrier
	s_setprio 1
	s_waitcnt lgkmcnt(0)
	v_mfma_f32_16x16x128_f8f6f4 v[94:97], v[2:9], v[194:201], v[94:97]
	v_mfma_f32_16x16x128_f8f6f4 v[90:93], v[10:17], v[194:201], v[90:93]
	v_mfma_f32_16x16x128_f8f6f4 v[86:89], v[2:9], v[202:209], v[86:89]
	v_mfma_f32_16x16x128_f8f6f4 v[82:85], v[10:17], v[202:209], v[82:85]
	v_mfma_f32_16x16x128_f8f6f4 v[66:69], v[2:9], v[210:217], v[66:69]
	v_mfma_f32_16x16x128_f8f6f4 v[58:61], v[10:17], v[210:217], v[58:61]
	v_mfma_f32_16x16x128_f8f6f4 v[54:57], v[2:9], v[218:225], v[54:57]
	v_mfma_f32_16x16x128_f8f6f4 v[50:53], v[10:17], v[218:225], v[50:53]
	s_setprio 0
	s_setprio 1
	v_mfma_f32_16x16x128_f8f6f4 v[78:81], v[18:25], v[194:201], v[78:81]
	v_mfma_f32_16x16x128_f8f6f4 v[74:77], v[26:33], v[194:201], v[74:77]
	v_mfma_f32_16x16x128_f8f6f4 v[70:73], v[18:25], v[202:209], v[70:73]
	v_mfma_f32_16x16x128_f8f6f4 v[62:65], v[26:33], v[202:209], v[62:65]
	v_mfma_f32_16x16x128_f8f6f4 v[46:49], v[18:25], v[210:217], v[46:49]
	v_mfma_f32_16x16x128_f8f6f4 v[42:45], v[26:33], v[210:217], v[42:45]
	v_mfma_f32_16x16x128_f8f6f4 v[38:41], v[18:25], v[218:225], v[38:41]
	v_mfma_f32_16x16x128_f8f6f4 v[34:37], v[26:33], v[218:225], v[34:37]
	s_setprio 0
	s_add_i32 s81, s81, 2
	s_add_u32 s44, s44, 0x100
	s_addc_u32 s45, s45, 0
	s_add_u32 s35, s35, 0x100
	s_addc_u32 s80, s80, 0
	s_cmp_gt_u32 s81, 5
	s_cbranch_scc1 .Lrot1856_exit
	s_cmp_eq_u32 s81, 4
	s_cselect_b64 s[46:47], -1, 0
	s_cmp_lg_u32 s81, 4
	s_cbranch_scc1 .Lrot1856_head
	s_barrier
